# baseline (speedup 1.0000x reference)
_Z8k_stageAPKfS0_S0_S0_PDF16_PKDF16_S0_S1_ii:
	s_load_dwordx2 s[64:65], s[0:1], 0x40
	v_readfirstlane_b32 s94, v0
	s_nop 0
	s_lshr_b32 s94, s94, 6
	s_load_dwordx8 s[4:11], s[0:1], 0x0
	v_readfirstlane_b32 s14, v0
	s_lshr_b32 s15, s2, 5
	s_lshl_b32 s2, s2, 7
	s_lshr_b32 s20, s14, 6
	s_and_b32 s12, s2, 0xf80
	s_lshl_b32 s13, s15, 12
	s_mov_b32 s18, s3
	s_cmpk_lt_u32 s14, 0x100
	s_waitcnt lgkmcnt(0)
	s_cselect_b32 s2, s4, s6
	s_cselect_b32 s3, s5, s7
	s_cselect_b32 s4, s8, s10
	s_cselect_b32 s5, s9, s11
	s_cmp_eq_u32 s18, 0
	s_cselect_b32 s3, s3, s5
	s_cselect_b32 s2, s2, s4
	s_lshr_b32 s5, s14, 1
	s_lshl_b32 s4, s15, 7
	s_and_b32 s5, s5, 0x60
	v_bfe_u32 v1, v0, 5, 1
	s_or_b32 s4, s5, s4
	v_lshl_or_b32 v82, v1, 3, s4
	v_mov_b32_e32 v83, 0
	v_lshlrev_b64 v[2:3], 14, v[82:83]
	v_lshlrev_b32_e32 v78, 2, v0
	s_mov_b32 s17, 0
	v_lshl_add_u64 v[2:3], s[2:3], 0, v[2:3]
	s_lshl_b32 s16, s12, 2
	v_and_b32_e32 v79, 0x7c, v78
	v_lshl_add_u64 v[2:3], v[2:3], 0, s[16:17]
	v_lshlrev_b32_e32 v82, 2, v79
	v_lshl_add_u64 v[42:43], v[2:3], 0, v[82:83]
	s_movk_i32 s21, 0x4000
	v_add_co_u32_e32 v10, vcc, s21, v42
	s_mov_b32 s2, 0x8000
	s_nop 0
	v_addc_co_u32_e32 v11, vcc, 0, v43, vcc
	v_add_co_u32_e32 v18, vcc, s2, v42
	s_mov_b32 s2, 0xc000
	s_nop 0
	v_addc_co_u32_e32 v19, vcc, 0, v43, vcc
	v_add_co_u32_e32 v20, vcc, s2, v42
	s_mov_b32 s14, 0x10000
	s_nop 0
	v_addc_co_u32_e32 v21, vcc, 0, v43, vcc
	v_add_co_u32_e32 v26, vcc, s14, v42
	s_mov_b32 s2, 0x14000
	s_nop 0
	v_addc_co_u32_e32 v27, vcc, 0, v43, vcc
	v_add_co_u32_e32 v28, vcc, s2, v42
	s_mov_b32 s2, 0x18000
	s_nop 0
	v_addc_co_u32_e32 v29, vcc, 0, v43, vcc
	v_add_co_u32_e32 v34, vcc, s2, v42
	s_mov_b32 s2, 0x1c000
	s_nop 0
	v_addc_co_u32_e32 v35, vcc, 0, v43, vcc
	v_add_co_u32_e32 v36, vcc, s2, v42
	s_mov_b32 s2, 0x40000
	s_nop 0
	v_addc_co_u32_e32 v37, vcc, 0, v43, vcc
	v_add_co_u32_e32 v66, vcc, s2, v42
	s_mov_b32 s2, 0x44000
	s_nop 0
	v_addc_co_u32_e32 v67, vcc, 0, v43, vcc
	v_add_co_u32_e32 v68, vcc, s2, v42
	s_mov_b32 s2, 0x48000
	s_nop 0
	v_addc_co_u32_e32 v69, vcc, 0, v43, vcc
	global_load_dwordx4 v[2:5], v[42:43], off nt
	global_load_dwordx4 v[6:9], v[10:11], off nt
	v_add_co_u32_e32 v44, vcc, s2, v42
	global_load_dwordx4 v[10:13], v[18:19], off nt
	global_load_dwordx4 v[14:17], v[20:21], off nt
	s_nop 0
	global_load_dwordx4 v[18:21], v[26:27], off nt
	global_load_dwordx4 v[22:25], v[28:29], off nt
	s_nop 0
	global_load_dwordx4 v[26:29], v[34:35], off nt
	global_load_dwordx4 v[30:33], v[36:37], off nt
	v_addc_co_u32_e32 v45, vcc, 0, v43, vcc
	s_mov_b32 s2, 0x4c000
	v_add_co_u32_e32 v46, vcc, s2, v42
	s_mov_b32 s2, 0x50000
	s_nop 0
	v_addc_co_u32_e32 v47, vcc, 0, v43, vcc
	v_add_co_u32_e32 v70, vcc, s2, v42
	s_mov_b32 s2, 0x54000
	s_nop 0
	v_addc_co_u32_e32 v71, vcc, 0, v43, vcc
	v_add_co_u32_e32 v72, vcc, s2, v42
	s_mov_b32 s2, 0x58000
	s_nop 0
	v_addc_co_u32_e32 v73, vcc, 0, v43, vcc
	v_add_co_u32_e32 v74, vcc, s2, v42
	s_mov_b32 s2, 0x5c000
	s_nop 0
	v_addc_co_u32_e32 v75, vcc, 0, v43, vcc
	v_add_co_u32_e32 v76, vcc, s2, v42
	global_load_dwordx4 v[34:37], v[44:45], off nt
	global_load_dwordx4 v[38:41], v[46:47], off nt
	v_addc_co_u32_e32 v77, vcc, 0, v43, vcc
	global_load_dwordx4 v[42:45], v[74:75], off nt
	global_load_dwordx4 v[46:49], v[76:77], off nt
	global_load_dwordx4 v[50:53], v[70:71], off nt
	global_load_dwordx4 v[54:57], v[72:73], off nt
	global_load_dwordx4 v[58:61], v[66:67], off nt
	global_load_dwordx4 v[62:65], v[68:69], off nt
	v_lshl_or_b32 v1, s20, 2, v1
	v_lshrrev_b32_e32 v70, 5, v0
	v_or_b32_e32 v141, 0x200, v0
	v_or_b32_e32 v142, 0x600, v0
	s_or_b32 s16, s13, s12
	s_ashr_i32 s19, s18, 31
	s_lshl_b64 s[12:13], s[16:17], 9
	s_mov_b32 s15, 0x20000
	v_or_b32_e32 v144, 0xa00, v0
	v_bfe_u32 v140, v0, 4, 2
	v_and_b32_e32 v145, 15, v0
	v_lshlrev_b32_e32 v220, 9, v145
	s_waitcnt vmcnt(14)
	v_cvt_pk_f16_f32 v66, v2, v6
	v_lshlrev_b32_e32 v6, 9, v79
	v_bitop3_b32 v2, v78, v1, 12 bitop3:0x6c
	s_waitcnt vmcnt(12)
	v_cvt_pk_f16_f32 v67, v10, v14
	s_waitcnt vmcnt(10)
	v_cvt_pk_f16_f32 v68, v18, v22
	s_waitcnt vmcnt(8)
	v_cvt_pk_f16_f32 v69, v26, v30
	v_lshl_add_u32 v2, v2, 4, v6
	ds_write_b128 v2, v[66:69]
	v_cvt_pk_f16_f32 v66, v3, v7
	v_or_b32_e32 v7, 1, v79
	v_lshlrev_b32_e32 v10, 9, v7
	v_bitop3_b32 v2, v7, v1, 13 bitop3:0x6c
	v_cvt_pk_f16_f32 v69, v27, v31
	v_cvt_pk_f16_f32 v68, v19, v23
	v_cvt_pk_f16_f32 v67, v11, v15
	v_lshl_add_u32 v2, v2, 4, v10
	ds_write_b128 v2, v[66:69]
	v_cvt_pk_f16_f32 v66, v4, v8
	v_or_b32_e32 v8, 2, v79
	v_lshlrev_b32_e32 v11, 9, v8
	v_bitop3_b32 v2, v8, v1, 14 bitop3:0x6c
	v_cvt_pk_f16_f32 v69, v28, v32
	v_cvt_pk_f16_f32 v68, v20, v24
	v_cvt_pk_f16_f32 v67, v12, v16
	v_lshl_add_u32 v2, v2, 4, v11
	v_cvt_pk_f16_f32 v12, v5, v9
	v_or_b32_e32 v9, 3, v79
	ds_write_b128 v2, v[66:69]
	v_lshlrev_b32_e32 v16, 9, v9
	v_bitop3_b32 v2, v9, v1, 15 bitop3:0x6c
	v_cvt_pk_f16_f32 v15, v29, v33
	v_cvt_pk_f16_f32 v14, v21, v25
	v_cvt_pk_f16_f32 v13, v13, v17
	v_lshl_add_u32 v2, v2, 4, v16
	v_or_b32_e32 v1, 2, v1
	ds_write_b128 v2, v[12:15]
	v_bitop3_b32 v12, v78, v1, 12 bitop3:0x6c
	s_waitcnt vmcnt(4)
	v_cvt_pk_f16_f32 v5, v42, v46
	s_waitcnt vmcnt(2)
	v_cvt_pk_f16_f32 v4, v50, v54
	v_cvt_pk_f16_f32 v3, v34, v38
	s_waitcnt vmcnt(0)
	v_cvt_pk_f16_f32 v2, v58, v62
	v_lshl_add_u32 v6, v12, 4, v6
	ds_write_b128 v6, v[2:5]
	v_bitop3_b32 v6, v7, v1, 13 bitop3:0x6c
	v_cvt_pk_f16_f32 v5, v43, v47
	v_cvt_pk_f16_f32 v4, v51, v55
	v_cvt_pk_f16_f32 v3, v35, v39
	v_cvt_pk_f16_f32 v2, v59, v63
	v_lshl_add_u32 v6, v6, 4, v10
	ds_write_b128 v6, v[2:5]
	v_bitop3_b32 v6, v8, v1, 14 bitop3:0x6c
	v_cvt_pk_f16_f32 v5, v44, v48
	v_cvt_pk_f16_f32 v4, v52, v56
	v_cvt_pk_f16_f32 v3, v36, v40
	v_cvt_pk_f16_f32 v2, v60, v64
	v_lshl_add_u32 v6, v6, 4, v11
	v_bitop3_b32 v1, v9, v1, 15 bitop3:0x6c
	ds_write_b128 v6, v[2:5]
	v_cvt_pk_f16_f32 v5, v45, v49
	v_cvt_pk_f16_f32 v4, v53, v57
	v_cvt_pk_f16_f32 v3, v37, v41
	v_cvt_pk_f16_f32 v2, v61, v65
	v_lshl_add_u32 v1, v1, 4, v16
	ds_write_b128 v1, v[2:5]
	v_bitop3_b32 v2, v70, v0, 31 bitop3:0x78
	v_lshlrev_b32_e32 v1, 9, v70
	v_lshlrev_b32_e32 v22, 4, v2
	v_or_b32_e32 v10, v22, v1
	s_waitcnt lgkmcnt(0)
	s_barrier
	ds_read_b128 v[2:5], v10
	s_load_dwordx8 s[4:11], s[0:1], 0x20
	s_load_dwordx2 s[2:3], s[0:1], 0x40
	v_lshlrev_b32_e32 v24, 4, v0
	v_and_b32_e32 v25, 0x1e00, v24
	v_or_b32_e32 v26, v22, v25
	s_waitcnt lgkmcnt(0)
	v_pk_max_f16 v6, v5, v5
	v_and_b32_e32 v18, 31, v0
	v_pk_max_f16 v9, v6, 0
	v_pk_max_f16 v6, v4, v4
	v_lshlrev_b32_e32 v29, 4, v18
	v_pk_max_f16 v8, v6, 0
	v_pk_max_f16 v6, v3, v3
	s_lshl_b64 s[0:1], s[18:19], 23
	v_pk_max_f16 v7, v6, 0
	v_pk_max_f16 v6, v2, v2
	s_add_u32 s0, s4, s0
	v_pk_max_f16 v6, v6, 0
	ds_write_b128 v10, v[6:9]
	v_lshlrev_b32_e32 v6, 4, v141
	v_and_b32_e32 v23, 0x3e00, v6
	v_or_b32_e32 v14, v22, v23
	ds_read_b128 v[6:9], v14
	s_addc_u32 s1, s5, s1
	s_add_u32 s12, s0, s12
	s_addc_u32 s0, s1, s13
	s_and_b32 s13, s0, 0xffff
	s_waitcnt lgkmcnt(0)
	v_pk_max_f16 v10, v9, v9
	v_or_b32_e32 v1, v1, v29
	v_pk_max_f16 v13, v10, 0
	v_pk_max_f16 v10, v8, v8
	buffer_store_dwordx4 v[2:5], v1, s[12:15], 0 offen sc1
	v_pk_max_f16 v12, v10, 0
	v_pk_max_f16 v10, v7, v7
	v_or_b32_e32 v1, v23, v29
	v_pk_max_f16 v11, v10, 0
	v_pk_max_f16 v10, v6, v6
	buffer_store_dwordx4 v[6:9], v1, s[12:15], 0 offen sc1
	v_pk_max_f16 v10, v10, 0
	ds_write_b128 v14, v[10:13]
	ds_read_b128 v[10:13], v26 offset:16384
	v_or_b32_e32 v25, v25, v29
	v_or_b32_e32 v6, 0x4000, v25
	s_mov_b32 s0, 0xfe00
	s_waitcnt lgkmcnt(0)
	v_pk_max_f16 v14, v13, v13
	s_nop 0
	v_pk_max_f16 v17, v14, 0
	v_pk_max_f16 v14, v12, v12
	buffer_store_dwordx4 v[10:13], v6, s[12:15], 0 offen sc1
	v_pk_max_f16 v16, v14, 0
	v_pk_max_f16 v14, v11, v11
	s_nop 0
	v_pk_max_f16 v15, v14, 0
	v_pk_max_f16 v14, v10, v10
	s_nop 0
	v_pk_max_f16 v14, v14, 0
	ds_write_b128 v26, v[14:17] offset:16384
	v_lshlrev_b32_e32 v14, 4, v142
	v_and_b32_e32 v27, 0x7e00, v14
	v_or_b32_e32 v28, v22, v27
	ds_read_b128 v[14:17], v28
	v_or_b32_e32 v10, v27, v29
	s_waitcnt lgkmcnt(0)
	v_pk_max_f16 v18, v17, v17
	s_nop 0
	v_pk_max_f16 v21, v18, 0
	v_pk_max_f16 v18, v16, v16
	buffer_store_dwordx4 v[14:17], v10, s[12:15], 0 offen sc1
	v_pk_max_f16 v20, v18, 0
	v_pk_max_f16 v18, v15, v15
	v_or_b32_e32 v10, 0x8000, v25
	v_pk_max_f16 v19, v18, 0
	v_pk_max_f16 v18, v14, v14
	s_nop 0
	v_pk_max_f16 v18, v18, 0
	ds_write_b128 v28, v[18:21]
	ds_read_b128 v[18:21], v26 offset:32768
	s_waitcnt lgkmcnt(0)
	v_pk_max_f16 v1, v21, v21
	s_nop 0
	v_pk_max_f16 v5, v1, 0
	v_pk_max_f16 v1, v20, v20
	buffer_store_dwordx4 v[18:21], v10, s[12:15], 0 offen sc1
	v_pk_max_f16 v4, v1, 0
	v_pk_max_f16 v1, v19, v19
	s_nop 0
	v_pk_max_f16 v3, v1, 0
	v_pk_max_f16 v1, v18, v18
	s_nop 0
	v_pk_max_f16 v2, v1, 0
	v_lshlrev_b32_e32 v1, 4, v144
	v_and_b32_e32 v1, 0xbe00, v1
	ds_write_b128 v26, v[2:5] offset:32768
	v_or_b32_e32 v23, v22, v1
	ds_read_b128 v[2:5], v23
	v_or_b32_e32 v1, v1, v29
	s_waitcnt lgkmcnt(0)
	v_pk_max_f16 v6, v5, v5
	s_nop 0
	v_pk_max_f16 v9, v6, 0
	v_pk_max_f16 v6, v4, v4
	buffer_store_dwordx4 v[2:5], v1, s[12:15], 0 offen sc1
	v_pk_max_f16 v8, v6, 0
	v_pk_max_f16 v6, v3, v3
	v_or_b32_e32 v1, 0xc000, v25
	v_pk_max_f16 v7, v6, 0
	v_pk_max_f16 v6, v2, v2
	s_nop 0
	v_pk_max_f16 v6, v6, 0
	ds_write_b128 v23, v[6:9]
	ds_read_b128 v[6:9], v26 offset:49152
	s_waitcnt lgkmcnt(0)
	v_pk_max_f16 v10, v9, v9
	s_nop 0
	v_pk_max_f16 v13, v10, 0
	v_pk_max_f16 v10, v8, v8
	buffer_store_dwordx4 v[6:9], v1, s[12:15], 0 offen sc1
	v_pk_max_f16 v12, v10, 0
	v_pk_max_f16 v10, v7, v7
	s_nop 0
	v_pk_max_f16 v11, v10, 0
	v_pk_max_f16 v10, v6, v6
	s_nop 0
	v_pk_max_f16 v10, v10, 0
	ds_write_b128 v26, v[10:13] offset:49152
	v_mov_b32_e32 v10, 0xe000
	v_bitop3_b32 v14, v24, s0, v10 bitop3:0xc8
	s_mul_i32 s0, s3, s18
	v_or_b32_e32 v15, v22, v14
	s_add_i32 s0, s0, s2
	ds_read_b128 v[10:13], v15
	s_mul_i32 s2, s0, 0x60000
	s_mul_hi_i32 s1, s0, 0x60000
	s_add_u32 s2, s6, s2
	s_mulk_i32 s0, 0x300
	s_addc_u32 s3, s7, s1
	s_ashr_i32 s1, s0, 31
	s_lshl_b64 s[0:1], s[0:1], 2
	v_or_b32_e32 v1, v14, v29
	s_add_u32 s4, s8, s0
	s_waitcnt lgkmcnt(0)
	buffer_store_dwordx4 v[10:13], v1, s[12:15], 0 offen sc1
	v_pk_max_f16 v1, v13, v13
	s_addc_u32 s5, s9, s1
	s_mul_i32 s0, s18, 0x1800000
	v_pk_max_f16 v5, v1, 0
	v_pk_max_f16 v1, v12, v12
	s_mul_hi_i32 s1, s18, 0x1800000
	s_add_u32 s0, s10, s0
	v_pk_max_f16 v4, v1, 0
	v_pk_max_f16 v1, v11, v11
	s_addc_u32 s1, s11, s1
	v_pk_max_f16 v3, v1, 0
	v_pk_max_f16 v1, v10, v10
	s_and_b32 s1, s1, 0xffff
	s_mul_i32 s7, s20, 0x6000
	v_pk_max_f16 v2, v1, 0
	v_and_b32_e32 v1, 63, v0
	s_mul_hi_u32 s6, s20, 0x6000
	s_add_u32 s2, s2, s7
	s_addc_u32 s3, s3, s6
	v_lshlrev_b32_e32 v82, 4, v1
	v_lshl_add_u64 v[118:119], s[2:3], 0, v[82:83]
	s_movk_i32 s6, 0x1000
	v_add_co_u32_e32 v50, vcc, s6, v118
	s_movk_i32 s6, 0x2000
	s_nop 0
	v_addc_co_u32_e32 v51, vcc, 0, v119, vcc
	ds_write_b128 v15, v[2:5]
	v_add_co_u32_e32 v52, vcc, s6, v118
	global_load_dwordx4 v[2:5], v82, s[2:3] offset:1024
	global_load_dwordx4 v[6:9], v82, s[2:3] offset:2048
	v_addc_co_u32_e32 v53, vcc, 0, v119, vcc
	global_load_dwordx4 v[10:13], v82, s[2:3] offset:3072
	global_load_dwordx4 v[14:17], v[52:53], off offset:-4096
	global_load_dwordx4 v[18:21], v[50:51], off offset:1024
	global_load_dwordx4 v[22:25], v[50:51], off offset:2048
	global_load_dwordx4 v[26:29], v82, s[2:3]
	global_load_dwordx4 v[30:33], v[50:51], off offset:3072
	global_load_dwordx4 v[34:37], v[52:53], off
	global_load_dwordx4 v[38:41], v[52:53], off offset:1024
	global_load_dwordx4 v[42:45], v[52:53], off offset:2048
	global_load_dwordx4 v[46:49], v[52:53], off offset:3072
	s_movk_i32 s2, 0x3000
	v_add_co_u32_e32 v116, vcc, s2, v118
	s_waitcnt lgkmcnt(0)
	s_nop 0
	v_addc_co_u32_e32 v117, vcc, 0, v119, vcc
	v_add_co_u32_e32 v132, vcc, s21, v118
	s_barrier
	s_nop 0
	v_addc_co_u32_e32 v133, vcc, 0, v119, vcc
	global_load_dwordx4 v[50:53], v[132:133], off offset:-4096
	global_load_dwordx4 v[54:57], v[116:117], off offset:1024
	global_load_dwordx4 v[58:61], v[116:117], off offset:2048
	v_bitop3_b32 v1, v140, v0, 15 bitop3:0x78
	v_lshl_or_b32 v134, v1, 4, v220
	ds_read_b128 v[62:65], v134
	ds_read_b128 v[66:69], v134 offset:8192
	ds_read_b128 v[70:73], v134 offset:16384
	ds_read_b128 v[74:77], v134 offset:24576
	ds_read_b128 v[78:81], v134 offset:32768
	ds_read_b128 v[84:87], v134 offset:40960
	ds_read_b128 v[88:91], v134 offset:49152
	ds_read_b128 v[92:95], v134 offset:57344
	s_mul_i32 s7, s20, 48
	v_lshl_or_b32 v82, v140, 2, s7
	s_mul_i32 s7, s20, 0x60
	s_add_i32 s7, s7, 0x10000
	v_mul_u32_u24_e32 v1, 0x556, v0
	v_lshl_or_b32 v250, v140, 3, s7
	s_or_b32 s7, s16, 64
	v_lshrrev_b32_e32 v143, 16, v1
	s_movk_i32 s6, 0x600
	s_mov_b32 s2, 0x1800000
	s_mov_b32 s3, s15
	v_or_b32_e32 v139, s7, v143
	s_waitcnt vmcnt(8) lgkmcnt(7)
	v_mfma_f32_16x16x32_f16 v[96:99], v[26:29], v[62:65], 0
	s_waitcnt lgkmcnt(6)
	v_mfma_f32_16x16x32_f16 v[100:103], v[26:29], v[66:69], 0
	s_waitcnt lgkmcnt(5)
	v_mfma_f32_16x16x32_f16 v[104:107], v[26:29], v[70:73], 0
	s_waitcnt lgkmcnt(4)
	v_mfma_f32_16x16x32_f16 v[108:111], v[26:29], v[74:77], 0
	s_waitcnt lgkmcnt(3)
	v_mfma_f32_16x16x32_f16 v[112:115], v[26:29], v[78:81], 0
	s_waitcnt lgkmcnt(2)
	v_mfma_f32_16x16x32_f16 v[120:123], v[26:29], v[84:87], 0
	s_waitcnt lgkmcnt(1)
	v_mfma_f32_16x16x32_f16 v[124:127], v[26:29], v[88:91], 0
	s_waitcnt lgkmcnt(0)
	v_mfma_f32_16x16x32_f16 v[26:29], v[26:29], v[92:95], 0
	v_mfma_f32_16x16x32_f16 v[128:131], v[2:5], v[62:65], 0
	v_mfma_f32_16x16x32_f16 v[146:149], v[2:5], v[66:69], 0
	v_mfma_f32_16x16x32_f16 v[150:153], v[2:5], v[70:73], 0
	v_mfma_f32_16x16x32_f16 v[154:157], v[2:5], v[74:77], 0
	v_mfma_f32_16x16x32_f16 v[158:161], v[2:5], v[78:81], 0
	v_mfma_f32_16x16x32_f16 v[162:165], v[2:5], v[84:87], 0
	v_mfma_f32_16x16x32_f16 v[166:169], v[2:5], v[88:91], 0
	v_mfma_f32_16x16x32_f16 v[2:5], v[2:5], v[92:95], 0
	v_mfma_f32_16x16x32_f16 v[62:65], v[6:9], v[62:65], 0
	v_mfma_f32_16x16x32_f16 v[66:69], v[6:9], v[66:69], 0
	v_mfma_f32_16x16x32_f16 v[70:73], v[6:9], v[70:73], 0
	v_mfma_f32_16x16x32_f16 v[74:77], v[6:9], v[74:77], 0
	v_mfma_f32_16x16x32_f16 v[78:81], v[6:9], v[78:81], 0
	v_mfma_f32_16x16x32_f16 v[84:87], v[6:9], v[84:87], 0
	v_mfma_f32_16x16x32_f16 v[88:91], v[6:9], v[88:91], 0
	v_mfma_f32_16x16x32_f16 v[6:9], v[6:9], v[92:95], 0
	global_load_dwordx4 v[92:95], v[116:117], off offset:3072
	global_load_dwordx4 v[170:173], v[132:133], off
	global_load_dwordx4 v[174:177], v[132:133], off offset:1024
	v_bitop3_b32 v1, v140, v145, 4 bitop3:0x36
	v_lshl_or_b32 v1, v1, 4, v220
	ds_read_b128 v[178:181], v1
	ds_read_b128 v[182:185], v1 offset:8192
	ds_read_b128 v[186:189], v1 offset:16384
	ds_read_b128 v[190:193], v1 offset:24576
	ds_read_b128 v[194:197], v1 offset:32768
	ds_read_b128 v[198:201], v1 offset:40960
	ds_read_b128 v[202:205], v1 offset:49152
	ds_read_b128 v[206:209], v1 offset:57344
	s_waitcnt lgkmcnt(7)
	v_mfma_f32_16x16x32_f16 v[96:99], v[10:13], v[178:181], v[96:99]
	s_waitcnt lgkmcnt(6)
	v_mfma_f32_16x16x32_f16 v[100:103], v[10:13], v[182:185], v[100:103]
	s_waitcnt lgkmcnt(5)
	v_mfma_f32_16x16x32_f16 v[104:107], v[10:13], v[186:189], v[104:107]
	s_waitcnt lgkmcnt(4)
	v_mfma_f32_16x16x32_f16 v[108:111], v[10:13], v[190:193], v[108:111]
	s_waitcnt lgkmcnt(3)
	v_mfma_f32_16x16x32_f16 v[112:115], v[10:13], v[194:197], v[112:115]
	s_waitcnt lgkmcnt(2)
	v_mfma_f32_16x16x32_f16 v[120:123], v[10:13], v[198:201], v[120:123]
	s_waitcnt lgkmcnt(1)
	v_mfma_f32_16x16x32_f16 v[124:127], v[10:13], v[202:205], v[124:127]
	s_waitcnt lgkmcnt(0)
	v_mfma_f32_16x16x32_f16 v[10:13], v[10:13], v[206:209], v[26:29]
	v_mfma_f32_16x16x32_f16 v[26:29], v[14:17], v[178:181], v[128:131]
	v_mfma_f32_16x16x32_f16 v[128:131], v[14:17], v[182:185], v[146:149]
	v_mfma_f32_16x16x32_f16 v[146:149], v[14:17], v[186:189], v[150:153]
	v_mfma_f32_16x16x32_f16 v[150:153], v[14:17], v[190:193], v[154:157]
	v_mfma_f32_16x16x32_f16 v[154:157], v[14:17], v[194:197], v[158:161]
	v_mfma_f32_16x16x32_f16 v[158:161], v[14:17], v[198:201], v[162:165]
	v_mfma_f32_16x16x32_f16 v[162:165], v[14:17], v[202:205], v[166:169]
	v_mfma_f32_16x16x32_f16 v[2:5], v[14:17], v[206:209], v[2:5]
	v_mfma_f32_16x16x32_f16 v[14:17], v[18:21], v[178:181], v[62:65]
	v_mfma_f32_16x16x32_f16 v[62:65], v[18:21], v[182:185], v[66:69]
	v_mfma_f32_16x16x32_f16 v[66:69], v[18:21], v[186:189], v[70:73]
	v_mfma_f32_16x16x32_f16 v[70:73], v[18:21], v[190:193], v[74:77]
	v_mfma_f32_16x16x32_f16 v[74:77], v[18:21], v[194:197], v[78:81]
	v_mfma_f32_16x16x32_f16 v[78:81], v[18:21], v[198:201], v[84:87]
	v_mfma_f32_16x16x32_f16 v[84:87], v[18:21], v[202:205], v[88:91]
	v_mfma_f32_16x16x32_f16 v[6:9], v[18:21], v[206:209], v[6:9]
	s_movk_i32 s8, 0x5000
	v_add_co_u32_e32 v116, vcc, s8, v118
	global_load_dwordx4 v[88:91], v[132:133], off offset:2048
	global_load_dwordx4 v[166:169], v[132:133], off offset:3072
	v_addc_co_u32_e32 v117, vcc, 0, v119, vcc
	global_load_dwordx4 v[178:181], v[116:117], off
	v_bitop3_b32 v18, v140, v145, 8 bitop3:0x36
	v_lshl_or_b32 v133, v18, 4, v220
	ds_read_b128 v[18:21], v133
	ds_read_b128 v[182:185], v133 offset:8192
	ds_read_b128 v[186:189], v133 offset:16384
	ds_read_b128 v[190:193], v133 offset:24576
	ds_read_b128 v[194:197], v133 offset:32768
	ds_read_b128 v[198:201], v133 offset:40960
	ds_read_b128 v[202:205], v133 offset:49152
	ds_read_b128 v[206:209], v133 offset:57344
	s_waitcnt lgkmcnt(7)
	v_mfma_f32_16x16x32_f16 v[96:99], v[22:25], v[18:21], v[96:99]
	s_waitcnt lgkmcnt(6)
	v_mfma_f32_16x16x32_f16 v[100:103], v[22:25], v[182:185], v[100:103]
	s_waitcnt lgkmcnt(5)
	v_mfma_f32_16x16x32_f16 v[104:107], v[22:25], v[186:189], v[104:107]
	s_waitcnt lgkmcnt(4)
	v_mfma_f32_16x16x32_f16 v[108:111], v[22:25], v[190:193], v[108:111]
	s_waitcnt lgkmcnt(3)
	v_mfma_f32_16x16x32_f16 v[112:115], v[22:25], v[194:197], v[112:115]
	s_waitcnt lgkmcnt(2)
	v_mfma_f32_16x16x32_f16 v[120:123], v[22:25], v[198:201], v[120:123]
	s_waitcnt lgkmcnt(1)
	v_mfma_f32_16x16x32_f16 v[124:127], v[22:25], v[202:205], v[124:127]
	s_waitcnt lgkmcnt(0)
	v_mfma_f32_16x16x32_f16 v[10:13], v[22:25], v[206:209], v[10:13]
	s_waitcnt vmcnt(13)
	v_mfma_f32_16x16x32_f16 v[22:25], v[30:33], v[18:21], v[26:29]
	v_mfma_f32_16x16x32_f16 v[26:29], v[30:33], v[182:185], v[128:131]
	v_mfma_f32_16x16x32_f16 v[128:131], v[30:33], v[186:189], v[146:149]
	v_mfma_f32_16x16x32_f16 v[146:149], v[30:33], v[190:193], v[150:153]
	v_mfma_f32_16x16x32_f16 v[150:153], v[30:33], v[194:197], v[154:157]
	v_mfma_f32_16x16x32_f16 v[154:157], v[30:33], v[198:201], v[158:161]
	v_mfma_f32_16x16x32_f16 v[158:161], v[30:33], v[202:205], v[162:165]
	v_mfma_f32_16x16x32_f16 v[2:5], v[30:33], v[206:209], v[2:5]
	s_waitcnt vmcnt(12)
	v_mfma_f32_16x16x32_f16 v[14:17], v[34:37], v[18:21], v[14:17]
	v_mfma_f32_16x16x32_f16 v[18:21], v[34:37], v[182:185], v[62:65]
	v_mfma_f32_16x16x32_f16 v[30:33], v[34:37], v[186:189], v[66:69]
	v_mfma_f32_16x16x32_f16 v[62:65], v[34:37], v[190:193], v[70:73]
	v_mfma_f32_16x16x32_f16 v[66:69], v[34:37], v[194:197], v[74:77]
	v_mfma_f32_16x16x32_f16 v[70:73], v[34:37], v[198:201], v[78:81]
	v_mfma_f32_16x16x32_f16 v[74:77], v[34:37], v[202:205], v[84:87]
	v_mfma_f32_16x16x32_f16 v[6:9], v[34:37], v[206:209], v[6:9]
	s_nop 0
	global_load_dwordx4 v[78:81], v[116:117], off offset:1024
	global_load_dwordx4 v[162:165], v[116:117], off offset:2048
	global_load_dwordx4 v[182:185], v[116:117], off offset:3072
	v_bitop3_b32 v34, v140, v145, 12 bitop3:0x36
	v_lshl_or_b32 v135, v34, 4, v220
	ds_read_b128 v[34:37], v135
	ds_read_b128 v[84:87], v135 offset:8192
	ds_read_b128 v[186:189], v135 offset:16384
	ds_read_b128 v[190:193], v135 offset:24576
	ds_read_b128 v[194:197], v135 offset:32768
	ds_read_b128 v[198:201], v135 offset:40960
	ds_read_b128 v[202:205], v135 offset:49152
	ds_read_b128 v[206:209], v135 offset:57344
	s_waitcnt vmcnt(14) lgkmcnt(7)
	v_mfma_f32_16x16x32_f16 v[96:99], v[38:41], v[34:37], v[96:99]
	s_waitcnt lgkmcnt(6)
	v_mfma_f32_16x16x32_f16 v[100:103], v[38:41], v[84:87], v[100:103]
	s_waitcnt lgkmcnt(5)
	v_mfma_f32_16x16x32_f16 v[104:107], v[38:41], v[186:189], v[104:107]
	s_waitcnt lgkmcnt(4)
	v_mfma_f32_16x16x32_f16 v[108:111], v[38:41], v[190:193], v[108:111]
	s_waitcnt lgkmcnt(3)
	v_mfma_f32_16x16x32_f16 v[112:115], v[38:41], v[194:197], v[112:115]
	s_waitcnt lgkmcnt(2)
	v_mfma_f32_16x16x32_f16 v[120:123], v[38:41], v[198:201], v[120:123]
	s_waitcnt lgkmcnt(1)
	v_mfma_f32_16x16x32_f16 v[124:127], v[38:41], v[202:205], v[124:127]
	s_waitcnt lgkmcnt(0)
	v_mfma_f32_16x16x32_f16 v[210:213], v[38:41], v[206:209], v[10:13]
	s_waitcnt vmcnt(13)
	v_mfma_f32_16x16x32_f16 v[22:25], v[42:45], v[34:37], v[22:25]
	v_mfma_f32_16x16x32_f16 v[214:217], v[42:45], v[84:87], v[26:29]
	v_mfma_f32_16x16x32_f16 v[128:131], v[42:45], v[186:189], v[128:131]
	v_mfma_f32_16x16x32_f16 v[146:149], v[42:45], v[190:193], v[146:149]
	v_mfma_f32_16x16x32_f16 v[150:153], v[42:45], v[194:197], v[150:153]
	v_mfma_f32_16x16x32_f16 v[154:157], v[42:45], v[198:201], v[154:157]
	v_mfma_f32_16x16x32_f16 v[158:161], v[42:45], v[202:205], v[158:161]
	v_mfma_f32_16x16x32_f16 v[2:5], v[42:45], v[206:209], v[2:5]
	s_waitcnt vmcnt(12)
	v_mfma_f32_16x16x32_f16 v[14:17], v[46:49], v[34:37], v[14:17]
	v_mfma_f32_16x16x32_f16 v[18:21], v[46:49], v[84:87], v[18:21]
	v_mfma_f32_16x16x32_f16 v[30:33], v[46:49], v[186:189], v[30:33]
	v_mfma_f32_16x16x32_f16 v[34:37], v[46:49], v[190:193], v[62:65]
	v_mfma_f32_16x16x32_f16 v[42:45], v[46:49], v[194:197], v[66:69]
	v_mfma_f32_16x16x32_f16 v[62:65], v[46:49], v[198:201], v[70:73]
	v_mfma_f32_16x16x32_f16 v[66:69], v[46:49], v[202:205], v[74:77]
	v_mfma_f32_16x16x32_f16 v[6:9], v[46:49], v[206:209], v[6:9]
	s_mov_b32 s8, 0x30000
	v_add_co_u32_e32 v116, vcc, s8, v118
	s_mov_b32 s8, 0x31000
	s_nop 0
	v_addc_co_u32_e32 v117, vcc, 0, v119, vcc
	v_add_co_u32_e32 v218, vcc, s8, v118
	v_bitop3_b32 v46, v140, v145, 16 bitop3:0x36
	s_nop 0
	v_addc_co_u32_e32 v219, vcc, 0, v119, vcc
	global_load_dwordx4 v[38:41], v[218:219], off offset:-4096
	global_load_dwordx4 v[26:29], v[116:117], off offset:1024
	global_load_dwordx4 v[10:13], v[116:117], off offset:2048
	v_lshl_or_b32 v136, v46, 4, v220
	ds_read_b128 v[46:49], v136
	ds_read_b128 v[70:73], v136 offset:8192
	ds_read_b128 v[74:77], v136 offset:16384
	ds_read_b128 v[84:87], v136 offset:24576
	ds_read_b128 v[186:189], v136 offset:32768
	ds_read_b128 v[190:193], v136 offset:40960
	ds_read_b128 v[194:197], v136 offset:49152
	ds_read_b128 v[198:201], v136 offset:57344
	s_waitcnt vmcnt(14) lgkmcnt(7)
	v_mfma_f32_16x16x32_f16 v[96:99], v[50:53], v[46:49], v[96:99]
	s_waitcnt lgkmcnt(6)
	v_mfma_f32_16x16x32_f16 v[100:103], v[50:53], v[70:73], v[100:103]
	s_waitcnt lgkmcnt(5)
	v_mfma_f32_16x16x32_f16 v[104:107], v[50:53], v[74:77], v[104:107]
	s_waitcnt lgkmcnt(4)
	v_mfma_f32_16x16x32_f16 v[108:111], v[50:53], v[84:87], v[108:111]
	s_waitcnt lgkmcnt(3)
	v_mfma_f32_16x16x32_f16 v[112:115], v[50:53], v[186:189], v[112:115]
	s_waitcnt lgkmcnt(2)
	v_mfma_f32_16x16x32_f16 v[120:123], v[50:53], v[190:193], v[120:123]
	s_waitcnt lgkmcnt(1)
	v_mfma_f32_16x16x32_f16 v[124:127], v[50:53], v[194:197], v[124:127]
	s_waitcnt lgkmcnt(0)
	v_mfma_f32_16x16x32_f16 v[50:53], v[50:53], v[198:201], v[210:213]
	s_waitcnt vmcnt(13)
	v_mfma_f32_16x16x32_f16 v[202:205], v[54:57], v[46:49], v[22:25]
	v_mfma_f32_16x16x32_f16 v[206:209], v[54:57], v[70:73], v[214:217]
	v_mfma_f32_16x16x32_f16 v[128:131], v[54:57], v[74:77], v[128:131]
	v_mfma_f32_16x16x32_f16 v[146:149], v[54:57], v[84:87], v[146:149]
	v_mfma_f32_16x16x32_f16 v[150:153], v[54:57], v[186:189], v[150:153]
	v_mfma_f32_16x16x32_f16 v[154:157], v[54:57], v[190:193], v[154:157]
	v_mfma_f32_16x16x32_f16 v[158:161], v[54:57], v[194:197], v[158:161]
	v_mfma_f32_16x16x32_f16 v[54:57], v[54:57], v[198:201], v[2:5]
	s_waitcnt vmcnt(12)
	v_mfma_f32_16x16x32_f16 v[14:17], v[58:61], v[46:49], v[14:17]
	v_mfma_f32_16x16x32_f16 v[18:21], v[58:61], v[70:73], v[18:21]
	v_mfma_f32_16x16x32_f16 v[30:33], v[58:61], v[74:77], v[30:33]
	v_mfma_f32_16x16x32_f16 v[34:37], v[58:61], v[84:87], v[34:37]
	v_mfma_f32_16x16x32_f16 v[42:45], v[58:61], v[186:189], v[42:45]
	v_mfma_f32_16x16x32_f16 v[46:49], v[58:61], v[190:193], v[62:65]
	v_mfma_f32_16x16x32_f16 v[62:65], v[58:61], v[194:197], v[66:69]
	v_mfma_f32_16x16x32_f16 v[58:61], v[58:61], v[198:201], v[6:9]
	global_load_dwordx4 v[22:25], v[116:117], off offset:3072
	s_nop 1
	global_load_dwordx4 v[6:9], v[218:219], off
	global_load_dwordx4 v[2:5], v[218:219], off offset:1024
	v_bitop3_b32 v66, v140, v145, 20 bitop3:0x36
	v_lshl_or_b32 v137, v66, 4, v220
	ds_read_b128 v[66:69], v137
	ds_read_b128 v[70:73], v137 offset:8192
	ds_read_b128 v[74:77], v137 offset:16384
	ds_read_b128 v[84:87], v137 offset:24576
	ds_read_b128 v[186:189], v137 offset:32768
	ds_read_b128 v[190:193], v137 offset:40960
	ds_read_b128 v[194:197], v137 offset:49152
	ds_read_b128 v[198:201], v137 offset:57344
	s_waitcnt vmcnt(14) lgkmcnt(7)
	v_mfma_f32_16x16x32_f16 v[96:99], v[92:95], v[66:69], v[96:99]
	s_waitcnt lgkmcnt(6)
	v_mfma_f32_16x16x32_f16 v[100:103], v[92:95], v[70:73], v[100:103]
	s_waitcnt lgkmcnt(5)
	v_mfma_f32_16x16x32_f16 v[104:107], v[92:95], v[74:77], v[104:107]
	s_waitcnt lgkmcnt(4)
	v_mfma_f32_16x16x32_f16 v[108:111], v[92:95], v[84:87], v[108:111]
	s_waitcnt lgkmcnt(3)
	v_mfma_f32_16x16x32_f16 v[112:115], v[92:95], v[186:189], v[112:115]
	s_waitcnt lgkmcnt(2)
	v_mfma_f32_16x16x32_f16 v[210:213], v[92:95], v[190:193], v[120:123]
	s_waitcnt lgkmcnt(1)
	v_mfma_f32_16x16x32_f16 v[124:127], v[92:95], v[194:197], v[124:127]
	s_waitcnt lgkmcnt(0)
	v_mfma_f32_16x16x32_f16 v[50:53], v[92:95], v[198:201], v[50:53]
	s_waitcnt vmcnt(13)
	v_mfma_f32_16x16x32_f16 v[92:95], v[170:173], v[66:69], v[202:205]
	v_mfma_f32_16x16x32_f16 v[202:205], v[170:173], v[70:73], v[206:209]
	v_mfma_f32_16x16x32_f16 v[128:131], v[170:173], v[74:77], v[128:131]
	v_mfma_f32_16x16x32_f16 v[146:149], v[170:173], v[84:87], v[146:149]
	v_mfma_f32_16x16x32_f16 v[150:153], v[170:173], v[186:189], v[150:153]
	v_mfma_f32_16x16x32_f16 v[154:157], v[170:173], v[190:193], v[154:157]
	v_mfma_f32_16x16x32_f16 v[158:161], v[170:173], v[194:197], v[158:161]
	v_mfma_f32_16x16x32_f16 v[54:57], v[170:173], v[198:201], v[54:57]
	s_waitcnt vmcnt(12)
	v_mfma_f32_16x16x32_f16 v[66:69], v[174:177], v[66:69], v[14:17]
	v_mfma_f32_16x16x32_f16 v[70:73], v[174:177], v[70:73], v[18:21]
	v_mfma_f32_16x16x32_f16 v[74:77], v[174:177], v[74:77], v[30:33]
	v_mfma_f32_16x16x32_f16 v[34:37], v[174:177], v[84:87], v[34:37]
	v_mfma_f32_16x16x32_f16 v[42:45], v[174:177], v[186:189], v[42:45]
	v_mfma_f32_16x16x32_f16 v[46:49], v[174:177], v[190:193], v[46:49]
	v_mfma_f32_16x16x32_f16 v[62:65], v[174:177], v[194:197], v[62:65]
	v_mfma_f32_16x16x32_f16 v[58:61], v[174:177], v[198:201], v[58:61]
	s_mov_b32 s8, 0x33000
	v_add_co_u32_e32 v122, vcc, s8, v118
	global_load_dwordx4 v[30:33], v[218:219], off offset:2048
	global_load_dwordx4 v[14:17], v[218:219], off offset:3072
	v_addc_co_u32_e32 v123, vcc, 0, v119, vcc
	global_load_dwordx4 v[18:21], v[122:123], off offset:-4096
	v_bitop3_b32 v84, v140, v145, 24 bitop3:0x36
	v_lshl_or_b32 v138, v84, 4, v220
	ds_read_b128 v[84:87], v138
	ds_read_b128 v[170:173], v138 offset:8192
	ds_read_b128 v[174:177], v138 offset:16384
	ds_read_b128 v[186:189], v138 offset:24576
	ds_read_b128 v[190:193], v138 offset:32768
	ds_read_b128 v[194:197], v138 offset:40960
	ds_read_b128 v[198:201], v138 offset:49152
	ds_read_b128 v[206:209], v138 offset:57344
	s_mov_b32 s8, 0x32000
	v_add_co_u32_e32 v116, vcc, s8, v118
	s_nop 1
	v_addc_co_u32_e32 v117, vcc, 0, v119, vcc
	s_waitcnt vmcnt(14) lgkmcnt(7)
	v_mfma_f32_16x16x32_f16 v[96:99], v[88:91], v[84:87], v[96:99]
	s_waitcnt lgkmcnt(6)
	v_mfma_f32_16x16x32_f16 v[100:103], v[88:91], v[170:173], v[100:103]
	s_waitcnt lgkmcnt(5)
	v_mfma_f32_16x16x32_f16 v[104:107], v[88:91], v[174:177], v[104:107]
	s_waitcnt lgkmcnt(4)
	v_mfma_f32_16x16x32_f16 v[108:111], v[88:91], v[186:189], v[108:111]
	s_waitcnt lgkmcnt(3)
	v_mfma_f32_16x16x32_f16 v[112:115], v[88:91], v[190:193], v[112:115]
	s_waitcnt lgkmcnt(2)
	v_mfma_f32_16x16x32_f16 v[210:213], v[88:91], v[194:197], v[210:213]
	s_waitcnt lgkmcnt(1)
	v_mfma_f32_16x16x32_f16 v[124:127], v[88:91], v[198:201], v[124:127]
	s_waitcnt lgkmcnt(0)
	v_mfma_f32_16x16x32_f16 v[50:53], v[88:91], v[206:209], v[50:53]
	s_waitcnt vmcnt(13)
	v_mfma_f32_16x16x32_f16 v[90:93], v[166:169], v[84:87], v[92:95]
	v_mfma_f32_16x16x32_f16 v[202:205], v[166:169], v[170:173], v[202:205]
	v_mfma_f32_16x16x32_f16 v[128:131], v[166:169], v[174:177], v[128:131]
	v_mfma_f32_16x16x32_f16 v[146:149], v[166:169], v[186:189], v[146:149]
	v_mfma_f32_16x16x32_f16 v[150:153], v[166:169], v[190:193], v[150:153]
	v_mfma_f32_16x16x32_f16 v[154:157], v[166:169], v[194:197], v[154:157]
	v_mfma_f32_16x16x32_f16 v[158:161], v[166:169], v[198:201], v[158:161]
	v_mfma_f32_16x16x32_f16 v[54:57], v[166:169], v[206:209], v[54:57]
	s_waitcnt vmcnt(12)
	v_mfma_f32_16x16x32_f16 v[166:169], v[178:181], v[84:87], v[66:69]
	v_mfma_f32_16x16x32_f16 v[170:173], v[178:181], v[170:173], v[70:73]
	v_mfma_f32_16x16x32_f16 v[174:177], v[178:181], v[174:177], v[74:77]
	v_mfma_f32_16x16x32_f16 v[186:189], v[178:181], v[186:189], v[34:37]
	v_mfma_f32_16x16x32_f16 v[190:193], v[178:181], v[190:193], v[42:45]
	v_mfma_f32_16x16x32_f16 v[194:197], v[178:181], v[194:197], v[46:49]
	v_mfma_f32_16x16x32_f16 v[198:201], v[178:181], v[198:201], v[62:65]
	v_mfma_f32_16x16x32_f16 v[178:181], v[178:181], v[206:209], v[58:61]
	s_nop 0
	global_load_dwordx4 v[46:49], v[116:117], off offset:1024
	global_load_dwordx4 v[42:45], v[116:117], off offset:2048
	global_load_dwordx4 v[34:37], v[116:117], off offset:3072
	v_bitop3_b32 v58, v140, v145, 28 bitop3:0x36
	v_lshl_or_b32 v140, v58, 4, v220
	ds_read_b128 v[58:61], v140
	ds_read_b128 v[62:65], v140 offset:8192
	ds_read_b128 v[206:209], v140 offset:16384
	ds_read_b128 v[214:217], v140 offset:24576
	ds_read_b128 v[218:221], v140 offset:32768
	ds_read_b128 v[222:225], v140 offset:40960
	ds_read_b128 v[226:229], v140 offset:49152
	ds_read_b128 v[230:233], v140 offset:57344
	s_waitcnt vmcnt(14) lgkmcnt(7)
	v_mfma_f32_16x16x32_f16 v[234:237], v[78:81], v[58:61], v[96:99]
	s_waitcnt lgkmcnt(6)
	v_mfma_f32_16x16x32_f16 v[238:241], v[78:81], v[62:65], v[100:103]
	s_waitcnt lgkmcnt(5)
	v_mfma_f32_16x16x32_f16 v[242:245], v[78:81], v[206:209], v[104:107]
	s_waitcnt lgkmcnt(4)
	v_mfma_f32_16x16x32_f16 v[246:249], v[78:81], v[214:217], v[108:111]
	s_waitcnt lgkmcnt(3)
	v_mfma_f32_16x16x32_f16 v[106:109], v[78:81], v[218:221], v[112:115]
	s_waitcnt lgkmcnt(2)
	v_mfma_f32_16x16x32_f16 v[102:105], v[78:81], v[222:225], v[210:213]
	s_waitcnt lgkmcnt(1)
	v_mfma_f32_16x16x32_f16 v[94:97], v[78:81], v[226:229], v[124:127]
	s_waitcnt lgkmcnt(0)
	v_mfma_f32_16x16x32_f16 v[86:89], v[78:81], v[230:233], v[50:53]
	s_waitcnt vmcnt(13)
	v_mfma_f32_16x16x32_f16 v[124:127], v[162:165], v[58:61], v[90:93]
	v_mfma_f32_16x16x32_f16 v[202:205], v[162:165], v[62:65], v[202:205]
	v_mfma_f32_16x16x32_f16 v[210:213], v[162:165], v[206:209], v[128:131]
	v_mfma_f32_16x16x32_f16 v[146:149], v[162:165], v[214:217], v[146:149]
	v_mfma_f32_16x16x32_f16 v[78:81], v[162:165], v[218:221], v[150:153]
	v_mfma_f32_16x16x32_f16 v[74:77], v[162:165], v[222:225], v[154:157]
	v_mfma_f32_16x16x32_f16 v[70:73], v[162:165], v[226:229], v[158:161]
	v_mfma_f32_16x16x32_f16 v[66:69], v[162:165], v[230:233], v[54:57]
	s_waitcnt vmcnt(12)
	v_mfma_f32_16x16x32_f16 v[150:153], v[182:185], v[58:61], v[166:169]
	v_mfma_f32_16x16x32_f16 v[154:157], v[182:185], v[62:65], v[170:173]
	v_mfma_f32_16x16x32_f16 v[114:117], v[182:185], v[206:209], v[174:177]
	v_mfma_f32_16x16x32_f16 v[110:113], v[182:185], v[214:217], v[186:189]
	v_mfma_f32_16x16x32_f16 v[62:65], v[182:185], v[218:221], v[190:193]
	v_mfma_f32_16x16x32_f16 v[58:61], v[182:185], v[222:225], v[194:197]
	v_mfma_f32_16x16x32_f16 v[54:57], v[182:185], v[226:229], v[198:201]
	v_mfma_f32_16x16x32_f16 v[50:53], v[182:185], v[230:233], v[178:181]
	v_lshl_add_u64 v[120:121], v[82:83], 2, s[4:5]
	global_load_dwordx4 v[98:101], v[120:121], off
	global_load_dwordx4 v[90:93], v[120:121], off offset:64
	global_load_dwordx4 v[82:85], v[120:121], off offset:128
	s_movk_i32 s5, 0x310
	v_mad_u32_u24 v130, v145, s5, v250
	v_mov_b32_e32 v158, v239
	v_mov_b32_e32 v159, v240
	v_mov_b32_e32 v160, v243
	v_mov_b32_e32 v161, v244
	v_mov_b32_e32 v162, v247
	v_mov_b32_e32 v163, v248
	v_mov_b32_e32 v164, v203
	v_mov_b32_e32 v165, v204
	v_mov_b32_e32 v169, v148
	v_mov_b32_e32 v166, v211
	v_mov_b32_e32 v167, v212
	v_mov_b32_e32 v168, v147
	s_barrier
	v_add_u32_e32 v132, 0x3000, v130
	v_add_u32_e32 v131, 0x6000, v130
	s_mov_b32 s4, 0xfffffd0
	v_mul_lo_u32 v176, v143, s4
	s_waitcnt vmcnt(2)
	v_pk_add_f32 v[170:171], v[234:235], v[98:99]
	v_pk_add_f32 v[172:173], v[236:237], v[100:101]
	v_add_f32_e32 v145, v238, v98
	v_pk_mov_b32 v[128:129], v[98:99], v[100:101] op_sel:[1,0]
	v_add_f32_e32 v99, v241, v101
	s_waitcnt vmcnt(1)
	v_pk_add_f32 v[124:125], v[124:125], v[90:91]
	v_pk_add_f32 v[174:175], v[126:127], v[92:93]
	v_add_f32_e32 v180, v202, v90
	v_pk_mov_b32 v[126:127], v[90:91], v[92:93] op_sel:[1,0]
	v_add_f32_e32 v91, v205, v93
	v_add_f32_e32 v100, v242, v98
	v_add_f32_e32 v177, v245, v101
	v_add_f32_e32 v92, v210, v90
	v_add_f32_e32 v181, v213, v93
	v_add_f32_e32 v183, v149, v93
	v_cvt_pk_f16_f32 v149, v172, v173
	v_cvt_f16_f32_e32 v145, v145
	v_cvt_f16_f32_e32 v99, v99
	v_cvt_pk_f16_f32 v148, v170, v171
	v_cvt_f16_f32_e32 v100, v100
	v_cvt_f16_f32_e32 v170, v177
	v_cvt_pk_f16_f32 v124, v124, v125
	v_cvt_pk_f16_f32 v125, v174, v175
	v_add_f32_e32 v182, v146, v90
	s_waitcnt vmcnt(0)
	v_pk_add_f32 v[146:147], v[150:151], v[82:83]
	v_pk_add_f32 v[150:151], v[158:159], v[128:129]
	v_pk_add_f32 v[158:159], v[160:161], v[128:129]
	v_pk_add_f32 v[160:161], v[162:163], v[128:129]
	v_pk_add_f32 v[162:163], v[164:165], v[126:127]
	v_pk_add_f32 v[164:165], v[166:167], v[126:127]
	v_cvt_pk_f16_f32 v146, v146, v147
	v_cvt_pk_f16_f32 v147, v150, v151
	v_cvt_pk_f16_f32 v150, v158, v159
	v_cvt_pk_f16_f32 v151, v160, v161
	ds_write2_b64 v130, v[148:149], v[124:125] offset1:4
	v_pack_b32_f16 v124, v145, v147
	v_alignbit_b32 v125, v99, v147, 16
	v_cvt_pk_f16_f32 v158, v180, v162
	v_cvt_pk_f16_f32 v159, v163, v91
	v_pack_b32_f16 v148, v100, v150
	v_alignbit_b32 v149, v170, v150, 16
	v_cvt_pk_f16_f32 v160, v92, v164
	v_cvt_pk_f16_f32 v161, v165, v181
	ds_write2_b64 v132, v[124:125], v[158:159] offset0:32 offset1:36
	ds_write2_b64 v131, v[148:149], v[160:161] offset0:64 offset1:68
	v_pk_add_f32 v[124:125], v[152:153], v[84:85]
	v_add_f32_e32 v92, v154, v82
	v_cvt_pk_f16_f32 v147, v124, v125
	v_pk_mov_b32 v[124:125], v[82:83], v[84:85] op_sel:[1,0]
	v_add_f32_e32 v83, v157, v85
	ds_write_b64 v130, v[146:147] offset:64
	v_mov_b32_e32 v146, v155
	v_mov_b32_e32 v147, v156
	v_pk_add_f32 v[146:147], v[146:147], v[124:125]
	v_add_f32_e32 v178, v246, v98
	v_cvt_pk_f16_f32 v146, v92, v146
	v_cvt_pk_f16_f32 v147, v147, v83
	v_add_f32_e32 v83, v114, v82
	v_add_f32_e32 v84, v117, v85
	v_mov_b32_e32 v114, v115
	v_mov_b32_e32 v115, v116
	v_pk_add_f32 v[114:115], v[114:115], v[124:125]
	v_add_f32_e32 v179, v249, v101
	v_cvt_pk_f16_f32 v114, v83, v114
	v_cvt_pk_f16_f32 v115, v115, v84
	v_add_f32_e32 v83, v110, v82
	v_add_f32_e32 v84, v113, v85
	v_mov_b32_e32 v110, v111
	v_mov_b32_e32 v111, v112
	v_cvt_f16_f32_e32 v171, v178
	v_cvt_f16_f32_e32 v172, v179
	v_pk_add_f32 v[166:167], v[168:169], v[126:127]
	v_pk_add_f32 v[110:111], v[110:111], v[124:125]
	v_cvt_pk_f16_f32 v110, v83, v110
	v_cvt_pk_f16_f32 v111, v111, v84
	v_or_b32_e32 v83, s16, v143
	ds_write_b64 v130, v[110:111] offset:37696
	v_add_lshl_u32 v111, v176, v0, 4
	v_mul_lo_u32 v112, v83, s6
	v_mul_u32_u24_e32 v83, 0x310, v143
	v_mul_u32_u24_e32 v84, 0x556, v141
	v_pack_b32_f16 v150, v171, v151
	v_alignbit_b32 v151, v172, v151, 16
	v_cvt_pk_f16_f32 v162, v182, v166
	v_cvt_pk_f16_f32 v163, v167, v183
	v_add_u32_e32 v91, 0x9000, v130
	v_add3_u32 v83, v111, v83, s14
	v_lshrrev_b32_e32 v154, 16, v84
	ds_write2_b64 v91, v[150:151], v[162:163] offset0:96 offset1:100
	ds_write_b64 v130, v[146:147] offset:12608
	ds_write_b64 v130, v[114:115] offset:25152
	s_waitcnt lgkmcnt(0)
	s_barrier
	ds_read_b128 v[114:117], v83
	v_mul_lo_u32 v84, v154, s4
	v_add_lshl_u32 v113, v84, v141, 4
	v_mul_u32_u24_e32 v84, 0x310, v154
	v_add3_u32 v84, v113, v84, s14
	ds_read_b128 v[146:149], v84
	v_add_u32_e32 v92, v111, v112
	s_waitcnt lgkmcnt(1)
	buffer_store_dwordx4 v[114:117], v92, s[0:3], 0 offen sc1
	v_or_b32_e32 v92, s16, v154
	s_nop 0
	v_mul_lo_u32 v114, v92, s6
	v_add_u32_e32 v92, v113, v114
	s_waitcnt lgkmcnt(0)
	buffer_store_dwordx4 v[146:149], v92, s[0:3], 0 offen sc1
	v_or_b32_e32 v92, 0x400, v0
	v_mul_u32_u24_e32 v99, 0x556, v92
	v_lshrrev_b32_e32 v155, 16, v99
	v_mul_lo_u32 v99, v155, s4
	v_add_lshl_u32 v115, v99, v92, 4
	v_mul_u32_u24_e32 v92, 0x310, v155
	v_mul_u32_u24_e32 v99, 0x556, v142
	v_add3_u32 v92, v115, v92, s14
	v_lshrrev_b32_e32 v156, 16, v99
	ds_read_b128 v[146:149], v92
	v_mul_lo_u32 v99, v156, s4
	v_add_lshl_u32 v117, v99, v142, 4
	v_mul_u32_u24_e32 v99, 0x310, v156
	v_or_b32_e32 v100, s16, v155
	v_add3_u32 v99, v117, v99, s14
	v_mul_lo_u32 v116, v100, s6
	ds_read_b128 v[150:153], v99
	v_add_u32_e32 v100, v115, v116
	s_waitcnt lgkmcnt(1)
	buffer_store_dwordx4 v[146:149], v100, s[0:3], 0 offen sc1
	v_or_b32_e32 v100, s16, v156
	v_mul_lo_u32 v142, v100, s6
	v_add_u32_e32 v100, v117, v142
	v_or_b32_e32 v0, 0x800, v0
	s_waitcnt lgkmcnt(0)
	buffer_store_dwordx4 v[150:153], v100, s[0:3], 0 offen sc1
	v_mul_u32_u24_e32 v100, 0xaab, v0
	v_lshrrev_b32_e32 v157, 17, v100
	v_mul_lo_u32 v100, v157, s4
	v_or_b32_e32 v110, s16, v157
	v_add_lshl_u32 v143, v100, v0, 4
	v_mul_lo_u32 v141, v110, s6
	v_mul_u32_u24_e32 v100, 0x310, v157
	v_mul_u32_u24_e32 v110, 0xaab, v144
	v_add3_u32 v100, v100, v143, s14
	v_lshrrev_b32_e32 v158, 17, v110
	ds_read_b128 v[146:149], v100
	v_mul_lo_u32 v110, v158, s4
	v_add_lshl_u32 v144, v110, v144, 4
	v_mul_u32_u24_e32 v110, 0x310, v158
	v_add3_u32 v110, v110, v144, s14
	ds_read_b128 v[150:153], v110
	v_add_u32_e32 v0, v143, v141
	s_waitcnt lgkmcnt(1)
	buffer_store_dwordx4 v[146:149], v0, s[0:3], 0 offen sc1
	v_or_b32_e32 v0, s16, v158
	v_mul_lo_u32 v145, v0, s6
	v_add_u32_e32 v0, v144, v145
	s_waitcnt lgkmcnt(0)
	buffer_store_dwordx4 v[150:153], v0, s[0:3], 0 offen sc1
	v_add_f32_e32 v0, v106, v98
	v_mov_b32_e32 v106, v107
	v_mov_b32_e32 v107, v108
	v_pk_add_f32 v[106:107], v[106:107], v[128:129]
	v_add_f32_e32 v108, v109, v101
	v_cvt_pk_f16_f32 v106, v0, v106
	v_add_f32_e32 v0, v102, v98
	v_mov_b32_e32 v102, v103
	v_mov_b32_e32 v103, v104
	v_pk_add_f32 v[102:103], v[102:103], v[128:129]
	v_add_f32_e32 v104, v105, v101
	v_cvt_pk_f16_f32 v102, v0, v102
	v_add_f32_e32 v0, v94, v98
	v_mov_b32_e32 v94, v95
	v_mov_b32_e32 v95, v96
	v_pk_add_f32 v[94:95], v[94:95], v[128:129]
	v_add_f32_e32 v96, v97, v101
	v_cvt_pk_f16_f32 v94, v0, v94
	v_add_f32_e32 v0, v86, v98
	v_mov_b32_e32 v86, v87
	v_mov_b32_e32 v87, v88
	v_pk_add_f32 v[86:87], v[86:87], v[128:129]
	v_add_f32_e32 v88, v89, v101
	v_cvt_pk_f16_f32 v86, v0, v86
	v_add_f32_e32 v0, v78, v90
	v_mov_b32_e32 v78, v79
	v_mov_b32_e32 v79, v80
	v_pk_add_f32 v[78:79], v[78:79], v[126:127]
	v_add_f32_e32 v80, v81, v93
	v_cvt_pk_f16_f32 v78, v0, v78
	v_add_f32_e32 v0, v74, v90
	v_mov_b32_e32 v74, v75
	v_mov_b32_e32 v75, v76
	v_pk_add_f32 v[74:75], v[74:75], v[126:127]
	v_add_f32_e32 v76, v77, v93
	v_cvt_pk_f16_f32 v74, v0, v74
	v_add_f32_e32 v0, v70, v90
	v_mov_b32_e32 v70, v71
	v_mov_b32_e32 v71, v72
	v_pk_add_f32 v[70:71], v[70:71], v[126:127]
	v_add_f32_e32 v72, v73, v93
	v_cvt_pk_f16_f32 v70, v0, v70
	v_add_f32_e32 v0, v66, v90
	v_mov_b32_e32 v66, v67
	v_mov_b32_e32 v67, v68
	v_pk_add_f32 v[66:67], v[66:67], v[126:127]
	v_add_f32_e32 v68, v69, v93
	v_cvt_pk_f16_f32 v66, v0, v66
	v_add_f32_e32 v0, v62, v82
	v_mov_b32_e32 v62, v63
	v_mov_b32_e32 v63, v64
	v_pk_add_f32 v[62:63], v[62:63], v[124:125]
	v_add_f32_e32 v64, v65, v85
	v_cvt_pk_f16_f32 v62, v0, v62
	v_add_f32_e32 v0, v58, v82
	v_mov_b32_e32 v58, v59
	v_mov_b32_e32 v59, v60
	v_pk_add_f32 v[58:59], v[58:59], v[124:125]
	v_add_f32_e32 v60, v61, v85
	v_cvt_pk_f16_f32 v58, v0, v58
	v_add_f32_e32 v0, v54, v82
	v_mov_b32_e32 v54, v55
	v_mov_b32_e32 v55, v56
	v_pk_add_f32 v[54:55], v[54:55], v[124:125]
	v_add_f32_e32 v56, v57, v85
	v_cvt_pk_f16_f32 v54, v0, v54
	v_add_f32_e32 v0, v50, v82
	v_mov_b32_e32 v50, v51
	v_mov_b32_e32 v51, v52
	v_add_f32_e32 v52, v53, v85
	v_pk_add_f32 v[50:51], v[50:51], v[124:125]
	v_cvt_pk_f16_f32 v107, v107, v108
	v_cvt_pk_f16_f32 v103, v103, v104
	v_cvt_pk_f16_f32 v95, v95, v96
	v_cvt_pk_f16_f32 v87, v87, v88
	v_cvt_pk_f16_f32 v79, v79, v80
	v_cvt_pk_f16_f32 v75, v75, v76
	v_cvt_pk_f16_f32 v71, v71, v72
	v_cvt_pk_f16_f32 v67, v67, v68
	v_cvt_pk_f16_f32 v63, v63, v64
	v_cvt_pk_f16_f32 v59, v59, v60
	v_cvt_pk_f16_f32 v55, v55, v56
	v_cvt_pk_f16_f32 v50, v0, v50
	v_cvt_pk_f16_f32 v51, v51, v52
	s_barrier
	ds_write2_b64 v130, v[106:107], v[78:79] offset1:4
	ds_write2_b64 v132, v[102:103], v[74:75] offset0:32 offset1:36
	ds_write2_b64 v131, v[94:95], v[70:71] offset0:64 offset1:68
	ds_write2_b64 v91, v[86:87], v[66:67] offset0:96 offset1:100
	ds_write_b64 v130, v[62:63] offset:64
	ds_write_b64 v130, v[58:59] offset:12608
	ds_write_b64 v130, v[54:55] offset:25152
	ds_write_b64 v130, v[50:51] offset:37696
	s_waitcnt lgkmcnt(0)
	s_barrier
	global_load_dwordx4 v[50:53], v[122:123], off
	global_load_dwordx4 v[54:57], v[122:123], off offset:1024
	global_load_dwordx4 v[58:61], v[122:123], off offset:2048
	ds_read_b128 v[62:65], v83
	ds_read_b128 v[70:73], v84
	v_mul_lo_u32 v68, v139, s6
	v_add_u32_e32 v0, v68, v111
	ds_read_b128 v[74:77], v99
	s_waitcnt lgkmcnt(2)
	buffer_store_dwordx4 v[62:65], v0, s[0:3], 0 offen sc1
	v_or_b32_e32 v0, s7, v154
	v_mul_lo_u32 v69, v0, s6
	ds_read_b128 v[62:65], v92
	v_add_u32_e32 v0, v113, v69
	s_waitcnt lgkmcnt(2)
	buffer_store_dwordx4 v[70:73], v0, s[0:3], 0 offen sc1
	v_or_b32_e32 v0, s7, v155
	s_nop 0
	v_mul_lo_u32 v72, v0, s6
	v_add_u32_e32 v0, v115, v72
	s_waitcnt lgkmcnt(0)
	buffer_store_dwordx4 v[62:65], v0, s[0:3], 0 offen sc1
	v_or_b32_e32 v0, s7, v156
	v_mul_lo_u32 v70, v0, s6
	ds_read_b128 v[62:65], v100
	v_add_u32_e32 v0, v117, v70
	buffer_store_dwordx4 v[74:77], v0, s[0:3], 0 offen sc1
	v_or_b32_e32 v0, s7, v157
	v_mul_lo_u32 v71, v0, s6
	v_add_u32_e32 v0, v143, v71
	ds_read_b128 v[74:77], v110
	s_waitcnt lgkmcnt(1)
	buffer_store_dwordx4 v[62:65], v0, s[0:3], 0 offen sc1
	ds_read_b128 v[62:65], v134
	ds_read_b128 v[78:81], v134 offset:8192
	ds_read_b128 v[86:89], v134 offset:16384
	ds_read_b128 v[94:97], v134 offset:24576
	ds_read_b128 v[102:105], v134 offset:32768
	ds_read_b128 v[106:109], v134 offset:40960
	ds_read_b128 v[124:127], v134 offset:49152
	ds_read_b128 v[146:149], v134 offset:57344
	v_or_b32_e32 v0, s7, v158
	v_mul_lo_u32 v73, v0, s6
	v_add_u32_e32 v0, v144, v73
	s_waitcnt lgkmcnt(8)
	buffer_store_dwordx4 v[74:77], v0, s[0:3], 0 offen sc1
	s_waitcnt lgkmcnt(7)
	s_nop 0
	v_mfma_f32_16x16x32_f16 v[74:77], v[38:41], v[62:65], 0
	s_waitcnt lgkmcnt(6)
	v_mfma_f32_16x16x32_f16 v[150:153], v[38:41], v[78:81], 0
	s_waitcnt lgkmcnt(5)
	v_mfma_f32_16x16x32_f16 v[154:157], v[38:41], v[86:89], 0
	s_waitcnt lgkmcnt(4)
	v_mfma_f32_16x16x32_f16 v[158:161], v[38:41], v[94:97], 0
	s_waitcnt lgkmcnt(3)
	v_mfma_f32_16x16x32_f16 v[162:165], v[38:41], v[102:105], 0
	s_waitcnt lgkmcnt(2)
	v_mfma_f32_16x16x32_f16 v[166:169], v[38:41], v[106:109], 0
	s_waitcnt lgkmcnt(1)
	v_mfma_f32_16x16x32_f16 v[170:173], v[38:41], v[124:127], 0
	s_waitcnt lgkmcnt(0)
	v_mfma_f32_16x16x32_f16 v[38:41], v[38:41], v[146:149], 0
	v_mfma_f32_16x16x32_f16 v[174:177], v[26:29], v[62:65], 0
	v_mfma_f32_16x16x32_f16 v[178:181], v[26:29], v[78:81], 0
	v_mfma_f32_16x16x32_f16 v[182:185], v[26:29], v[86:89], 0
	v_mfma_f32_16x16x32_f16 v[186:189], v[26:29], v[94:97], 0
	v_mfma_f32_16x16x32_f16 v[190:193], v[26:29], v[102:105], 0
	v_mfma_f32_16x16x32_f16 v[194:197], v[26:29], v[106:109], 0
	v_mfma_f32_16x16x32_f16 v[198:201], v[26:29], v[124:127], 0
	v_mfma_f32_16x16x32_f16 v[26:29], v[26:29], v[146:149], 0
	v_mfma_f32_16x16x32_f16 v[62:65], v[10:13], v[62:65], 0
	v_mfma_f32_16x16x32_f16 v[78:81], v[10:13], v[78:81], 0
	v_mfma_f32_16x16x32_f16 v[86:89], v[10:13], v[86:89], 0
	v_mfma_f32_16x16x32_f16 v[94:97], v[10:13], v[94:97], 0
	v_mfma_f32_16x16x32_f16 v[102:105], v[10:13], v[102:105], 0
	v_mfma_f32_16x16x32_f16 v[106:109], v[10:13], v[106:109], 0
	v_mfma_f32_16x16x32_f16 v[124:127], v[10:13], v[124:127], 0
	v_mfma_f32_16x16x32_f16 v[10:13], v[10:13], v[146:149], 0
	s_mov_b32 s4, 0x34000
	v_add_co_u32_e32 v66, vcc, s4, v118
	s_mov_b32 s4, 0x35000
	s_nop 0
	v_addc_co_u32_e32 v67, vcc, 0, v119, vcc
	v_add_co_u32_e32 v118, vcc, s4, v118
	s_nop 1
	v_addc_co_u32_e32 v119, vcc, 0, v119, vcc
	global_load_dwordx4 v[146:149], v[118:119], off offset:-4096
	global_load_dwordx4 v[202:205], v[122:123], off offset:3072
	global_load_dwordx4 v[206:209], v[66:67], off offset:1024
	ds_read_b128 v[210:213], v1
	ds_read_b128 v[214:217], v1 offset:8192
	ds_read_b128 v[218:221], v1 offset:16384
	ds_read_b128 v[222:225], v1 offset:24576
	ds_read_b128 v[226:229], v1 offset:32768
	ds_read_b128 v[230:233], v1 offset:40960
	ds_read_b128 v[234:237], v1 offset:49152
	ds_read_b128 v[238:241], v1 offset:57344
	s_waitcnt lgkmcnt(7)
	v_mfma_f32_16x16x32_f16 v[74:77], v[22:25], v[210:213], v[74:77]
	s_waitcnt lgkmcnt(6)
	v_mfma_f32_16x16x32_f16 v[150:153], v[22:25], v[214:217], v[150:153]
	s_waitcnt lgkmcnt(5)
	v_mfma_f32_16x16x32_f16 v[154:157], v[22:25], v[218:221], v[154:157]
	s_waitcnt lgkmcnt(4)
	v_mfma_f32_16x16x32_f16 v[158:161], v[22:25], v[222:225], v[158:161]
	s_waitcnt lgkmcnt(3)
	v_mfma_f32_16x16x32_f16 v[162:165], v[22:25], v[226:229], v[162:165]
	s_waitcnt lgkmcnt(2)
	v_mfma_f32_16x16x32_f16 v[166:169], v[22:25], v[230:233], v[166:169]
	s_waitcnt lgkmcnt(1)
	v_mfma_f32_16x16x32_f16 v[170:173], v[22:25], v[234:237], v[170:173]
	s_waitcnt lgkmcnt(0)
	v_mfma_f32_16x16x32_f16 v[22:25], v[22:25], v[238:241], v[38:41]
	v_mfma_f32_16x16x32_f16 v[38:41], v[6:9], v[210:213], v[174:177]
	v_mfma_f32_16x16x32_f16 v[174:177], v[6:9], v[214:217], v[178:181]
	v_mfma_f32_16x16x32_f16 v[178:181], v[6:9], v[218:221], v[182:185]
	v_mfma_f32_16x16x32_f16 v[182:185], v[6:9], v[222:225], v[186:189]
	v_mfma_f32_16x16x32_f16 v[186:189], v[6:9], v[226:229], v[190:193]
	v_mfma_f32_16x16x32_f16 v[190:193], v[6:9], v[230:233], v[194:197]
	v_mfma_f32_16x16x32_f16 v[194:197], v[6:9], v[234:237], v[198:201]
	v_mfma_f32_16x16x32_f16 v[6:9], v[6:9], v[238:241], v[26:29]
	v_mfma_f32_16x16x32_f16 v[26:29], v[2:5], v[210:213], v[62:65]
	v_mfma_f32_16x16x32_f16 v[62:65], v[2:5], v[214:217], v[78:81]
	v_mfma_f32_16x16x32_f16 v[78:81], v[2:5], v[218:221], v[86:89]
	v_mfma_f32_16x16x32_f16 v[86:89], v[2:5], v[222:225], v[94:97]
	v_mfma_f32_16x16x32_f16 v[94:97], v[2:5], v[226:229], v[102:105]
	v_mfma_f32_16x16x32_f16 v[102:105], v[2:5], v[230:233], v[106:109]
	v_mfma_f32_16x16x32_f16 v[106:109], v[2:5], v[234:237], v[124:127]
	v_mfma_f32_16x16x32_f16 v[0:3], v[2:5], v[238:241], v[10:13]
	s_nop 2
	global_load_dwordx4 v[10:13], v[66:67], off offset:2048
	global_load_dwordx4 v[122:125], v[66:67], off offset:3072
	global_load_dwordx4 v[126:129], v[118:119], off
	ds_read_b128 v[198:201], v133
	ds_read_b128 v[210:213], v133 offset:8192
	ds_read_b128 v[214:217], v133 offset:16384
	ds_read_b128 v[218:221], v133 offset:24576
	ds_read_b128 v[222:225], v133 offset:32768
	ds_read_b128 v[226:229], v133 offset:40960
	ds_read_b128 v[230:233], v133 offset:49152
	ds_read_b128 v[234:237], v133 offset:57344
	s_waitcnt lgkmcnt(7)
	v_mfma_f32_16x16x32_f16 v[74:77], v[30:33], v[198:201], v[74:77]
	s_waitcnt lgkmcnt(6)
	v_mfma_f32_16x16x32_f16 v[150:153], v[30:33], v[210:213], v[150:153]
	s_waitcnt lgkmcnt(5)
	v_mfma_f32_16x16x32_f16 v[154:157], v[30:33], v[214:217], v[154:157]
	s_waitcnt lgkmcnt(4)
	v_mfma_f32_16x16x32_f16 v[158:161], v[30:33], v[218:221], v[158:161]
	s_waitcnt lgkmcnt(3)
	v_mfma_f32_16x16x32_f16 v[162:165], v[30:33], v[222:225], v[162:165]
	s_waitcnt lgkmcnt(2)
	v_mfma_f32_16x16x32_f16 v[166:169], v[30:33], v[226:229], v[166:169]
	s_waitcnt lgkmcnt(1)
	v_mfma_f32_16x16x32_f16 v[170:173], v[30:33], v[230:233], v[170:173]
	s_waitcnt lgkmcnt(0)
	v_mfma_f32_16x16x32_f16 v[22:25], v[30:33], v[234:237], v[22:25]
	v_mfma_f32_16x16x32_f16 v[30:33], v[14:17], v[198:201], v[38:41]
	v_mfma_f32_16x16x32_f16 v[38:41], v[14:17], v[210:213], v[174:177]
	v_mfma_f32_16x16x32_f16 v[174:177], v[14:17], v[214:217], v[178:181]
	v_mfma_f32_16x16x32_f16 v[178:181], v[14:17], v[218:221], v[182:185]
	v_mfma_f32_16x16x32_f16 v[182:185], v[14:17], v[222:225], v[186:189]
	v_mfma_f32_16x16x32_f16 v[186:189], v[14:17], v[226:229], v[190:193]
	v_mfma_f32_16x16x32_f16 v[190:193], v[14:17], v[230:233], v[194:197]
	v_mfma_f32_16x16x32_f16 v[4:7], v[14:17], v[234:237], v[6:9]
	v_mfma_f32_16x16x32_f16 v[14:17], v[18:21], v[198:201], v[26:29]
	v_mfma_f32_16x16x32_f16 v[26:29], v[18:21], v[210:213], v[62:65]
	v_mfma_f32_16x16x32_f16 v[62:65], v[18:21], v[214:217], v[78:81]
	v_mfma_f32_16x16x32_f16 v[78:81], v[18:21], v[218:221], v[86:89]
	v_mfma_f32_16x16x32_f16 v[86:89], v[18:21], v[222:225], v[94:97]
	v_mfma_f32_16x16x32_f16 v[94:97], v[18:21], v[226:229], v[102:105]
	v_mfma_f32_16x16x32_f16 v[102:105], v[18:21], v[230:233], v[106:109]
	v_mfma_f32_16x16x32_f16 v[0:3], v[18:21], v[234:237], v[0:3]
	global_load_dwordx4 v[18:21], v[118:119], off offset:1024
	s_nop 0
	global_load_dwordx4 v[106:109], v[118:119], off offset:2048
	global_load_dwordx4 v[194:197], v[118:119], off offset:3072
	ds_read_b128 v[198:201], v135
	ds_read_b128 v[210:213], v135 offset:8192
	ds_read_b128 v[214:217], v135 offset:16384
	ds_read_b128 v[218:221], v135 offset:24576
	ds_read_b128 v[222:225], v135 offset:32768
	ds_read_b128 v[226:229], v135 offset:40960
	ds_read_b128 v[230:233], v135 offset:49152
	ds_read_b128 v[234:237], v135 offset:57344
	s_waitcnt lgkmcnt(7)
	v_mfma_f32_16x16x32_f16 v[74:77], v[46:49], v[198:201], v[74:77]
	s_waitcnt lgkmcnt(6)
	v_mfma_f32_16x16x32_f16 v[150:153], v[46:49], v[210:213], v[150:153]
	s_waitcnt lgkmcnt(5)
	v_mfma_f32_16x16x32_f16 v[154:157], v[46:49], v[214:217], v[154:157]
	s_waitcnt lgkmcnt(4)
	v_mfma_f32_16x16x32_f16 v[158:161], v[46:49], v[218:221], v[158:161]
	s_waitcnt lgkmcnt(3)
	v_mfma_f32_16x16x32_f16 v[162:165], v[46:49], v[222:225], v[162:165]
	s_waitcnt lgkmcnt(2)
	v_mfma_f32_16x16x32_f16 v[166:169], v[46:49], v[226:229], v[166:169]
	s_waitcnt lgkmcnt(1)
	v_mfma_f32_16x16x32_f16 v[170:173], v[46:49], v[230:233], v[170:173]
	s_waitcnt lgkmcnt(0)
	v_mfma_f32_16x16x32_f16 v[22:25], v[46:49], v[234:237], v[22:25]
	v_mfma_f32_16x16x32_f16 v[30:33], v[42:45], v[198:201], v[30:33]
	v_mfma_f32_16x16x32_f16 v[38:41], v[42:45], v[210:213], v[38:41]
	v_mfma_f32_16x16x32_f16 v[46:49], v[42:45], v[214:217], v[174:177]
	v_mfma_f32_16x16x32_f16 v[174:177], v[42:45], v[218:221], v[178:181]
	v_mfma_f32_16x16x32_f16 v[178:181], v[42:45], v[222:225], v[182:185]
	v_mfma_f32_16x16x32_f16 v[182:185], v[42:45], v[226:229], v[186:189]
	v_mfma_f32_16x16x32_f16 v[186:189], v[42:45], v[230:233], v[190:193]
	v_mfma_f32_16x16x32_f16 v[4:7], v[42:45], v[234:237], v[4:7]
	v_mfma_f32_16x16x32_f16 v[14:17], v[34:37], v[198:201], v[14:17]
	v_mfma_f32_16x16x32_f16 v[26:29], v[34:37], v[210:213], v[26:29]
	v_mfma_f32_16x16x32_f16 v[42:45], v[34:37], v[214:217], v[62:65]
	v_mfma_f32_16x16x32_f16 v[62:65], v[34:37], v[218:221], v[78:81]
	v_mfma_f32_16x16x32_f16 v[78:81], v[34:37], v[222:225], v[86:89]
	v_mfma_f32_16x16x32_f16 v[86:89], v[34:37], v[226:229], v[94:97]
	v_mfma_f32_16x16x32_f16 v[94:97], v[34:37], v[230:233], v[102:105]
	v_mfma_f32_16x16x32_f16 v[0:3], v[34:37], v[234:237], v[0:3]
	ds_read_b128 v[34:37], v136
	s_nop 0
	ds_read_b128 v[102:105], v136 offset:8192
	ds_read_b128 v[190:193], v136 offset:16384
	ds_read_b128 v[198:201], v136 offset:24576
	ds_read_b128 v[210:213], v136 offset:32768
	ds_read_b128 v[214:217], v136 offset:40960
	ds_read_b128 v[218:221], v136 offset:49152
	ds_read_b128 v[222:225], v136 offset:57344
	s_waitcnt vmcnt(17) lgkmcnt(7)
	v_mfma_f32_16x16x32_f16 v[74:77], v[50:53], v[34:37], v[74:77]
	s_waitcnt lgkmcnt(6)
	v_mfma_f32_16x16x32_f16 v[150:153], v[50:53], v[102:105], v[150:153]
	s_waitcnt lgkmcnt(5)
	v_mfma_f32_16x16x32_f16 v[154:157], v[50:53], v[190:193], v[154:157]
	s_waitcnt lgkmcnt(4)
	v_mfma_f32_16x16x32_f16 v[158:161], v[50:53], v[198:201], v[158:161]
	s_waitcnt lgkmcnt(3)
	v_mfma_f32_16x16x32_f16 v[162:165], v[50:53], v[210:213], v[162:165]
	s_waitcnt lgkmcnt(2)
	v_mfma_f32_16x16x32_f16 v[166:169], v[50:53], v[214:217], v[166:169]
	s_waitcnt lgkmcnt(1)
	v_mfma_f32_16x16x32_f16 v[170:173], v[50:53], v[218:221], v[170:173]
	s_waitcnt lgkmcnt(0)
	v_mfma_f32_16x16x32_f16 v[22:25], v[50:53], v[222:225], v[22:25]
	s_waitcnt vmcnt(16)
	v_mfma_f32_16x16x32_f16 v[30:33], v[54:57], v[34:37], v[30:33]
	v_mfma_f32_16x16x32_f16 v[38:41], v[54:57], v[102:105], v[38:41]
	v_mfma_f32_16x16x32_f16 v[46:49], v[54:57], v[190:193], v[46:49]
	v_mfma_f32_16x16x32_f16 v[50:53], v[54:57], v[198:201], v[174:177]
	v_mfma_f32_16x16x32_f16 v[174:177], v[54:57], v[210:213], v[178:181]
	v_mfma_f32_16x16x32_f16 v[178:181], v[54:57], v[214:217], v[182:185]
	v_mfma_f32_16x16x32_f16 v[182:185], v[54:57], v[218:221], v[186:189]
	v_mfma_f32_16x16x32_f16 v[4:7], v[54:57], v[222:225], v[4:7]
	s_waitcnt vmcnt(15)
	v_mfma_f32_16x16x32_f16 v[14:17], v[58:61], v[34:37], v[14:17]
	v_mfma_f32_16x16x32_f16 v[26:29], v[58:61], v[102:105], v[26:29]
	v_mfma_f32_16x16x32_f16 v[34:37], v[58:61], v[190:193], v[42:45]
	v_mfma_f32_16x16x32_f16 v[42:45], v[58:61], v[198:201], v[62:65]
	v_mfma_f32_16x16x32_f16 v[54:57], v[58:61], v[210:213], v[78:81]
	v_mfma_f32_16x16x32_f16 v[62:65], v[58:61], v[214:217], v[86:89]
	v_mfma_f32_16x16x32_f16 v[78:81], v[58:61], v[218:221], v[94:97]
	v_mfma_f32_16x16x32_f16 v[0:3], v[58:61], v[222:225], v[0:3]
	ds_read_b128 v[58:61], v137
	ds_read_b128 v[86:89], v137 offset:8192
	ds_read_b128 v[94:97], v137 offset:16384
	ds_read_b128 v[102:105], v137 offset:24576
	ds_read_b128 v[186:189], v137 offset:32768
	ds_read_b128 v[190:193], v137 offset:40960
	ds_read_b128 v[198:201], v137 offset:49152
	ds_read_b128 v[134:137], v137 offset:57344
	s_waitcnt vmcnt(7) lgkmcnt(7)
	v_mfma_f32_16x16x32_f16 v[74:77], v[202:205], v[58:61], v[74:77]
	s_waitcnt lgkmcnt(6)
	v_mfma_f32_16x16x32_f16 v[150:153], v[202:205], v[86:89], v[150:153]
	s_waitcnt lgkmcnt(5)
	v_mfma_f32_16x16x32_f16 v[154:157], v[202:205], v[94:97], v[154:157]
	s_waitcnt lgkmcnt(4)
	v_mfma_f32_16x16x32_f16 v[158:161], v[202:205], v[102:105], v[158:161]
	s_waitcnt lgkmcnt(3)
	v_mfma_f32_16x16x32_f16 v[162:165], v[202:205], v[186:189], v[162:165]
	s_waitcnt lgkmcnt(2)
	v_mfma_f32_16x16x32_f16 v[166:169], v[202:205], v[190:193], v[166:169]
	s_waitcnt lgkmcnt(1)
	v_mfma_f32_16x16x32_f16 v[170:173], v[202:205], v[198:201], v[170:173]
	s_waitcnt lgkmcnt(0)
	v_mfma_f32_16x16x32_f16 v[22:25], v[202:205], v[134:137], v[22:25]
	v_mfma_f32_16x16x32_f16 v[30:33], v[146:149], v[58:61], v[30:33]
	v_mfma_f32_16x16x32_f16 v[38:41], v[146:149], v[86:89], v[38:41]
	v_mfma_f32_16x16x32_f16 v[46:49], v[146:149], v[94:97], v[46:49]
	v_mfma_f32_16x16x32_f16 v[50:53], v[146:149], v[102:105], v[50:53]
	v_mfma_f32_16x16x32_f16 v[174:177], v[146:149], v[186:189], v[174:177]
	v_mfma_f32_16x16x32_f16 v[178:181], v[146:149], v[190:193], v[178:181]
	v_mfma_f32_16x16x32_f16 v[182:185], v[146:149], v[198:201], v[182:185]
	v_mfma_f32_16x16x32_f16 v[4:7], v[146:149], v[134:137], v[4:7]
	s_waitcnt vmcnt(6)
	v_mfma_f32_16x16x32_f16 v[14:17], v[206:209], v[58:61], v[14:17]
	v_mfma_f32_16x16x32_f16 v[26:29], v[206:209], v[86:89], v[26:29]
	v_mfma_f32_16x16x32_f16 v[34:37], v[206:209], v[94:97], v[34:37]
	v_mfma_f32_16x16x32_f16 v[42:45], v[206:209], v[102:105], v[42:45]
	v_mfma_f32_16x16x32_f16 v[54:57], v[206:209], v[186:189], v[54:57]
	v_mfma_f32_16x16x32_f16 v[58:61], v[206:209], v[190:193], v[62:65]
	v_mfma_f32_16x16x32_f16 v[62:65], v[206:209], v[198:201], v[78:81]
	v_mfma_f32_16x16x32_f16 v[0:3], v[206:209], v[134:137], v[0:3]
	s_nop 1
	ds_read_b128 v[78:81], v138
	ds_read_b128 v[86:89], v138 offset:8192
	ds_read_b128 v[94:97], v138 offset:16384
	ds_read_b128 v[102:105], v138 offset:24576
	ds_read_b128 v[134:137], v138 offset:32768
	ds_read_b128 v[146:149], v138 offset:40960
	ds_read_b128 v[186:189], v138 offset:49152
	ds_read_b128 v[190:193], v138 offset:57344
	s_waitcnt vmcnt(5) lgkmcnt(7)
	v_mfma_f32_16x16x32_f16 v[74:77], v[10:13], v[78:81], v[74:77]
	s_waitcnt lgkmcnt(6)
	v_mfma_f32_16x16x32_f16 v[150:153], v[10:13], v[86:89], v[150:153]
	s_waitcnt lgkmcnt(5)
	v_mfma_f32_16x16x32_f16 v[154:157], v[10:13], v[94:97], v[154:157]
	s_waitcnt lgkmcnt(4)
	v_mfma_f32_16x16x32_f16 v[158:161], v[10:13], v[102:105], v[158:161]
	s_waitcnt lgkmcnt(3)
	v_mfma_f32_16x16x32_f16 v[162:165], v[10:13], v[134:137], v[162:165]
	s_waitcnt lgkmcnt(2)
	v_mfma_f32_16x16x32_f16 v[166:169], v[10:13], v[146:149], v[166:169]
	s_waitcnt lgkmcnt(1)
	v_mfma_f32_16x16x32_f16 v[170:173], v[10:13], v[186:189], v[170:173]
	s_waitcnt lgkmcnt(0)
	v_mfma_f32_16x16x32_f16 v[8:11], v[10:13], v[190:193], v[22:25]
	s_waitcnt vmcnt(4)
	v_mfma_f32_16x16x32_f16 v[22:25], v[122:125], v[78:81], v[30:33]
	v_mfma_f32_16x16x32_f16 v[30:33], v[122:125], v[86:89], v[38:41]
	v_mfma_f32_16x16x32_f16 v[198:201], v[122:125], v[94:97], v[46:49]
	v_mfma_f32_16x16x32_f16 v[48:51], v[122:125], v[102:105], v[50:53]
	v_mfma_f32_16x16x32_f16 v[174:177], v[122:125], v[134:137], v[174:177]
	v_mfma_f32_16x16x32_f16 v[178:181], v[122:125], v[146:149], v[178:181]
	v_mfma_f32_16x16x32_f16 v[182:185], v[122:125], v[186:189], v[182:185]
	v_mfma_f32_16x16x32_f16 v[4:7], v[122:125], v[190:193], v[4:7]
	s_waitcnt vmcnt(3)
	v_mfma_f32_16x16x32_f16 v[12:15], v[126:129], v[78:81], v[14:17]
	v_mfma_f32_16x16x32_f16 v[78:81], v[126:129], v[86:89], v[26:29]
	v_mfma_f32_16x16x32_f16 v[86:89], v[126:129], v[94:97], v[34:37]
	v_mfma_f32_16x16x32_f16 v[40:43], v[126:129], v[102:105], v[42:45]
	v_mfma_f32_16x16x32_f16 v[94:97], v[126:129], v[134:137], v[54:57]
	v_mfma_f32_16x16x32_f16 v[102:105], v[126:129], v[146:149], v[58:61]
	v_mfma_f32_16x16x32_f16 v[64:67], v[126:129], v[186:189], v[62:65]
	v_mfma_f32_16x16x32_f16 v[0:3], v[126:129], v[190:193], v[0:3]
	s_nop 1
	ds_read_b128 v[60:63], v140
	ds_read_b128 v[122:125], v140 offset:8192
	ds_read_b128 v[126:129], v140 offset:16384
	ds_read_b128 v[134:137], v140 offset:24576
	ds_read_b128 v[146:149], v140 offset:32768
	ds_read_b128 v[186:189], v140 offset:40960
	ds_read_b128 v[190:193], v140 offset:49152
	ds_read_b128 v[202:205], v140 offset:57344
	s_waitcnt vmcnt(2) lgkmcnt(7)
	v_mfma_f32_16x16x32_f16 v[74:77], v[18:21], v[60:63], v[74:77]
	s_waitcnt lgkmcnt(6)
	v_mfma_f32_16x16x32_f16 v[150:153], v[18:21], v[122:125], v[150:153]
	s_waitcnt lgkmcnt(5)
	v_mfma_f32_16x16x32_f16 v[154:157], v[18:21], v[126:129], v[154:157]
	s_waitcnt lgkmcnt(4)
	v_mfma_f32_16x16x32_f16 v[158:161], v[18:21], v[134:137], v[158:161]
	s_waitcnt lgkmcnt(3)
	v_mfma_f32_16x16x32_f16 v[56:59], v[18:21], v[146:149], v[162:165]
	s_waitcnt lgkmcnt(2)
	v_mfma_f32_16x16x32_f16 v[52:55], v[18:21], v[186:189], v[166:169]
	s_waitcnt lgkmcnt(1)
	v_mfma_f32_16x16x32_f16 v[44:47], v[18:21], v[190:193], v[170:173]
	s_waitcnt lgkmcnt(0)
	v_mfma_f32_16x16x32_f16 v[36:39], v[18:21], v[202:205], v[8:11]
	s_waitcnt vmcnt(1)
	v_mfma_f32_16x16x32_f16 v[162:165], v[106:109], v[60:63], v[22:25]
	v_mfma_f32_16x16x32_f16 v[166:169], v[106:109], v[122:125], v[30:33]
	v_mfma_f32_16x16x32_f16 v[170:173], v[106:109], v[126:129], v[198:201]
	v_mfma_f32_16x16x32_f16 v[198:201], v[106:109], v[134:137], v[48:51]
	v_mfma_f32_16x16x32_f16 v[32:35], v[106:109], v[146:149], v[174:177]
	v_mfma_f32_16x16x32_f16 v[24:27], v[106:109], v[186:189], v[178:181]
	v_mfma_f32_16x16x32_f16 v[20:23], v[106:109], v[190:193], v[182:185]
	v_mfma_f32_16x16x32_f16 v[16:19], v[106:109], v[202:205], v[4:7]
	s_waitcnt vmcnt(0)
	v_mfma_f32_16x16x32_f16 v[106:109], v[194:197], v[60:63], v[12:15]
	v_mfma_f32_16x16x32_f16 v[78:81], v[194:197], v[122:125], v[78:81]
	v_mfma_f32_16x16x32_f16 v[86:89], v[194:197], v[126:129], v[86:89]
	v_mfma_f32_16x16x32_f16 v[60:63], v[194:197], v[134:137], v[40:43]
	v_mfma_f32_16x16x32_f16 v[12:15], v[194:197], v[146:149], v[94:97]
	v_mfma_f32_16x16x32_f16 v[8:11], v[194:197], v[186:189], v[102:105]
	v_mfma_f32_16x16x32_f16 v[4:7], v[194:197], v[190:193], v[64:67]
	v_mfma_f32_16x16x32_f16 v[0:3], v[194:197], v[202:205], v[0:3]
	global_load_dwordx4 v[48:51], v[120:121], off offset:1536
	global_load_dwordx4 v[40:43], v[120:121], off offset:1600
	global_load_dwordx4 v[28:31], v[120:121], off offset:1664
	v_mov_b32_e32 v94, v155
	v_mov_b32_e32 v95, v156
	v_mov_b32_e32 v96, v159
	v_mov_b32_e32 v97, v160
	v_mov_b32_e32 v64, v151
	v_mov_b32_e32 v65, v152
	v_mov_b32_e32 v102, v167
	v_mov_b32_e32 v103, v168
	v_mov_b32_e32 v104, v171
	v_mov_b32_e32 v105, v172
	v_mov_b32_e32 v118, v199
	v_mov_b32_e32 v119, v200
	s_barrier
	s_waitcnt vmcnt(2)
	v_pk_add_f32 v[74:75], v[74:75], v[48:49]
	v_add_f32_e32 v82, v150, v48
	v_pk_mov_b32 v[120:121], v[48:49], v[50:51] op_sel:[1,0]
	v_add_f32_e32 v49, v153, v51
	s_waitcnt vmcnt(1)
	v_pk_add_f32 v[122:123], v[162:163], v[40:41]
	v_add_f32_e32 v98, v166, v40
	v_pk_mov_b32 v[66:67], v[40:41], v[42:43] op_sel:[1,0]
	v_add_f32_e32 v41, v169, v43
	v_pk_add_f32 v[76:77], v[76:77], v[50:51]
	v_add_f32_e32 v50, v154, v48
	v_add_f32_e32 v85, v157, v51
	v_add_f32_e32 v90, v158, v48
	v_add_f32_e32 v93, v161, v51
	v_pk_add_f32 v[124:125], v[164:165], v[42:43]
	v_add_f32_e32 v42, v170, v40
	v_add_f32_e32 v101, v173, v43
	v_add_f32_e32 v126, v198, v40
	v_add_f32_e32 v127, v201, v43
	v_cvt_f16_f32_e32 v98, v98
	v_cvt_f16_f32_e32 v41, v41
	v_cvt_pk_f16_f32 v74, v74, v75
	v_cvt_pk_f16_f32 v75, v76, v77
	v_cvt_f16_f32_e32 v50, v50
	v_pk_add_f32 v[76:77], v[94:95], v[120:121]
	v_cvt_f16_f32_e32 v85, v85
	v_cvt_f16_f32_e32 v90, v90
	v_pk_add_f32 v[94:95], v[96:97], v[120:121]
	v_cvt_f16_f32_e32 v93, v93
	v_cvt_pk_f16_f32 v96, v122, v123
	v_pk_add_f32 v[64:65], v[64:65], v[120:121]
	v_pk_add_f32 v[102:103], v[102:103], v[66:67]
	v_pk_add_f32 v[104:105], v[104:105], v[66:67]
	v_pk_add_f32 v[118:119], v[118:119], v[66:67]
	v_cvt_pk_f16_f32 v76, v76, v77
	v_cvt_pk_f16_f32 v77, v94, v95
	v_cvt_pk_f16_f32 v95, v102, v103
	s_waitcnt vmcnt(0)
	v_pk_add_f32 v[106:107], v[106:107], v[28:29]
	v_pk_add_f32 v[108:109], v[108:109], v[30:31]
	v_cvt_pk_f16_f32 v97, v124, v125
	v_cvt_pk_f16_f32 v64, v82, v64
	v_cvt_pk_f16_f32 v65, v65, v49
	v_pack_b32_f16 v94, v98, v95
	v_alignbit_b32 v95, v41, v95, 16
	v_add_f32_e32 v78, v78, v28
	v_cvt_pk_f16_f32 v106, v106, v107
	v_cvt_pk_f16_f32 v107, v108, v109
	ds_write2_b64 v130, v[74:75], v[96:97] offset1:4
	ds_write_b64 v130, v[106:107] offset:64
	v_pack_b32_f16 v74, v50, v76
	v_alignbit_b32 v75, v85, v76, 16
	v_pack_b32_f16 v76, v90, v77
	v_alignbit_b32 v77, v93, v77, 16
	v_cvt_pk_f16_f32 v96, v42, v104
	v_cvt_pk_f16_f32 v97, v105, v101
	v_cvt_pk_f16_f32 v102, v126, v118
	v_cvt_pk_f16_f32 v103, v119, v127
	ds_write2_b64 v132, v[64:65], v[94:95] offset0:32 offset1:36
	ds_write2_b64 v131, v[74:75], v[96:97] offset0:64 offset1:68
	ds_write2_b64 v91, v[76:77], v[102:103] offset0:96 offset1:100
	v_pk_mov_b32 v[64:65], v[28:29], v[30:31] op_sel:[1,0]
	v_add_f32_e32 v29, v81, v31
	v_mov_b32_e32 v74, v79
	v_mov_b32_e32 v75, v80
	v_pk_add_f32 v[74:75], v[74:75], v[64:65]
	v_add_f32_e32 v56, v56, v48
	v_cvt_pk_f16_f32 v74, v78, v74
	v_cvt_pk_f16_f32 v75, v75, v29
	v_add_f32_e32 v29, v86, v28
	v_add_f32_e32 v30, v89, v31
	ds_write_b64 v130, v[74:75] offset:12608
	v_mov_b32_e32 v74, v87
	v_mov_b32_e32 v75, v88
	v_pk_add_f32 v[74:75], v[74:75], v[64:65]
	v_add_f32_e32 v52, v52, v48
	v_cvt_pk_f16_f32 v74, v29, v74
	v_cvt_pk_f16_f32 v75, v75, v30
	v_add_f32_e32 v29, v60, v28
	v_add_f32_e32 v30, v63, v31
	v_mov_b32_e32 v60, v61
	v_mov_b32_e32 v61, v62
	v_pk_add_f32 v[60:61], v[60:61], v[64:65]
	ds_write_b64 v130, v[74:75] offset:25152
	v_cvt_pk_f16_f32 v60, v29, v60
	v_cvt_pk_f16_f32 v61, v61, v30
	ds_write_b64 v130, v[60:61] offset:37696
	s_waitcnt lgkmcnt(0)
	s_barrier
	ds_read_b128 v[60:63], v83
	ds_read_b128 v[74:77], v84
	v_add_u32_e32 v29, 0x300, v111
	v_add_u32_e32 v30, v29, v112
	v_add_f32_e32 v44, v44, v48
	s_waitcnt lgkmcnt(1)
	buffer_store_dwordx4 v[60:63], v30, s[0:3], 0 offen sc1
	v_add_u32_e32 v30, 0x300, v113
	ds_read_b128 v[60:63], v92
	v_add_u32_e32 v41, v30, v114
	s_waitcnt lgkmcnt(1)
	buffer_store_dwordx4 v[74:77], v41, s[0:3], 0 offen sc1
	ds_read_b128 v[74:77], v99
	v_add_u32_e32 v41, 0x300, v115
	v_add_u32_e32 v42, v41, v116
	s_waitcnt lgkmcnt(1)
	buffer_store_dwordx4 v[60:63], v42, s[0:3], 0 offen sc1
	v_add_u32_e32 v42, 0x300, v117
	ds_read_b128 v[60:63], v100
	v_add_u32_e32 v49, v42, v142
	s_waitcnt lgkmcnt(1)
	buffer_store_dwordx4 v[74:77], v49, s[0:3], 0 offen sc1
	ds_read_b128 v[74:77], v110
	v_add_u32_e32 v49, 0x300, v143
	v_add_u32_e32 v50, v49, v141
	s_waitcnt lgkmcnt(1)
	buffer_store_dwordx4 v[60:63], v50, s[0:3], 0 offen sc1
	v_add_u32_e32 v50, 0x300, v144
	v_add_f32_e32 v36, v36, v48
	v_add_u32_e32 v60, v50, v145
	s_waitcnt lgkmcnt(0)
	buffer_store_dwordx4 v[74:77], v60, s[0:3], 0 offen sc1
	v_cvt_f16_f32_e32 v60, v56
	v_mov_b32_e32 v56, v57
	v_mov_b32_e32 v57, v58
	v_add_f32_e32 v58, v59, v51
	v_cvt_f16_f32_e32 v58, v58
	v_pk_add_f32 v[56:57], v[56:57], v[120:121]
	v_add_f32_e32 v32, v32, v40
	v_cvt_pk_f16_f32 v57, v56, v57
	v_pack_b32_f16 v56, v60, v57
	v_alignbit_b32 v57, v58, v57, 16
	v_cvt_f16_f32_e32 v58, v52
	v_mov_b32_e32 v52, v53
	v_mov_b32_e32 v53, v54
	v_add_f32_e32 v54, v55, v51
	v_cvt_f16_f32_e32 v54, v54
	v_pk_add_f32 v[52:53], v[52:53], v[120:121]
	v_add_f32_e32 v24, v24, v40
	v_cvt_pk_f16_f32 v53, v52, v53
	v_pack_b32_f16 v52, v58, v53
	v_alignbit_b32 v53, v54, v53, 16
	v_cvt_f16_f32_e32 v54, v44
	v_mov_b32_e32 v44, v45
	v_mov_b32_e32 v45, v46
	v_add_f32_e32 v46, v47, v51
	v_cvt_f16_f32_e32 v46, v46
	v_pk_add_f32 v[44:45], v[44:45], v[120:121]
	s_nop 0
	v_cvt_pk_f16_f32 v45, v44, v45
	v_pack_b32_f16 v44, v54, v45
	v_alignbit_b32 v45, v46, v45, 16
	v_cvt_f16_f32_e32 v46, v36
	v_mov_b32_e32 v36, v37
	v_mov_b32_e32 v37, v38
	v_add_f32_e32 v38, v39, v51
	v_cvt_f16_f32_e32 v38, v38
	v_pk_add_f32 v[36:37], v[36:37], v[120:121]
	s_barrier
	v_cvt_pk_f16_f32 v37, v36, v37
	v_pack_b32_f16 v36, v46, v37
	v_alignbit_b32 v37, v38, v37, 16
	v_cvt_f16_f32_e32 v38, v32
	v_mov_b32_e32 v32, v33
	v_mov_b32_e32 v33, v34
	v_add_f32_e32 v34, v35, v43
	v_cvt_f16_f32_e32 v34, v34
	v_pk_add_f32 v[32:33], v[32:33], v[66:67]
	s_nop 0
	v_cvt_pk_f16_f32 v33, v32, v33
	v_pack_b32_f16 v32, v38, v33
	v_alignbit_b32 v33, v34, v33, 16
	ds_write2_b64 v130, v[56:57], v[32:33] offset1:4
	v_cvt_f16_f32_e32 v32, v24
	v_mov_b32_e32 v24, v25
	v_mov_b32_e32 v25, v26
	v_add_f32_e32 v26, v27, v43
	v_cvt_f16_f32_e32 v26, v26
	v_pk_add_f32 v[24:25], v[24:25], v[66:67]
	v_add_f32_e32 v20, v20, v40
	v_cvt_pk_f16_f32 v25, v24, v25
	v_pack_b32_f16 v24, v32, v25
	v_alignbit_b32 v25, v26, v25, 16
	ds_write2_b64 v132, v[52:53], v[24:25] offset0:32 offset1:36
	v_cvt_f16_f32_e32 v24, v20
	v_mov_b32_e32 v20, v21
	v_mov_b32_e32 v21, v22
	v_add_f32_e32 v22, v23, v43
	v_cvt_f16_f32_e32 v22, v22
	v_pk_add_f32 v[20:21], v[20:21], v[66:67]
	v_add_f32_e32 v16, v16, v40
	v_cvt_pk_f16_f32 v21, v20, v21
	v_pack_b32_f16 v20, v24, v21
	v_alignbit_b32 v21, v22, v21, 16
	ds_write2_b64 v131, v[44:45], v[20:21] offset0:64 offset1:68
	v_cvt_f16_f32_e32 v20, v16
	v_mov_b32_e32 v16, v17
	v_mov_b32_e32 v17, v18
	v_add_f32_e32 v18, v19, v43
	v_cvt_f16_f32_e32 v18, v18
	v_pk_add_f32 v[16:17], v[16:17], v[66:67]
	v_add_f32_e32 v12, v12, v28
	v_cvt_pk_f16_f32 v17, v16, v17
	v_pack_b32_f16 v16, v20, v17
	v_alignbit_b32 v17, v18, v17, 16
	ds_write2_b64 v91, v[36:37], v[16:17] offset0:96 offset1:100
	v_cvt_f16_f32_e32 v16, v12
	v_mov_b32_e32 v12, v13
	v_mov_b32_e32 v13, v14
	v_add_f32_e32 v14, v15, v31
	v_cvt_f16_f32_e32 v14, v14
	v_pk_add_f32 v[12:13], v[12:13], v[64:65]
	v_add_f32_e32 v8, v8, v28
	v_cvt_pk_f16_f32 v13, v12, v13
	v_pack_b32_f16 v12, v16, v13
	v_alignbit_b32 v13, v14, v13, 16
	ds_write_b64 v130, v[12:13] offset:64
	v_cvt_f16_f32_e32 v12, v8
	v_mov_b32_e32 v8, v9
	v_mov_b32_e32 v9, v10
	v_add_f32_e32 v10, v11, v31
	v_cvt_f16_f32_e32 v10, v10
	v_pk_add_f32 v[8:9], v[8:9], v[64:65]
	v_add_f32_e32 v4, v4, v28
	v_cvt_pk_f16_f32 v9, v8, v9
	v_pack_b32_f16 v8, v12, v9
	v_alignbit_b32 v9, v10, v9, 16
	ds_write_b64 v130, v[8:9] offset:12608
	v_cvt_f16_f32_e32 v8, v4
	v_mov_b32_e32 v4, v5
	v_mov_b32_e32 v5, v6
	v_add_f32_e32 v6, v7, v31
	v_cvt_f16_f32_e32 v6, v6
	v_pk_add_f32 v[4:5], v[4:5], v[64:65]
	v_add_f32_e32 v0, v0, v28
	v_cvt_pk_f16_f32 v5, v4, v5
	v_pack_b32_f16 v4, v8, v5
	v_alignbit_b32 v5, v6, v5, 16
	ds_write_b64 v130, v[4:5] offset:25152
	v_cvt_f16_f32_e32 v4, v0
	v_mov_b32_e32 v0, v1
	v_mov_b32_e32 v1, v2
	v_add_f32_e32 v2, v3, v31
	v_cvt_f16_f32_e32 v2, v2
	v_pk_add_f32 v[0:1], v[0:1], v[64:65]
	v_add_u32_e32 v8, v29, v68
	v_cvt_pk_f16_f32 v1, v0, v1
	v_pack_b32_f16 v0, v4, v1
	v_alignbit_b32 v1, v2, v1, 16
	ds_write_b64 v130, v[0:1] offset:37696
	s_waitcnt lgkmcnt(0)
	s_barrier
	ds_read_b128 v[0:3], v83
	ds_read_b128 v[4:7], v84
	v_add_u32_e32 v12, v42, v70
	s_waitcnt lgkmcnt(1)
	buffer_store_dwordx4 v[0:3], v8, s[0:3], 0 offen sc1
	ds_read_b128 v[0:3], v92
	v_add_u32_e32 v8, v30, v69
	s_waitcnt lgkmcnt(1)
	buffer_store_dwordx4 v[4:7], v8, s[0:3], 0 offen sc1
	v_add_u32_e32 v8, v41, v72
	ds_read_b128 v[4:7], v99
	s_waitcnt lgkmcnt(1)
	buffer_store_dwordx4 v[0:3], v8, s[0:3], 0 offen sc1
	ds_read_b128 v[0:3], v100
	ds_read_b128 v[8:11], v110
	s_waitcnt lgkmcnt(2)
	buffer_store_dwordx4 v[4:7], v12, s[0:3], 0 offen sc1
	s_nop 1
	v_add_u32_e32 v4, v49, v71
	s_waitcnt lgkmcnt(1)
	buffer_store_dwordx4 v[0:3], v4, s[0:3], 0 offen sc1
	s_nop 1
	v_add_u32_e32 v0, v50, v73
	s_waitcnt lgkmcnt(0)
	buffer_store_dwordx4 v[8:11], v0, s[0:3], 0 offen sc1
	s_endpgm

.LBB3_82:
	s_setprio 0
	s_mul_i32 s0, s9, s3
	s_lshl_b32 s1, s30, 6
	s_add_i32 s0, s0, s8
	s_or_b32 s1, s1, s31
	s_or_b32 s7, s1, s11
	s_mul_i32 s4, s0, 0x60000
	s_mul_hi_i32 s1, s0, 0x60000
	s_waitcnt lgkmcnt(0)
	s_add_u32 s6, s12, s4
	s_mulk_i32 s0, 0x300
	s_addc_u32 s8, s13, s1
	s_ashr_i32 s1, s0, 31
	s_lshl_b64 s[0:1], s[0:1], 2
	s_add_u32 s4, s14, s0
	s_addc_u32 s5, s15, s1
	s_mul_i32 s0, s2, 0x1800000
	s_mul_hi_u32 s1, s3, 0x1800000
	s_add_i32 s1, s1, s0
	s_mul_i32 s0, s3, 0x1800000
	s_add_u32 s0, s20, s0
	v_readfirstlane_b32 s2, v0
	s_addc_u32 s1, s21, s1
	s_lshr_b32 s9, s2, 6
	s_and_b32 s1, s1, 0xffff
	s_mul_i32 s2, s9, 0x6000
	v_and_b32_e32 v2, 63, v0
	s_mul_hi_u32 s3, s9, 0x6000
	s_add_u32 s2, s6, s2
	s_addc_u32 s3, s8, s3
	v_lshlrev_b32_e32 v82, 4, v2
	v_mov_b32_e32 v83, 0
	v_lshl_add_u64 v[118:119], s[2:3], 0, v[82:83]
	s_movk_i32 s6, 0x1000
	v_add_co_u32_e32 v50, vcc, s6, v118
	s_movk_i32 s6, 0x2000
	s_nop 0
	v_addc_co_u32_e32 v51, vcc, 0, v119, vcc
	v_add_co_u32_e32 v52, vcc, s6, v118
	global_load_dwordx4 v[2:5], v82, s[2:3] offset:1024
	global_load_dwordx4 v[6:9], v82, s[2:3] offset:2048
	v_addc_co_u32_e32 v53, vcc, 0, v119, vcc
	global_load_dwordx4 v[10:13], v82, s[2:3] offset:3072
	global_load_dwordx4 v[14:17], v[52:53], off offset:-4096
	global_load_dwordx4 v[18:21], v[50:51], off offset:1024
	global_load_dwordx4 v[22:25], v[50:51], off offset:2048
	global_load_dwordx4 v[26:29], v82, s[2:3]
	global_load_dwordx4 v[30:33], v[50:51], off offset:3072
	global_load_dwordx4 v[34:37], v[52:53], off
	global_load_dwordx4 v[38:41], v[52:53], off offset:1024
	global_load_dwordx4 v[42:45], v[52:53], off offset:2048
	global_load_dwordx4 v[46:49], v[52:53], off offset:3072
	s_movk_i32 s2, 0x3000
	v_add_co_u32_e32 v116, vcc, s2, v118
	s_movk_i32 s2, 0x4000
	s_nop 0
	v_addc_co_u32_e32 v117, vcc, 0, v119, vcc
	v_add_co_u32_e32 v156, vcc, s2, v118
	s_nop 1
	v_addc_co_u32_e32 v157, vcc, 0, v119, vcc
	s_barrier
	global_load_dwordx4 v[50:53], v[156:157], off offset:-4096
	global_load_dwordx4 v[54:57], v[116:117], off offset:1024
	global_load_dwordx4 v[58:61], v[116:117], off offset:2048
	v_mul_u32_u24_e32 v62, 0x556, v0
	v_lshlrev_b32_e32 v132, 9, v1
	v_lshrrev_b32_e32 v142, 16, v62
	v_xor_b32_e32 v62, v158, v1
	v_lshl_or_b32 v135, v62, 4, v132
	ds_read_b128 v[62:65], v135
	ds_read_b128 v[66:69], v135 offset:8192
	ds_read_b128 v[70:73], v135 offset:16384
	ds_read_b128 v[74:77], v135 offset:24576
	ds_read_b128 v[78:81], v135 offset:32768
	ds_read_b128 v[84:87], v135 offset:40960
	ds_read_b128 v[88:91], v135 offset:49152
	ds_read_b128 v[92:95], v135 offset:57344
	s_mul_i32 s6, s9, 48
	v_lshl_or_b32 v82, v158, 2, s6
	s_mul_i32 s6, s9, 0x60
	s_add_i32 s6, s6, 0x10000
	v_lshlrev_b32_e32 v96, 3, v142
	s_movk_i32 s9, 0x47
	v_lshl_or_b32 v248, v158, 3, s6
	s_or_b32 s6, s7, 8
	v_bitop3_b32 v143, v96, s9, v142 bitop3:0xc8
	s_mov_b32 s2, 0x1800000
	s_mov_b32 s3, 0x20000
	s_mov_b32 s8, 0x10000
	v_or_b32_e32 v140, s6, v143
	s_waitcnt vmcnt(8) lgkmcnt(7)
	v_mfma_f32_16x16x32_f16 v[96:99], v[26:29], v[62:65], 0
	s_waitcnt lgkmcnt(6)
	v_mfma_f32_16x16x32_f16 v[100:103], v[26:29], v[66:69], 0
	s_waitcnt lgkmcnt(5)
	v_mfma_f32_16x16x32_f16 v[104:107], v[26:29], v[70:73], 0
	s_waitcnt lgkmcnt(4)
	v_mfma_f32_16x16x32_f16 v[108:111], v[26:29], v[74:77], 0
	s_waitcnt lgkmcnt(3)
	v_mfma_f32_16x16x32_f16 v[112:115], v[26:29], v[78:81], 0
	s_waitcnt lgkmcnt(2)
	v_mfma_f32_16x16x32_f16 v[120:123], v[26:29], v[84:87], 0
	s_waitcnt lgkmcnt(1)
	v_mfma_f32_16x16x32_f16 v[124:127], v[26:29], v[88:91], 0
	s_waitcnt lgkmcnt(0)
	v_mfma_f32_16x16x32_f16 v[26:29], v[26:29], v[92:95], 0
	v_mfma_f32_16x16x32_f16 v[128:131], v[2:5], v[62:65], 0
	v_mfma_f32_16x16x32_f16 v[136:139], v[2:5], v[66:69], 0
	v_mfma_f32_16x16x32_f16 v[144:147], v[2:5], v[70:73], 0
	v_mfma_f32_16x16x32_f16 v[148:151], v[2:5], v[74:77], 0
	v_mfma_f32_16x16x32_f16 v[152:155], v[2:5], v[78:81], 0
	v_mfma_f32_16x16x32_f16 v[160:163], v[2:5], v[84:87], 0
	v_mfma_f32_16x16x32_f16 v[164:167], v[2:5], v[88:91], 0
	v_mfma_f32_16x16x32_f16 v[2:5], v[2:5], v[92:95], 0
	v_mfma_f32_16x16x32_f16 v[62:65], v[6:9], v[62:65], 0
	v_mfma_f32_16x16x32_f16 v[66:69], v[6:9], v[66:69], 0
	v_mfma_f32_16x16x32_f16 v[70:73], v[6:9], v[70:73], 0
	v_mfma_f32_16x16x32_f16 v[74:77], v[6:9], v[74:77], 0
	v_mfma_f32_16x16x32_f16 v[78:81], v[6:9], v[78:81], 0
	v_mfma_f32_16x16x32_f16 v[84:87], v[6:9], v[84:87], 0
	v_mfma_f32_16x16x32_f16 v[88:91], v[6:9], v[88:91], 0
	v_mfma_f32_16x16x32_f16 v[6:9], v[6:9], v[92:95], 0
	global_load_dwordx4 v[92:95], v[116:117], off offset:3072
	global_load_dwordx4 v[168:171], v[156:157], off
	global_load_dwordx4 v[172:175], v[156:157], off offset:1024
	v_bitop3_b32 v116, v158, v1, 4 bitop3:0x36
	v_lshl_or_b32 v133, v116, 4, v132
	ds_read_b128 v[176:179], v133
	ds_read_b128 v[180:183], v133 offset:8192
	ds_read_b128 v[184:187], v133 offset:16384
	ds_read_b128 v[188:191], v133 offset:24576
	ds_read_b128 v[192:195], v133 offset:32768
	ds_read_b128 v[196:199], v133 offset:40960
	ds_read_b128 v[200:203], v133 offset:49152
	ds_read_b128 v[204:207], v133 offset:57344
	s_waitcnt lgkmcnt(7)
	v_mfma_f32_16x16x32_f16 v[96:99], v[10:13], v[176:179], v[96:99]
	s_waitcnt lgkmcnt(6)
	v_mfma_f32_16x16x32_f16 v[100:103], v[10:13], v[180:183], v[100:103]
	s_waitcnt lgkmcnt(5)
	v_mfma_f32_16x16x32_f16 v[104:107], v[10:13], v[184:187], v[104:107]
	s_waitcnt lgkmcnt(4)
	v_mfma_f32_16x16x32_f16 v[108:111], v[10:13], v[188:191], v[108:111]
	s_waitcnt lgkmcnt(3)
	v_mfma_f32_16x16x32_f16 v[112:115], v[10:13], v[192:195], v[112:115]
	s_waitcnt lgkmcnt(2)
	v_mfma_f32_16x16x32_f16 v[120:123], v[10:13], v[196:199], v[120:123]
	s_waitcnt lgkmcnt(1)
	v_mfma_f32_16x16x32_f16 v[124:127], v[10:13], v[200:203], v[124:127]
	s_waitcnt lgkmcnt(0)
	v_mfma_f32_16x16x32_f16 v[10:13], v[10:13], v[204:207], v[26:29]
	v_mfma_f32_16x16x32_f16 v[26:29], v[14:17], v[176:179], v[128:131]
	v_mfma_f32_16x16x32_f16 v[128:131], v[14:17], v[180:183], v[136:139]
	v_mfma_f32_16x16x32_f16 v[136:139], v[14:17], v[184:187], v[144:147]
	v_mfma_f32_16x16x32_f16 v[144:147], v[14:17], v[188:191], v[148:151]
	v_mfma_f32_16x16x32_f16 v[148:151], v[14:17], v[192:195], v[152:155]
	v_mfma_f32_16x16x32_f16 v[152:155], v[14:17], v[196:199], v[160:163]
	v_mfma_f32_16x16x32_f16 v[160:163], v[14:17], v[200:203], v[164:167]
	v_mfma_f32_16x16x32_f16 v[2:5], v[14:17], v[204:207], v[2:5]
	v_mfma_f32_16x16x32_f16 v[14:17], v[18:21], v[176:179], v[62:65]
	v_mfma_f32_16x16x32_f16 v[62:65], v[18:21], v[180:183], v[66:69]
	v_mfma_f32_16x16x32_f16 v[66:69], v[18:21], v[184:187], v[70:73]
	v_mfma_f32_16x16x32_f16 v[70:73], v[18:21], v[188:191], v[74:77]
	v_mfma_f32_16x16x32_f16 v[74:77], v[18:21], v[192:195], v[78:81]
	v_mfma_f32_16x16x32_f16 v[78:81], v[18:21], v[196:199], v[84:87]
	v_mfma_f32_16x16x32_f16 v[84:87], v[18:21], v[200:203], v[88:91]
	v_mfma_f32_16x16x32_f16 v[6:9], v[18:21], v[204:207], v[6:9]
	s_movk_i32 s9, 0x5000
	v_add_co_u32_e32 v116, vcc, s9, v118
	global_load_dwordx4 v[88:91], v[156:157], off offset:2048
	global_load_dwordx4 v[164:167], v[156:157], off offset:3072
	v_addc_co_u32_e32 v117, vcc, 0, v119, vcc
	global_load_dwordx4 v[176:179], v[116:117], off
	v_bitop3_b32 v18, v158, v1, 8 bitop3:0x36
	v_lshl_or_b32 v134, v18, 4, v132
	ds_read_b128 v[18:21], v134
	ds_read_b128 v[180:183], v134 offset:8192
	ds_read_b128 v[184:187], v134 offset:16384
	ds_read_b128 v[188:191], v134 offset:24576
	ds_read_b128 v[192:195], v134 offset:32768
	ds_read_b128 v[196:199], v134 offset:40960
	ds_read_b128 v[200:203], v134 offset:49152
	ds_read_b128 v[204:207], v134 offset:57344
	s_waitcnt lgkmcnt(7)
	v_mfma_f32_16x16x32_f16 v[96:99], v[22:25], v[18:21], v[96:99]
	s_waitcnt lgkmcnt(6)
	v_mfma_f32_16x16x32_f16 v[100:103], v[22:25], v[180:183], v[100:103]
	s_waitcnt lgkmcnt(5)
	v_mfma_f32_16x16x32_f16 v[104:107], v[22:25], v[184:187], v[104:107]
	s_waitcnt lgkmcnt(4)
	v_mfma_f32_16x16x32_f16 v[108:111], v[22:25], v[188:191], v[108:111]
	s_waitcnt lgkmcnt(3)
	v_mfma_f32_16x16x32_f16 v[112:115], v[22:25], v[192:195], v[112:115]
	s_waitcnt lgkmcnt(2)
	v_mfma_f32_16x16x32_f16 v[120:123], v[22:25], v[196:199], v[120:123]
	s_waitcnt lgkmcnt(1)
	v_mfma_f32_16x16x32_f16 v[124:127], v[22:25], v[200:203], v[124:127]
	s_waitcnt lgkmcnt(0)
	v_mfma_f32_16x16x32_f16 v[10:13], v[22:25], v[204:207], v[10:13]
	s_waitcnt vmcnt(13)
	v_mfma_f32_16x16x32_f16 v[22:25], v[30:33], v[18:21], v[26:29]
	v_mfma_f32_16x16x32_f16 v[26:29], v[30:33], v[180:183], v[128:131]
	v_mfma_f32_16x16x32_f16 v[128:131], v[30:33], v[184:187], v[136:139]
	v_mfma_f32_16x16x32_f16 v[144:147], v[30:33], v[188:191], v[144:147]
	v_mfma_f32_16x16x32_f16 v[148:151], v[30:33], v[192:195], v[148:151]
	v_mfma_f32_16x16x32_f16 v[152:155], v[30:33], v[196:199], v[152:155]
	v_mfma_f32_16x16x32_f16 v[160:163], v[30:33], v[200:203], v[160:163]
	v_mfma_f32_16x16x32_f16 v[2:5], v[30:33], v[204:207], v[2:5]
	s_waitcnt vmcnt(12)
	v_mfma_f32_16x16x32_f16 v[14:17], v[34:37], v[18:21], v[14:17]
	v_mfma_f32_16x16x32_f16 v[18:21], v[34:37], v[180:183], v[62:65]
	v_mfma_f32_16x16x32_f16 v[30:33], v[34:37], v[184:187], v[66:69]
	v_mfma_f32_16x16x32_f16 v[62:65], v[34:37], v[188:191], v[70:73]
	v_mfma_f32_16x16x32_f16 v[66:69], v[34:37], v[192:195], v[74:77]
	v_mfma_f32_16x16x32_f16 v[70:73], v[34:37], v[196:199], v[78:81]
	v_mfma_f32_16x16x32_f16 v[74:77], v[34:37], v[200:203], v[84:87]
	v_mfma_f32_16x16x32_f16 v[6:9], v[34:37], v[204:207], v[6:9]
	s_nop 0
	global_load_dwordx4 v[78:81], v[116:117], off offset:1024
	global_load_dwordx4 v[180:183], v[116:117], off offset:2048
	global_load_dwordx4 v[184:187], v[116:117], off offset:3072
	v_bitop3_b32 v34, v158, v1, 12 bitop3:0x36
	v_lshl_or_b32 v136, v34, 4, v132
	ds_read_b128 v[34:37], v136
	ds_read_b128 v[84:87], v136 offset:8192
	ds_read_b128 v[188:191], v136 offset:16384
	ds_read_b128 v[192:195], v136 offset:24576
	ds_read_b128 v[196:199], v136 offset:32768
	ds_read_b128 v[200:203], v136 offset:40960
	ds_read_b128 v[204:207], v136 offset:49152
	ds_read_b128 v[208:211], v136 offset:57344
	s_waitcnt vmcnt(14) lgkmcnt(7)
	v_mfma_f32_16x16x32_f16 v[96:99], v[38:41], v[34:37], v[96:99]
	s_waitcnt lgkmcnt(6)
	v_mfma_f32_16x16x32_f16 v[100:103], v[38:41], v[84:87], v[100:103]
	s_waitcnt lgkmcnt(5)
	v_mfma_f32_16x16x32_f16 v[104:107], v[38:41], v[188:191], v[104:107]
	s_waitcnt lgkmcnt(4)
	v_mfma_f32_16x16x32_f16 v[108:111], v[38:41], v[192:195], v[108:111]
	s_waitcnt lgkmcnt(3)
	v_mfma_f32_16x16x32_f16 v[112:115], v[38:41], v[196:199], v[112:115]
	s_waitcnt lgkmcnt(2)
	v_mfma_f32_16x16x32_f16 v[120:123], v[38:41], v[200:203], v[120:123]
	s_waitcnt lgkmcnt(1)
	v_mfma_f32_16x16x32_f16 v[124:127], v[38:41], v[204:207], v[124:127]
	s_waitcnt lgkmcnt(0)
	v_mfma_f32_16x16x32_f16 v[212:215], v[38:41], v[208:211], v[10:13]
	s_waitcnt vmcnt(13)
	v_mfma_f32_16x16x32_f16 v[22:25], v[42:45], v[34:37], v[22:25]
	v_mfma_f32_16x16x32_f16 v[216:219], v[42:45], v[84:87], v[26:29]
	v_mfma_f32_16x16x32_f16 v[128:131], v[42:45], v[188:191], v[128:131]
	v_mfma_f32_16x16x32_f16 v[144:147], v[42:45], v[192:195], v[144:147]
	v_mfma_f32_16x16x32_f16 v[148:151], v[42:45], v[196:199], v[148:151]
	v_mfma_f32_16x16x32_f16 v[152:155], v[42:45], v[200:203], v[152:155]
	v_mfma_f32_16x16x32_f16 v[160:163], v[42:45], v[204:207], v[160:163]
	v_mfma_f32_16x16x32_f16 v[2:5], v[42:45], v[208:211], v[2:5]
	s_waitcnt vmcnt(12)
	v_mfma_f32_16x16x32_f16 v[14:17], v[46:49], v[34:37], v[14:17]
	v_mfma_f32_16x16x32_f16 v[18:21], v[46:49], v[84:87], v[18:21]
	v_mfma_f32_16x16x32_f16 v[30:33], v[46:49], v[188:191], v[30:33]
	v_mfma_f32_16x16x32_f16 v[34:37], v[46:49], v[192:195], v[62:65]
	v_mfma_f32_16x16x32_f16 v[42:45], v[46:49], v[196:199], v[66:69]
	v_mfma_f32_16x16x32_f16 v[62:65], v[46:49], v[200:203], v[70:73]
	v_mfma_f32_16x16x32_f16 v[66:69], v[46:49], v[204:207], v[74:77]
	v_mfma_f32_16x16x32_f16 v[6:9], v[46:49], v[208:211], v[6:9]
	s_mov_b32 s9, 0x30000
	v_add_co_u32_e32 v116, vcc, s9, v118
	s_mov_b32 s9, 0x31000
	s_nop 0
	v_addc_co_u32_e32 v117, vcc, 0, v119, vcc
	v_add_co_u32_e32 v156, vcc, s9, v118
	v_bitop3_b32 v46, v158, v1, 16 bitop3:0x36
	s_nop 0
	v_addc_co_u32_e32 v157, vcc, 0, v119, vcc
	global_load_dwordx4 v[38:41], v[156:157], off offset:-4096
	global_load_dwordx4 v[26:29], v[116:117], off offset:1024
	global_load_dwordx4 v[10:13], v[116:117], off offset:2048
	v_lshl_or_b32 v137, v46, 4, v132
	ds_read_b128 v[46:49], v137
	ds_read_b128 v[70:73], v137 offset:8192
	ds_read_b128 v[74:77], v137 offset:16384
	ds_read_b128 v[84:87], v137 offset:24576
	ds_read_b128 v[188:191], v137 offset:32768
	ds_read_b128 v[192:195], v137 offset:40960
	ds_read_b128 v[196:199], v137 offset:49152
	ds_read_b128 v[200:203], v137 offset:57344
	s_waitcnt vmcnt(14) lgkmcnt(7)
	v_mfma_f32_16x16x32_f16 v[96:99], v[50:53], v[46:49], v[96:99]
	s_waitcnt lgkmcnt(6)
	v_mfma_f32_16x16x32_f16 v[100:103], v[50:53], v[70:73], v[100:103]
	s_waitcnt lgkmcnt(5)
	v_mfma_f32_16x16x32_f16 v[104:107], v[50:53], v[74:77], v[104:107]
	s_waitcnt lgkmcnt(4)
	v_mfma_f32_16x16x32_f16 v[108:111], v[50:53], v[84:87], v[108:111]
	s_waitcnt lgkmcnt(3)
	v_mfma_f32_16x16x32_f16 v[112:115], v[50:53], v[188:191], v[112:115]
	s_waitcnt lgkmcnt(2)
	v_mfma_f32_16x16x32_f16 v[120:123], v[50:53], v[192:195], v[120:123]
	s_waitcnt lgkmcnt(1)
	v_mfma_f32_16x16x32_f16 v[124:127], v[50:53], v[196:199], v[124:127]
	s_waitcnt lgkmcnt(0)
	v_mfma_f32_16x16x32_f16 v[50:53], v[50:53], v[200:203], v[212:215]
	s_waitcnt vmcnt(13)
	v_mfma_f32_16x16x32_f16 v[204:207], v[54:57], v[46:49], v[22:25]
	v_mfma_f32_16x16x32_f16 v[208:211], v[54:57], v[70:73], v[216:219]
	v_mfma_f32_16x16x32_f16 v[128:131], v[54:57], v[74:77], v[128:131]
	v_mfma_f32_16x16x32_f16 v[144:147], v[54:57], v[84:87], v[144:147]
	v_mfma_f32_16x16x32_f16 v[148:151], v[54:57], v[188:191], v[148:151]
	v_mfma_f32_16x16x32_f16 v[152:155], v[54:57], v[192:195], v[152:155]
	v_mfma_f32_16x16x32_f16 v[160:163], v[54:57], v[196:199], v[160:163]
	v_mfma_f32_16x16x32_f16 v[54:57], v[54:57], v[200:203], v[2:5]
	s_waitcnt vmcnt(12)
	v_mfma_f32_16x16x32_f16 v[14:17], v[58:61], v[46:49], v[14:17]
	v_mfma_f32_16x16x32_f16 v[18:21], v[58:61], v[70:73], v[18:21]
	v_mfma_f32_16x16x32_f16 v[30:33], v[58:61], v[74:77], v[30:33]
	v_mfma_f32_16x16x32_f16 v[34:37], v[58:61], v[84:87], v[34:37]
	v_mfma_f32_16x16x32_f16 v[42:45], v[58:61], v[188:191], v[42:45]
	v_mfma_f32_16x16x32_f16 v[46:49], v[58:61], v[192:195], v[62:65]
	v_mfma_f32_16x16x32_f16 v[62:65], v[58:61], v[196:199], v[66:69]
	v_mfma_f32_16x16x32_f16 v[58:61], v[58:61], v[200:203], v[6:9]
	global_load_dwordx4 v[22:25], v[116:117], off offset:3072
	s_nop 1
	global_load_dwordx4 v[6:9], v[156:157], off
	global_load_dwordx4 v[2:5], v[156:157], off offset:1024
	v_bitop3_b32 v66, v158, v1, 20 bitop3:0x36
	v_lshl_or_b32 v138, v66, 4, v132
	ds_read_b128 v[66:69], v138
	ds_read_b128 v[70:73], v138 offset:8192
	ds_read_b128 v[74:77], v138 offset:16384
	ds_read_b128 v[84:87], v138 offset:24576
	ds_read_b128 v[188:191], v138 offset:32768
	ds_read_b128 v[192:195], v138 offset:40960
	ds_read_b128 v[196:199], v138 offset:49152
	ds_read_b128 v[200:203], v138 offset:57344
	s_waitcnt vmcnt(14) lgkmcnt(7)
	v_mfma_f32_16x16x32_f16 v[96:99], v[92:95], v[66:69], v[96:99]
	s_waitcnt lgkmcnt(6)
	v_mfma_f32_16x16x32_f16 v[100:103], v[92:95], v[70:73], v[100:103]
	s_waitcnt lgkmcnt(5)
	v_mfma_f32_16x16x32_f16 v[104:107], v[92:95], v[74:77], v[104:107]
	s_waitcnt lgkmcnt(4)
	v_mfma_f32_16x16x32_f16 v[108:111], v[92:95], v[84:87], v[108:111]
	s_waitcnt lgkmcnt(3)
	v_mfma_f32_16x16x32_f16 v[112:115], v[92:95], v[188:191], v[112:115]
	s_waitcnt lgkmcnt(2)
	v_mfma_f32_16x16x32_f16 v[212:215], v[92:95], v[192:195], v[120:123]
	s_waitcnt lgkmcnt(1)
	v_mfma_f32_16x16x32_f16 v[124:127], v[92:95], v[196:199], v[124:127]
	s_waitcnt lgkmcnt(0)
	v_mfma_f32_16x16x32_f16 v[50:53], v[92:95], v[200:203], v[50:53]
	s_waitcnt vmcnt(13)
	v_mfma_f32_16x16x32_f16 v[92:95], v[168:171], v[66:69], v[204:207]
	v_mfma_f32_16x16x32_f16 v[204:207], v[168:171], v[70:73], v[208:211]
	v_mfma_f32_16x16x32_f16 v[128:131], v[168:171], v[74:77], v[128:131]
	v_mfma_f32_16x16x32_f16 v[144:147], v[168:171], v[84:87], v[144:147]
	v_mfma_f32_16x16x32_f16 v[148:151], v[168:171], v[188:191], v[148:151]
	v_mfma_f32_16x16x32_f16 v[152:155], v[168:171], v[192:195], v[152:155]
	v_mfma_f32_16x16x32_f16 v[160:163], v[168:171], v[196:199], v[160:163]
	v_mfma_f32_16x16x32_f16 v[54:57], v[168:171], v[200:203], v[54:57]
	s_waitcnt vmcnt(12)
	v_mfma_f32_16x16x32_f16 v[66:69], v[172:175], v[66:69], v[14:17]
	v_mfma_f32_16x16x32_f16 v[70:73], v[172:175], v[70:73], v[18:21]
	v_mfma_f32_16x16x32_f16 v[74:77], v[172:175], v[74:77], v[30:33]
	v_mfma_f32_16x16x32_f16 v[34:37], v[172:175], v[84:87], v[34:37]
	v_mfma_f32_16x16x32_f16 v[42:45], v[172:175], v[188:191], v[42:45]
	v_mfma_f32_16x16x32_f16 v[46:49], v[172:175], v[192:195], v[46:49]
	v_mfma_f32_16x16x32_f16 v[62:65], v[172:175], v[196:199], v[62:65]
	v_mfma_f32_16x16x32_f16 v[58:61], v[172:175], v[200:203], v[58:61]
	s_mov_b32 s9, 0x33000
	v_add_co_u32_e32 v122, vcc, s9, v118
	global_load_dwordx4 v[30:33], v[156:157], off offset:2048
	global_load_dwordx4 v[14:17], v[156:157], off offset:3072
	v_addc_co_u32_e32 v123, vcc, 0, v119, vcc
	global_load_dwordx4 v[18:21], v[122:123], off offset:-4096
	v_bitop3_b32 v84, v158, v1, 24 bitop3:0x36
	v_lshl_or_b32 v139, v84, 4, v132
	ds_read_b128 v[84:87], v139
	ds_read_b128 v[168:171], v139 offset:8192
	ds_read_b128 v[172:175], v139 offset:16384
	ds_read_b128 v[188:191], v139 offset:24576
	ds_read_b128 v[192:195], v139 offset:32768
	ds_read_b128 v[196:199], v139 offset:40960
	ds_read_b128 v[200:203], v139 offset:49152
	ds_read_b128 v[208:211], v139 offset:57344
	s_mov_b32 s9, 0x32000
	v_add_co_u32_e32 v116, vcc, s9, v118
	s_nop 1
	v_addc_co_u32_e32 v117, vcc, 0, v119, vcc
	s_waitcnt vmcnt(14) lgkmcnt(7)
	v_mfma_f32_16x16x32_f16 v[96:99], v[88:91], v[84:87], v[96:99]
	s_waitcnt lgkmcnt(6)
	v_mfma_f32_16x16x32_f16 v[100:103], v[88:91], v[168:171], v[100:103]
	s_waitcnt lgkmcnt(5)
	v_mfma_f32_16x16x32_f16 v[104:107], v[88:91], v[172:175], v[104:107]
	s_waitcnt lgkmcnt(4)
	v_mfma_f32_16x16x32_f16 v[108:111], v[88:91], v[188:191], v[108:111]
	s_waitcnt lgkmcnt(3)
	v_mfma_f32_16x16x32_f16 v[112:115], v[88:91], v[192:195], v[112:115]
	s_waitcnt lgkmcnt(2)
	v_mfma_f32_16x16x32_f16 v[212:215], v[88:91], v[196:199], v[212:215]
	s_waitcnt lgkmcnt(1)
	v_mfma_f32_16x16x32_f16 v[124:127], v[88:91], v[200:203], v[124:127]
	s_waitcnt lgkmcnt(0)
	v_mfma_f32_16x16x32_f16 v[50:53], v[88:91], v[208:211], v[50:53]
	s_waitcnt vmcnt(13)
	v_mfma_f32_16x16x32_f16 v[90:93], v[164:167], v[84:87], v[92:95]
	v_mfma_f32_16x16x32_f16 v[204:207], v[164:167], v[168:171], v[204:207]
	v_mfma_f32_16x16x32_f16 v[128:131], v[164:167], v[172:175], v[128:131]
	v_mfma_f32_16x16x32_f16 v[144:147], v[164:167], v[188:191], v[144:147]
	v_mfma_f32_16x16x32_f16 v[148:151], v[164:167], v[192:195], v[148:151]
	v_mfma_f32_16x16x32_f16 v[152:155], v[164:167], v[196:199], v[152:155]
	v_mfma_f32_16x16x32_f16 v[160:163], v[164:167], v[200:203], v[160:163]
	v_mfma_f32_16x16x32_f16 v[54:57], v[164:167], v[208:211], v[54:57]
	s_waitcnt vmcnt(12)
	v_mfma_f32_16x16x32_f16 v[164:167], v[176:179], v[84:87], v[66:69]
	v_mfma_f32_16x16x32_f16 v[168:171], v[176:179], v[168:171], v[70:73]
	v_mfma_f32_16x16x32_f16 v[172:175], v[176:179], v[172:175], v[74:77]
	v_mfma_f32_16x16x32_f16 v[188:191], v[176:179], v[188:191], v[34:37]
	v_mfma_f32_16x16x32_f16 v[192:195], v[176:179], v[192:195], v[42:45]
	v_mfma_f32_16x16x32_f16 v[196:199], v[176:179], v[196:199], v[46:49]
	v_mfma_f32_16x16x32_f16 v[200:203], v[176:179], v[200:203], v[62:65]
	v_mfma_f32_16x16x32_f16 v[176:179], v[176:179], v[208:211], v[58:61]
	s_nop 0
	global_load_dwordx4 v[46:49], v[116:117], off offset:1024
	global_load_dwordx4 v[42:45], v[116:117], off offset:2048
	global_load_dwordx4 v[34:37], v[116:117], off offset:3072
	v_bitop3_b32 v58, v158, v1, 28 bitop3:0x36
	v_lshl_or_b32 v141, v58, 4, v132
	ds_read_b128 v[58:61], v141
	ds_read_b128 v[62:65], v141 offset:8192
	ds_read_b128 v[156:159], v141 offset:16384
	ds_read_b128 v[208:211], v141 offset:24576
	ds_read_b128 v[216:219], v141 offset:32768
	ds_read_b128 v[220:223], v141 offset:40960
	ds_read_b128 v[224:227], v141 offset:49152
	ds_read_b128 v[228:231], v141 offset:57344
	s_waitcnt vmcnt(14) lgkmcnt(7)
	v_mfma_f32_16x16x32_f16 v[232:235], v[78:81], v[58:61], v[96:99]
	s_waitcnt lgkmcnt(6)
	v_mfma_f32_16x16x32_f16 v[236:239], v[78:81], v[62:65], v[100:103]
	s_waitcnt lgkmcnt(5)
	v_mfma_f32_16x16x32_f16 v[240:243], v[78:81], v[156:159], v[104:107]
	s_waitcnt lgkmcnt(4)
	v_mfma_f32_16x16x32_f16 v[244:247], v[78:81], v[208:211], v[108:111]
	s_waitcnt lgkmcnt(3)
	v_mfma_f32_16x16x32_f16 v[106:109], v[78:81], v[216:219], v[112:115]
	s_waitcnt lgkmcnt(2)
	v_mfma_f32_16x16x32_f16 v[102:105], v[78:81], v[220:223], v[212:215]
	s_waitcnt lgkmcnt(1)
	v_mfma_f32_16x16x32_f16 v[94:97], v[78:81], v[224:227], v[124:127]
	s_waitcnt lgkmcnt(0)
	v_mfma_f32_16x16x32_f16 v[86:89], v[78:81], v[228:231], v[50:53]
	s_waitcnt vmcnt(13)
	v_mfma_f32_16x16x32_f16 v[124:127], v[180:183], v[58:61], v[90:93]
	v_mfma_f32_16x16x32_f16 v[204:207], v[180:183], v[62:65], v[204:207]
	v_mfma_f32_16x16x32_f16 v[212:215], v[180:183], v[156:159], v[128:131]
	v_mfma_f32_16x16x32_f16 v[144:147], v[180:183], v[208:211], v[144:147]
	v_mfma_f32_16x16x32_f16 v[78:81], v[180:183], v[216:219], v[148:151]
	v_mfma_f32_16x16x32_f16 v[74:77], v[180:183], v[220:223], v[152:155]
	v_mfma_f32_16x16x32_f16 v[70:73], v[180:183], v[224:227], v[160:163]
	v_mfma_f32_16x16x32_f16 v[66:69], v[180:183], v[228:231], v[54:57]
	s_waitcnt vmcnt(12)
	v_mfma_f32_16x16x32_f16 v[148:151], v[184:187], v[58:61], v[164:167]
	v_mfma_f32_16x16x32_f16 v[152:155], v[184:187], v[62:65], v[168:171]
	v_mfma_f32_16x16x32_f16 v[114:117], v[184:187], v[156:159], v[172:175]
	v_mfma_f32_16x16x32_f16 v[110:113], v[184:187], v[208:211], v[188:191]
	v_mfma_f32_16x16x32_f16 v[62:65], v[184:187], v[216:219], v[192:195]
	v_mfma_f32_16x16x32_f16 v[58:61], v[184:187], v[220:223], v[196:199]
	v_mfma_f32_16x16x32_f16 v[54:57], v[184:187], v[224:227], v[200:203]
	v_mfma_f32_16x16x32_f16 v[50:53], v[184:187], v[228:231], v[176:179]
	v_lshl_add_u64 v[120:121], v[82:83], 2, s[4:5]
	global_load_dwordx4 v[98:101], v[120:121], off
	global_load_dwordx4 v[90:93], v[120:121], off offset:64
	global_load_dwordx4 v[82:85], v[120:121], off offset:128
	s_movk_i32 s4, 0x310
	v_mad_u32_u24 v130, v1, s4, v248
	v_mov_b32_e32 v156, v237
	v_mov_b32_e32 v157, v238
	v_mov_b32_e32 v158, v241
	v_mov_b32_e32 v159, v242
	v_mov_b32_e32 v160, v245
	v_mov_b32_e32 v161, v246
	v_mov_b32_e32 v162, v205
	v_mov_b32_e32 v163, v206
	v_mov_b32_e32 v167, v146
	v_mov_b32_e32 v164, v213
	v_mov_b32_e32 v165, v214
	v_mov_b32_e32 v166, v145
	s_barrier
	v_add_u32_e32 v132, 0x3000, v130
	v_add_u32_e32 v131, 0x6000, v130
	s_mov_b32 s5, 0xfffffd0
	v_mul_lo_u32 v174, v142, s5
	s_movk_i32 s4, 0x600
	s_movk_i32 s9, 0xc7
	s_waitcnt vmcnt(2)
	v_pk_add_f32 v[168:169], v[232:233], v[98:99]
	v_pk_add_f32 v[170:171], v[234:235], v[100:101]
	v_add_f32_e32 v1, v236, v98
	v_pk_mov_b32 v[128:129], v[98:99], v[100:101] op_sel:[1,0]
	v_add_f32_e32 v99, v239, v101
	s_waitcnt vmcnt(1)
	v_pk_add_f32 v[124:125], v[124:125], v[90:91]
	v_pk_add_f32 v[172:173], v[126:127], v[92:93]
	v_add_f32_e32 v178, v204, v90
	v_pk_mov_b32 v[126:127], v[90:91], v[92:93] op_sel:[1,0]
	v_add_f32_e32 v91, v207, v93
	v_add_f32_e32 v100, v240, v98
	v_add_f32_e32 v175, v243, v101
	v_add_f32_e32 v92, v212, v90
	v_add_f32_e32 v179, v215, v93
	v_add_f32_e32 v181, v147, v93
	v_cvt_pk_f16_f32 v147, v170, v171
	v_cvt_f16_f32_e32 v1, v1
	v_cvt_f16_f32_e32 v99, v99
	v_cvt_pk_f16_f32 v146, v168, v169
	v_cvt_f16_f32_e32 v100, v100
	v_cvt_f16_f32_e32 v168, v175
	v_cvt_pk_f16_f32 v124, v124, v125
	v_cvt_pk_f16_f32 v125, v172, v173
	v_add_f32_e32 v180, v144, v90
	s_waitcnt vmcnt(0)
	v_pk_add_f32 v[144:145], v[148:149], v[82:83]
	v_pk_add_f32 v[148:149], v[156:157], v[128:129]
	v_pk_add_f32 v[156:157], v[158:159], v[128:129]
	v_pk_add_f32 v[158:159], v[160:161], v[128:129]
	v_pk_add_f32 v[160:161], v[162:163], v[126:127]
	v_pk_add_f32 v[162:163], v[164:165], v[126:127]
	v_cvt_pk_f16_f32 v144, v144, v145
	v_cvt_pk_f16_f32 v145, v148, v149
	v_cvt_pk_f16_f32 v148, v156, v157
	v_cvt_pk_f16_f32 v149, v158, v159
	ds_write2_b64 v130, v[146:147], v[124:125] offset1:4
	v_pack_b32_f16 v124, v1, v145
	v_alignbit_b32 v125, v99, v145, 16
	v_cvt_pk_f16_f32 v156, v178, v160
	v_cvt_pk_f16_f32 v157, v161, v91
	v_pack_b32_f16 v146, v100, v148
	v_alignbit_b32 v147, v168, v148, 16
	v_cvt_pk_f16_f32 v158, v92, v162
	v_cvt_pk_f16_f32 v159, v163, v179
	ds_write2_b64 v132, v[124:125], v[156:157] offset0:32 offset1:36
	ds_write2_b64 v131, v[146:147], v[158:159] offset0:64 offset1:68
	v_pk_add_f32 v[124:125], v[150:151], v[84:85]
	v_add_f32_e32 v1, v152, v82
	v_cvt_pk_f16_f32 v145, v124, v125
	v_pk_mov_b32 v[124:125], v[82:83], v[84:85] op_sel:[1,0]
	v_add_f32_e32 v83, v155, v85
	ds_write_b64 v130, v[144:145] offset:64
	v_mov_b32_e32 v144, v153
	v_mov_b32_e32 v145, v154
	v_pk_add_f32 v[144:145], v[144:145], v[124:125]
	v_add_f32_e32 v176, v244, v98
	v_cvt_pk_f16_f32 v144, v1, v144
	v_cvt_pk_f16_f32 v145, v145, v83
	v_add_f32_e32 v1, v114, v82
	v_add_f32_e32 v83, v117, v85
	v_mov_b32_e32 v114, v115
	v_mov_b32_e32 v115, v116
	v_pk_add_f32 v[114:115], v[114:115], v[124:125]
	v_add_f32_e32 v177, v247, v101
	v_cvt_pk_f16_f32 v114, v1, v114
	v_cvt_pk_f16_f32 v115, v115, v83
	v_add_f32_e32 v1, v110, v82
	v_add_f32_e32 v83, v113, v85
	v_mov_b32_e32 v110, v111
	v_mov_b32_e32 v111, v112
	v_cvt_f16_f32_e32 v169, v176
	v_cvt_f16_f32_e32 v170, v177
	v_pk_add_f32 v[164:165], v[166:167], v[126:127]
	v_pk_add_f32 v[110:111], v[110:111], v[124:125]
	v_cvt_pk_f16_f32 v110, v1, v110
	v_cvt_pk_f16_f32 v111, v111, v83
	ds_write_b64 v130, v[110:111] offset:37696
	v_add_lshl_u32 v111, v174, v0, 4
	v_mul_u32_u24_e32 v83, 0x310, v142
	v_pack_b32_f16 v148, v169, v149
	v_alignbit_b32 v149, v170, v149, 16
	v_cvt_pk_f16_f32 v160, v180, v164
	v_cvt_pk_f16_f32 v161, v165, v181
	v_add_u32_e32 v91, 0x9000, v130
	v_add3_u32 v83, v111, v83, s8
	v_or_b32_e32 v84, 0x200, v0
	ds_write2_b64 v91, v[148:149], v[160:161] offset0:96 offset1:100
	ds_write_b64 v130, v[144:145] offset:12608
	ds_write_b64 v130, v[114:115] offset:25152
	s_waitcnt lgkmcnt(0)
	s_barrier
	ds_read_b128 v[114:117], v83
	v_mul_u32_u24_e32 v92, 0x556, v84
	v_lshrrev_b32_e32 v92, 16, v92
	v_or_b32_e32 v1, s7, v143
	v_mul_lo_u32 v99, v92, s5
	v_mul_lo_u32 v112, v1, s4
	v_add_lshl_u32 v113, v99, v84, 4
	v_mul_u32_u24_e32 v84, 0x310, v92
	v_add_u32_e32 v1, v112, v111
	v_add3_u32 v84, v113, v84, s8
	ds_read_b128 v[142:145], v84
	s_waitcnt lgkmcnt(1)
	buffer_store_dwordx4 v[114:117], v1, s[0:3], 0 offen sc1
	v_lshlrev_b32_e32 v1, 3, v92
	v_bitop3_b32 v154, v1, s9, v92 bitop3:0xc8
	v_or_b32_e32 v1, s7, v154
	v_mul_lo_u32 v114, v1, s4
	v_add_u32_e32 v1, v114, v113
	s_waitcnt lgkmcnt(0)
	buffer_store_dwordx4 v[142:145], v1, s[0:3], 0 offen sc1
	v_or_b32_e32 v1, 0x400, v0
	v_mul_u32_u24_e32 v92, 0x556, v1
	v_lshrrev_b32_e32 v92, 16, v92
	v_mul_lo_u32 v99, v92, s5
	v_lshlrev_b32_e32 v100, 3, v92
	s_movk_i32 s9, 0x1c7
	v_bitop3_b32 v155, v100, s9, v92 bitop3:0xc8
	v_add_lshl_u32 v115, v99, v1, 4
	v_mul_u32_u24_e32 v92, 0x310, v92
	v_or_b32_e32 v100, s7, v155
	v_add3_u32 v92, v115, v92, s8
	v_or_b32_e32 v99, 0x600, v0
	v_mul_lo_u32 v116, v100, s4
	ds_read_b128 v[142:145], v92
	v_mul_u32_u24_e32 v100, 0x556, v99
	v_lshrrev_b32_e32 v100, 16, v100
	v_mul_lo_u32 v110, v100, s5
	v_add_lshl_u32 v117, v110, v99, 4
	v_mul_u32_u24_e32 v99, 0x310, v100
	v_add_u32_e32 v1, v116, v115
	v_add3_u32 v99, v117, v99, s8
	ds_read_b128 v[146:149], v99
	s_waitcnt lgkmcnt(1)
	buffer_store_dwordx4 v[142:145], v1, s[0:3], 0 offen sc1
	v_lshlrev_b32_e32 v1, 3, v100
	v_bitop3_b32 v156, v1, s9, v100 bitop3:0xc8
	v_add_u32_e32 v1, s7, v156
	v_mul_lo_u32 v142, v1, s4
	v_add_u32_e32 v1, v142, v117
	s_waitcnt lgkmcnt(0)
	buffer_store_dwordx4 v[146:149], v1, s[0:3], 0 offen sc1
	v_or_b32_e32 v1, 0x800, v0
	v_mul_u32_u24_e32 v100, 0xaab, v1
	v_lshrrev_b32_e32 v100, 17, v100
	v_mul_lo_u32 v110, v100, s5
	v_lshlrev_b32_e32 v143, 3, v100
	v_bitop3_b32 v157, v143, s9, v100 bitop3:0xc8
	v_add_lshl_u32 v144, v110, v1, 4
	v_mul_u32_u24_e32 v100, 0x310, v100
	v_or_b32_e32 v0, 0xa00, v0
	v_add3_u32 v100, v100, v144, s8
	v_mul_u32_u24_e32 v110, 0xaab, v0
	ds_read_b128 v[146:149], v100
	v_lshrrev_b32_e32 v158, 17, v110
	v_mul_lo_u32 v110, v158, s5
	v_or_b32_e32 v143, s7, v157
	v_add_lshl_u32 v145, v110, v0, 4
	v_mul_u32_u24_e32 v0, 0x310, v158
	v_mul_lo_u32 v143, v143, s4
	v_add3_u32 v110, v0, v145, s8
	v_add_u32_e32 v1, v143, v144
	ds_read_b128 v[150:153], v110
	v_lshlrev_b32_e32 v0, 3, v158
	s_movk_i32 s5, 0x3c7
	s_waitcnt lgkmcnt(1)
	buffer_store_dwordx4 v[146:149], v1, s[0:3], 0 offen sc1
	v_mov_b32_e32 v1, v108
	v_add_f32_e32 v102, v102, v98
	v_bitop3_b32 v147, v0, s5, v158 bitop3:0xc8
	v_add_u32_e32 v0, s7, v147
	v_mul_lo_u32 v146, v0, s4
	v_add_u32_e32 v0, v146, v145
	s_waitcnt lgkmcnt(0)
	buffer_store_dwordx4 v[150:153], v0, s[0:3], 0 offen sc1
	v_add_f32_e32 v0, v106, v98
	v_cvt_f16_f32_e32 v106, v0
	v_mov_b32_e32 v0, v107
	v_pk_add_f32 v[0:1], v[0:1], v[128:129]
	v_add_f32_e32 v94, v94, v98
	v_cvt_pk_f16_f32 v1, v0, v1
	v_pack_b32_f16 v0, v106, v1
	v_cvt_f16_f32_e32 v106, v102
	v_mov_b32_e32 v102, v103
	v_mov_b32_e32 v103, v104
	v_add_f32_e32 v104, v105, v101
	v_cvt_f16_f32_e32 v104, v104
	v_pk_add_f32 v[102:103], v[102:103], v[128:129]
	v_add_f32_e32 v86, v86, v98
	v_cvt_pk_f16_f32 v103, v102, v103
	v_pack_b32_f16 v102, v106, v103
	v_alignbit_b32 v103, v104, v103, 16
	v_cvt_f16_f32_e32 v104, v94
	v_mov_b32_e32 v94, v95
	v_mov_b32_e32 v95, v96
	v_add_f32_e32 v96, v97, v101
	v_cvt_f16_f32_e32 v96, v96
	v_pk_add_f32 v[94:95], v[94:95], v[128:129]
	v_add_f32_e32 v78, v78, v90
	v_cvt_pk_f16_f32 v95, v94, v95
	v_pack_b32_f16 v94, v104, v95
	v_alignbit_b32 v95, v96, v95, 16
	v_cvt_f16_f32_e32 v96, v86
	v_mov_b32_e32 v86, v87
	v_mov_b32_e32 v87, v88
	v_add_f32_e32 v88, v89, v101
	v_cvt_f16_f32_e32 v88, v88
	v_pk_add_f32 v[86:87], v[86:87], v[128:129]
	v_add_f32_e32 v107, v109, v101
	v_cvt_pk_f16_f32 v87, v86, v87
	v_pack_b32_f16 v86, v96, v87
	v_alignbit_b32 v87, v88, v87, 16
	v_cvt_f16_f32_e32 v88, v78
	v_mov_b32_e32 v78, v79
	v_mov_b32_e32 v79, v80
	v_add_f32_e32 v80, v81, v93
	v_cvt_f16_f32_e32 v107, v107
	v_cvt_f16_f32_e32 v80, v80
	v_pk_add_f32 v[78:79], v[78:79], v[126:127]
	s_nop 0
	v_cvt_pk_f16_f32 v79, v78, v79
	v_alignbit_b32 v1, v107, v1, 16
	v_pack_b32_f16 v78, v88, v79
	v_alignbit_b32 v79, v80, v79, 16
	s_barrier
	ds_write2_b64 v130, v[0:1], v[78:79] offset1:4
	v_add_f32_e32 v0, v74, v90
	v_cvt_f16_f32_e32 v74, v0
	v_mov_b32_e32 v0, v75
	v_add_f32_e32 v75, v77, v93
	v_cvt_f16_f32_e32 v75, v75
	v_mov_b32_e32 v1, v76
	v_pk_add_f32 v[0:1], v[0:1], v[126:127]
	s_nop 0
	v_cvt_pk_f16_f32 v1, v0, v1
	v_pack_b32_f16 v0, v74, v1
	v_alignbit_b32 v1, v75, v1, 16
	ds_write2_b64 v132, v[102:103], v[0:1] offset0:32 offset1:36
	v_add_f32_e32 v0, v70, v90
	v_cvt_f16_f32_e32 v70, v0
	v_mov_b32_e32 v0, v71
	v_add_f32_e32 v71, v73, v93
	v_cvt_f16_f32_e32 v71, v71
	v_mov_b32_e32 v1, v72
	v_pk_add_f32 v[0:1], v[0:1], v[126:127]
	s_nop 0
	v_cvt_pk_f16_f32 v1, v0, v1
	v_pack_b32_f16 v0, v70, v1
	v_alignbit_b32 v1, v71, v1, 16
	ds_write2_b64 v131, v[94:95], v[0:1] offset0:64 offset1:68
	v_add_f32_e32 v0, v66, v90
	v_cvt_f16_f32_e32 v66, v0
	v_mov_b32_e32 v0, v67
	v_add_f32_e32 v67, v69, v93
	v_cvt_f16_f32_e32 v67, v67
	v_mov_b32_e32 v1, v68
	v_pk_add_f32 v[0:1], v[0:1], v[126:127]
	v_mul_lo_u32 v68, v140, s4
	v_cvt_pk_f16_f32 v1, v0, v1
	v_pack_b32_f16 v0, v66, v1
	v_alignbit_b32 v1, v67, v1, 16
	ds_write2_b64 v91, v[86:87], v[0:1] offset0:96 offset1:100
	v_add_f32_e32 v0, v62, v82
	v_cvt_f16_f32_e32 v62, v0
	v_mov_b32_e32 v0, v63
	v_add_f32_e32 v63, v65, v85
	v_cvt_f16_f32_e32 v63, v63
	v_mov_b32_e32 v1, v64
	v_pk_add_f32 v[0:1], v[0:1], v[124:125]
	s_nop 0
	v_cvt_pk_f16_f32 v1, v0, v1
	v_pack_b32_f16 v0, v62, v1
	v_alignbit_b32 v1, v63, v1, 16
	ds_write_b64 v130, v[0:1] offset:64
	v_add_f32_e32 v0, v58, v82
	v_cvt_f16_f32_e32 v58, v0
	v_mov_b32_e32 v0, v59
	v_add_f32_e32 v59, v61, v85
	v_cvt_f16_f32_e32 v59, v59
	v_mov_b32_e32 v1, v60
	v_pk_add_f32 v[0:1], v[0:1], v[124:125]
	s_nop 0
	v_cvt_pk_f16_f32 v1, v0, v1
	v_pack_b32_f16 v0, v58, v1
	v_alignbit_b32 v1, v59, v1, 16
	ds_write_b64 v130, v[0:1] offset:12608
	v_add_f32_e32 v0, v54, v82
	v_cvt_f16_f32_e32 v54, v0
	v_mov_b32_e32 v0, v55
	v_add_f32_e32 v55, v57, v85
	v_cvt_f16_f32_e32 v55, v55
	v_mov_b32_e32 v1, v56
	v_pk_add_f32 v[0:1], v[0:1], v[124:125]
	s_nop 0
	v_cvt_pk_f16_f32 v1, v0, v1
	v_pack_b32_f16 v0, v54, v1
	v_alignbit_b32 v1, v55, v1, 16
	ds_write_b64 v130, v[0:1] offset:25152
	v_add_f32_e32 v0, v50, v82
	v_cvt_f16_f32_e32 v50, v0
	v_mov_b32_e32 v0, v51
	v_add_f32_e32 v51, v53, v85
	v_cvt_f16_f32_e32 v51, v51
	v_mov_b32_e32 v1, v52
	v_pk_add_f32 v[0:1], v[0:1], v[124:125]
	s_nop 0
	v_cvt_pk_f16_f32 v1, v0, v1
	v_pack_b32_f16 v0, v50, v1
	v_alignbit_b32 v1, v51, v1, 16
	ds_write_b64 v130, v[0:1] offset:37696
	s_waitcnt lgkmcnt(0)
	s_barrier
	global_load_dwordx4 v[50:53], v[122:123], off
	global_load_dwordx4 v[54:57], v[122:123], off offset:1024
	global_load_dwordx4 v[58:61], v[122:123], off offset:2048
	ds_read_b128 v[62:65], v83
	ds_read_b128 v[70:73], v84
	v_add_u32_e32 v0, v68, v111
	ds_read_b128 v[74:77], v99
	s_waitcnt lgkmcnt(2)
	buffer_store_dwordx4 v[62:65], v0, s[0:3], 0 offen sc1
	v_or_b32_e32 v0, s6, v154
	v_mul_lo_u32 v69, v0, s4
	ds_read_b128 v[62:65], v92
	v_add_u32_e32 v0, v69, v113
	s_waitcnt lgkmcnt(2)
	buffer_store_dwordx4 v[70:73], v0, s[0:3], 0 offen sc1
	v_or_b32_e32 v0, s6, v155
	s_nop 0
	v_mul_lo_u32 v72, v0, s4
	v_add_u32_e32 v0, v72, v115
	s_waitcnt lgkmcnt(0)
	buffer_store_dwordx4 v[62:65], v0, s[0:3], 0 offen sc1
	v_add_u32_e32 v0, s6, v156
	v_mul_lo_u32 v70, v0, s4
	ds_read_b128 v[62:65], v100
	v_add_u32_e32 v0, v70, v117
	buffer_store_dwordx4 v[74:77], v0, s[0:3], 0 offen sc1
	v_or_b32_e32 v0, s6, v157
	v_mul_lo_u32 v71, v0, s4
	v_add_u32_e32 v0, v71, v144
	ds_read_b128 v[74:77], v110
	s_waitcnt lgkmcnt(1)
	buffer_store_dwordx4 v[62:65], v0, s[0:3], 0 offen sc1
	ds_read_b128 v[62:65], v135
	ds_read_b128 v[78:81], v135 offset:8192
	ds_read_b128 v[86:89], v135 offset:16384
	ds_read_b128 v[94:97], v135 offset:24576
	ds_read_b128 v[102:105], v135 offset:32768
	ds_read_b128 v[106:109], v135 offset:40960
	ds_read_b128 v[124:127], v135 offset:49152
	ds_read_b128 v[148:151], v135 offset:57344
	v_add_u32_e32 v0, s6, v147
	v_mul_lo_u32 v73, v0, s4
	v_add_u32_e32 v0, v73, v145
	s_waitcnt lgkmcnt(8)
	buffer_store_dwordx4 v[74:77], v0, s[0:3], 0 offen sc1
	s_waitcnt lgkmcnt(7)
	s_nop 0
	v_mfma_f32_16x16x32_f16 v[74:77], v[38:41], v[62:65], 0
	s_waitcnt lgkmcnt(6)
	v_mfma_f32_16x16x32_f16 v[152:155], v[38:41], v[78:81], 0
	s_waitcnt lgkmcnt(5)
	v_mfma_f32_16x16x32_f16 v[156:159], v[38:41], v[86:89], 0
	s_waitcnt lgkmcnt(4)
	v_mfma_f32_16x16x32_f16 v[160:163], v[38:41], v[94:97], 0
	s_waitcnt lgkmcnt(3)
	v_mfma_f32_16x16x32_f16 v[164:167], v[38:41], v[102:105], 0
	s_waitcnt lgkmcnt(2)
	v_mfma_f32_16x16x32_f16 v[168:171], v[38:41], v[106:109], 0
	s_waitcnt lgkmcnt(1)
	v_mfma_f32_16x16x32_f16 v[172:175], v[38:41], v[124:127], 0
	s_waitcnt lgkmcnt(0)
	v_mfma_f32_16x16x32_f16 v[38:41], v[38:41], v[148:151], 0
	v_mfma_f32_16x16x32_f16 v[176:179], v[26:29], v[62:65], 0
	v_mfma_f32_16x16x32_f16 v[180:183], v[26:29], v[78:81], 0
	v_mfma_f32_16x16x32_f16 v[184:187], v[26:29], v[86:89], 0
	v_mfma_f32_16x16x32_f16 v[188:191], v[26:29], v[94:97], 0
	v_mfma_f32_16x16x32_f16 v[192:195], v[26:29], v[102:105], 0
	v_mfma_f32_16x16x32_f16 v[196:199], v[26:29], v[106:109], 0
	v_mfma_f32_16x16x32_f16 v[200:203], v[26:29], v[124:127], 0
	v_mfma_f32_16x16x32_f16 v[26:29], v[26:29], v[148:151], 0
	v_mfma_f32_16x16x32_f16 v[62:65], v[10:13], v[62:65], 0
	v_mfma_f32_16x16x32_f16 v[78:81], v[10:13], v[78:81], 0
	v_mfma_f32_16x16x32_f16 v[86:89], v[10:13], v[86:89], 0
	v_mfma_f32_16x16x32_f16 v[94:97], v[10:13], v[94:97], 0
	v_mfma_f32_16x16x32_f16 v[102:105], v[10:13], v[102:105], 0
	v_mfma_f32_16x16x32_f16 v[106:109], v[10:13], v[106:109], 0
	v_mfma_f32_16x16x32_f16 v[124:127], v[10:13], v[124:127], 0
	v_mfma_f32_16x16x32_f16 v[10:13], v[10:13], v[148:151], 0
	s_mov_b32 s4, 0x34000
	v_add_co_u32_e32 v66, vcc, s4, v118
	s_mov_b32 s4, 0x35000
	s_nop 0
	v_addc_co_u32_e32 v67, vcc, 0, v119, vcc
	v_add_co_u32_e32 v118, vcc, s4, v118
	s_nop 1
	v_addc_co_u32_e32 v119, vcc, 0, v119, vcc
	global_load_dwordx4 v[148:151], v[118:119], off offset:-4096
	global_load_dwordx4 v[204:207], v[122:123], off offset:3072
	global_load_dwordx4 v[208:211], v[66:67], off offset:1024
	ds_read_b128 v[212:215], v133
	ds_read_b128 v[216:219], v133 offset:8192
	ds_read_b128 v[220:223], v133 offset:16384
	ds_read_b128 v[224:227], v133 offset:24576
	ds_read_b128 v[228:231], v133 offset:32768
	ds_read_b128 v[232:235], v133 offset:40960
	ds_read_b128 v[236:239], v133 offset:49152
	ds_read_b128 v[240:243], v133 offset:57344
	s_waitcnt lgkmcnt(7)
	v_mfma_f32_16x16x32_f16 v[74:77], v[22:25], v[212:215], v[74:77]
	s_waitcnt lgkmcnt(6)
	v_mfma_f32_16x16x32_f16 v[152:155], v[22:25], v[216:219], v[152:155]
	s_waitcnt lgkmcnt(5)
	v_mfma_f32_16x16x32_f16 v[156:159], v[22:25], v[220:223], v[156:159]
	s_waitcnt lgkmcnt(4)
	v_mfma_f32_16x16x32_f16 v[160:163], v[22:25], v[224:227], v[160:163]
	s_waitcnt lgkmcnt(3)
	v_mfma_f32_16x16x32_f16 v[164:167], v[22:25], v[228:231], v[164:167]
	s_waitcnt lgkmcnt(2)
	v_mfma_f32_16x16x32_f16 v[168:171], v[22:25], v[232:235], v[168:171]
	s_waitcnt lgkmcnt(1)
	v_mfma_f32_16x16x32_f16 v[172:175], v[22:25], v[236:239], v[172:175]
	s_waitcnt lgkmcnt(0)
	v_mfma_f32_16x16x32_f16 v[22:25], v[22:25], v[240:243], v[38:41]
	v_mfma_f32_16x16x32_f16 v[38:41], v[6:9], v[212:215], v[176:179]
	v_mfma_f32_16x16x32_f16 v[176:179], v[6:9], v[216:219], v[180:183]
	v_mfma_f32_16x16x32_f16 v[180:183], v[6:9], v[220:223], v[184:187]
	v_mfma_f32_16x16x32_f16 v[184:187], v[6:9], v[224:227], v[188:191]
	v_mfma_f32_16x16x32_f16 v[188:191], v[6:9], v[228:231], v[192:195]
	v_mfma_f32_16x16x32_f16 v[192:195], v[6:9], v[232:235], v[196:199]
	v_mfma_f32_16x16x32_f16 v[196:199], v[6:9], v[236:239], v[200:203]
	v_mfma_f32_16x16x32_f16 v[6:9], v[6:9], v[240:243], v[26:29]
	v_mfma_f32_16x16x32_f16 v[26:29], v[2:5], v[212:215], v[62:65]
	v_mfma_f32_16x16x32_f16 v[62:65], v[2:5], v[216:219], v[78:81]
	v_mfma_f32_16x16x32_f16 v[78:81], v[2:5], v[220:223], v[86:89]
	v_mfma_f32_16x16x32_f16 v[86:89], v[2:5], v[224:227], v[94:97]
	v_mfma_f32_16x16x32_f16 v[94:97], v[2:5], v[228:231], v[102:105]
	v_mfma_f32_16x16x32_f16 v[102:105], v[2:5], v[232:235], v[106:109]
	v_mfma_f32_16x16x32_f16 v[106:109], v[2:5], v[236:239], v[124:127]
	v_mfma_f32_16x16x32_f16 v[0:3], v[2:5], v[240:243], v[10:13]
	s_nop 2
	global_load_dwordx4 v[10:13], v[66:67], off offset:2048
	global_load_dwordx4 v[122:125], v[66:67], off offset:3072
	global_load_dwordx4 v[126:129], v[118:119], off
	ds_read_b128 v[200:203], v134
	ds_read_b128 v[212:215], v134 offset:8192
	ds_read_b128 v[216:219], v134 offset:16384
	ds_read_b128 v[220:223], v134 offset:24576
	ds_read_b128 v[224:227], v134 offset:32768
	ds_read_b128 v[228:231], v134 offset:40960
	ds_read_b128 v[232:235], v134 offset:49152
	ds_read_b128 v[236:239], v134 offset:57344
	s_waitcnt lgkmcnt(7)
	v_mfma_f32_16x16x32_f16 v[74:77], v[30:33], v[200:203], v[74:77]
	s_waitcnt lgkmcnt(6)
	v_mfma_f32_16x16x32_f16 v[152:155], v[30:33], v[212:215], v[152:155]
	s_waitcnt lgkmcnt(5)
	v_mfma_f32_16x16x32_f16 v[156:159], v[30:33], v[216:219], v[156:159]
	s_waitcnt lgkmcnt(4)
	v_mfma_f32_16x16x32_f16 v[160:163], v[30:33], v[220:223], v[160:163]
	s_waitcnt lgkmcnt(3)
	v_mfma_f32_16x16x32_f16 v[164:167], v[30:33], v[224:227], v[164:167]
	s_waitcnt lgkmcnt(2)
	v_mfma_f32_16x16x32_f16 v[168:171], v[30:33], v[228:231], v[168:171]
	s_waitcnt lgkmcnt(1)
	v_mfma_f32_16x16x32_f16 v[172:175], v[30:33], v[232:235], v[172:175]
	s_waitcnt lgkmcnt(0)
	v_mfma_f32_16x16x32_f16 v[22:25], v[30:33], v[236:239], v[22:25]
	v_mfma_f32_16x16x32_f16 v[30:33], v[14:17], v[200:203], v[38:41]
	v_mfma_f32_16x16x32_f16 v[38:41], v[14:17], v[212:215], v[176:179]
	v_mfma_f32_16x16x32_f16 v[176:179], v[14:17], v[216:219], v[180:183]
	v_mfma_f32_16x16x32_f16 v[180:183], v[14:17], v[220:223], v[184:187]
	v_mfma_f32_16x16x32_f16 v[184:187], v[14:17], v[224:227], v[188:191]
	v_mfma_f32_16x16x32_f16 v[188:191], v[14:17], v[228:231], v[192:195]
	v_mfma_f32_16x16x32_f16 v[192:195], v[14:17], v[232:235], v[196:199]
	v_mfma_f32_16x16x32_f16 v[4:7], v[14:17], v[236:239], v[6:9]
	v_mfma_f32_16x16x32_f16 v[14:17], v[18:21], v[200:203], v[26:29]
	v_mfma_f32_16x16x32_f16 v[26:29], v[18:21], v[212:215], v[62:65]
	v_mfma_f32_16x16x32_f16 v[62:65], v[18:21], v[216:219], v[78:81]
	v_mfma_f32_16x16x32_f16 v[78:81], v[18:21], v[220:223], v[86:89]
	v_mfma_f32_16x16x32_f16 v[86:89], v[18:21], v[224:227], v[94:97]
	v_mfma_f32_16x16x32_f16 v[94:97], v[18:21], v[228:231], v[102:105]
	v_mfma_f32_16x16x32_f16 v[102:105], v[18:21], v[232:235], v[106:109]
	v_mfma_f32_16x16x32_f16 v[0:3], v[18:21], v[236:239], v[0:3]
	global_load_dwordx4 v[18:21], v[118:119], off offset:1024
	s_nop 0
	global_load_dwordx4 v[106:109], v[118:119], off offset:2048
	global_load_dwordx4 v[196:199], v[118:119], off offset:3072
	ds_read_b128 v[200:203], v136
	ds_read_b128 v[212:215], v136 offset:8192
	ds_read_b128 v[216:219], v136 offset:16384
	ds_read_b128 v[220:223], v136 offset:24576
	ds_read_b128 v[224:227], v136 offset:32768
	ds_read_b128 v[228:231], v136 offset:40960
	ds_read_b128 v[232:235], v136 offset:49152
	ds_read_b128 v[236:239], v136 offset:57344
	s_waitcnt lgkmcnt(7)
	v_mfma_f32_16x16x32_f16 v[74:77], v[46:49], v[200:203], v[74:77]
	s_waitcnt lgkmcnt(6)
	v_mfma_f32_16x16x32_f16 v[152:155], v[46:49], v[212:215], v[152:155]
	s_waitcnt lgkmcnt(5)
	v_mfma_f32_16x16x32_f16 v[156:159], v[46:49], v[216:219], v[156:159]
	s_waitcnt lgkmcnt(4)
	v_mfma_f32_16x16x32_f16 v[160:163], v[46:49], v[220:223], v[160:163]
	s_waitcnt lgkmcnt(3)
	v_mfma_f32_16x16x32_f16 v[164:167], v[46:49], v[224:227], v[164:167]
	s_waitcnt lgkmcnt(2)
	v_mfma_f32_16x16x32_f16 v[168:171], v[46:49], v[228:231], v[168:171]
	s_waitcnt lgkmcnt(1)
	v_mfma_f32_16x16x32_f16 v[172:175], v[46:49], v[232:235], v[172:175]
	s_waitcnt lgkmcnt(0)
	v_mfma_f32_16x16x32_f16 v[22:25], v[46:49], v[236:239], v[22:25]
	v_mfma_f32_16x16x32_f16 v[30:33], v[42:45], v[200:203], v[30:33]
	v_mfma_f32_16x16x32_f16 v[38:41], v[42:45], v[212:215], v[38:41]
	v_mfma_f32_16x16x32_f16 v[46:49], v[42:45], v[216:219], v[176:179]
	v_mfma_f32_16x16x32_f16 v[176:179], v[42:45], v[220:223], v[180:183]
	v_mfma_f32_16x16x32_f16 v[180:183], v[42:45], v[224:227], v[184:187]
	v_mfma_f32_16x16x32_f16 v[184:187], v[42:45], v[228:231], v[188:191]
	v_mfma_f32_16x16x32_f16 v[188:191], v[42:45], v[232:235], v[192:195]
	v_mfma_f32_16x16x32_f16 v[4:7], v[42:45], v[236:239], v[4:7]
	v_mfma_f32_16x16x32_f16 v[14:17], v[34:37], v[200:203], v[14:17]
	v_mfma_f32_16x16x32_f16 v[26:29], v[34:37], v[212:215], v[26:29]
	v_mfma_f32_16x16x32_f16 v[42:45], v[34:37], v[216:219], v[62:65]
	v_mfma_f32_16x16x32_f16 v[62:65], v[34:37], v[220:223], v[78:81]
	v_mfma_f32_16x16x32_f16 v[78:81], v[34:37], v[224:227], v[86:89]
	v_mfma_f32_16x16x32_f16 v[86:89], v[34:37], v[228:231], v[94:97]
	v_mfma_f32_16x16x32_f16 v[94:97], v[34:37], v[232:235], v[102:105]
	v_mfma_f32_16x16x32_f16 v[0:3], v[34:37], v[236:239], v[0:3]
	ds_read_b128 v[34:37], v137
	s_nop 0
	ds_read_b128 v[102:105], v137 offset:8192
	ds_read_b128 v[192:195], v137 offset:16384
	ds_read_b128 v[200:203], v137 offset:24576
	ds_read_b128 v[212:215], v137 offset:32768
	ds_read_b128 v[216:219], v137 offset:40960
	ds_read_b128 v[220:223], v137 offset:49152
	ds_read_b128 v[134:137], v137 offset:57344
	s_waitcnt vmcnt(17) lgkmcnt(7)
	v_mfma_f32_16x16x32_f16 v[74:77], v[50:53], v[34:37], v[74:77]
	s_waitcnt lgkmcnt(6)
	v_mfma_f32_16x16x32_f16 v[152:155], v[50:53], v[102:105], v[152:155]
	s_waitcnt lgkmcnt(5)
	v_mfma_f32_16x16x32_f16 v[156:159], v[50:53], v[192:195], v[156:159]
	s_waitcnt lgkmcnt(4)
	v_mfma_f32_16x16x32_f16 v[160:163], v[50:53], v[200:203], v[160:163]
	s_waitcnt lgkmcnt(3)
	v_mfma_f32_16x16x32_f16 v[164:167], v[50:53], v[212:215], v[164:167]
	s_waitcnt lgkmcnt(2)
	v_mfma_f32_16x16x32_f16 v[168:171], v[50:53], v[216:219], v[168:171]
	s_waitcnt lgkmcnt(1)
	v_mfma_f32_16x16x32_f16 v[172:175], v[50:53], v[220:223], v[172:175]
	s_waitcnt lgkmcnt(0)
	v_mfma_f32_16x16x32_f16 v[22:25], v[50:53], v[134:137], v[22:25]
	s_waitcnt vmcnt(16)
	v_mfma_f32_16x16x32_f16 v[30:33], v[54:57], v[34:37], v[30:33]
	v_mfma_f32_16x16x32_f16 v[38:41], v[54:57], v[102:105], v[38:41]
	v_mfma_f32_16x16x32_f16 v[46:49], v[54:57], v[192:195], v[46:49]
	v_mfma_f32_16x16x32_f16 v[50:53], v[54:57], v[200:203], v[176:179]
	v_mfma_f32_16x16x32_f16 v[176:179], v[54:57], v[212:215], v[180:183]
	v_mfma_f32_16x16x32_f16 v[180:183], v[54:57], v[216:219], v[184:187]
	v_mfma_f32_16x16x32_f16 v[184:187], v[54:57], v[220:223], v[188:191]
	v_mfma_f32_16x16x32_f16 v[4:7], v[54:57], v[134:137], v[4:7]
	s_waitcnt vmcnt(15)
	v_mfma_f32_16x16x32_f16 v[14:17], v[58:61], v[34:37], v[14:17]
	v_mfma_f32_16x16x32_f16 v[26:29], v[58:61], v[102:105], v[26:29]
	v_mfma_f32_16x16x32_f16 v[34:37], v[58:61], v[192:195], v[42:45]
	v_mfma_f32_16x16x32_f16 v[42:45], v[58:61], v[200:203], v[62:65]
	v_mfma_f32_16x16x32_f16 v[54:57], v[58:61], v[212:215], v[78:81]
	v_mfma_f32_16x16x32_f16 v[62:65], v[58:61], v[216:219], v[86:89]
	v_mfma_f32_16x16x32_f16 v[78:81], v[58:61], v[220:223], v[94:97]
	v_mfma_f32_16x16x32_f16 v[0:3], v[58:61], v[134:137], v[0:3]
	ds_read_b128 v[58:61], v138
	ds_read_b128 v[86:89], v138 offset:8192
	ds_read_b128 v[94:97], v138 offset:16384
	ds_read_b128 v[102:105], v138 offset:24576
	ds_read_b128 v[134:137], v138 offset:32768
	ds_read_b128 v[188:191], v138 offset:40960
	ds_read_b128 v[192:195], v138 offset:49152
	ds_read_b128 v[200:203], v138 offset:57344
	s_waitcnt vmcnt(7) lgkmcnt(7)
	v_mfma_f32_16x16x32_f16 v[74:77], v[204:207], v[58:61], v[74:77]
	s_waitcnt lgkmcnt(6)
	v_mfma_f32_16x16x32_f16 v[152:155], v[204:207], v[86:89], v[152:155]
	s_waitcnt lgkmcnt(5)
	v_mfma_f32_16x16x32_f16 v[156:159], v[204:207], v[94:97], v[156:159]
	s_waitcnt lgkmcnt(4)
	v_mfma_f32_16x16x32_f16 v[160:163], v[204:207], v[102:105], v[160:163]
	s_waitcnt lgkmcnt(3)
	v_mfma_f32_16x16x32_f16 v[164:167], v[204:207], v[134:137], v[164:167]
	s_waitcnt lgkmcnt(2)
	v_mfma_f32_16x16x32_f16 v[168:171], v[204:207], v[188:191], v[168:171]
	s_waitcnt lgkmcnt(1)
	v_mfma_f32_16x16x32_f16 v[172:175], v[204:207], v[192:195], v[172:175]
	s_waitcnt lgkmcnt(0)
	v_mfma_f32_16x16x32_f16 v[22:25], v[204:207], v[200:203], v[22:25]
	v_mfma_f32_16x16x32_f16 v[30:33], v[148:151], v[58:61], v[30:33]
	v_mfma_f32_16x16x32_f16 v[38:41], v[148:151], v[86:89], v[38:41]
	v_mfma_f32_16x16x32_f16 v[46:49], v[148:151], v[94:97], v[46:49]
	v_mfma_f32_16x16x32_f16 v[50:53], v[148:151], v[102:105], v[50:53]
	v_mfma_f32_16x16x32_f16 v[176:179], v[148:151], v[134:137], v[176:179]
	v_mfma_f32_16x16x32_f16 v[180:183], v[148:151], v[188:191], v[180:183]
	v_mfma_f32_16x16x32_f16 v[184:187], v[148:151], v[192:195], v[184:187]
	v_mfma_f32_16x16x32_f16 v[4:7], v[148:151], v[200:203], v[4:7]
	s_waitcnt vmcnt(6)
	v_mfma_f32_16x16x32_f16 v[14:17], v[208:211], v[58:61], v[14:17]
	v_mfma_f32_16x16x32_f16 v[26:29], v[208:211], v[86:89], v[26:29]
	v_mfma_f32_16x16x32_f16 v[34:37], v[208:211], v[94:97], v[34:37]
	v_mfma_f32_16x16x32_f16 v[42:45], v[208:211], v[102:105], v[42:45]
	v_mfma_f32_16x16x32_f16 v[54:57], v[208:211], v[134:137], v[54:57]
	v_mfma_f32_16x16x32_f16 v[58:61], v[208:211], v[188:191], v[62:65]
	v_mfma_f32_16x16x32_f16 v[62:65], v[208:211], v[192:195], v[78:81]
	v_mfma_f32_16x16x32_f16 v[0:3], v[208:211], v[200:203], v[0:3]
	s_nop 1
	ds_read_b128 v[78:81], v139
	ds_read_b128 v[86:89], v139 offset:8192
	ds_read_b128 v[94:97], v139 offset:16384
	ds_read_b128 v[102:105], v139 offset:24576
	ds_read_b128 v[134:137], v139 offset:32768
	ds_read_b128 v[148:151], v139 offset:40960
	ds_read_b128 v[188:191], v139 offset:49152
	ds_read_b128 v[192:195], v139 offset:57344
	s_waitcnt vmcnt(5) lgkmcnt(7)
	v_mfma_f32_16x16x32_f16 v[74:77], v[10:13], v[78:81], v[74:77]
	s_waitcnt lgkmcnt(6)
	v_mfma_f32_16x16x32_f16 v[152:155], v[10:13], v[86:89], v[152:155]
	s_waitcnt lgkmcnt(5)
	v_mfma_f32_16x16x32_f16 v[156:159], v[10:13], v[94:97], v[156:159]
	s_waitcnt lgkmcnt(4)
	v_mfma_f32_16x16x32_f16 v[160:163], v[10:13], v[102:105], v[160:163]
	s_waitcnt lgkmcnt(3)
	v_mfma_f32_16x16x32_f16 v[164:167], v[10:13], v[134:137], v[164:167]
	s_waitcnt lgkmcnt(2)
	v_mfma_f32_16x16x32_f16 v[168:171], v[10:13], v[148:151], v[168:171]
	s_waitcnt lgkmcnt(1)
	v_mfma_f32_16x16x32_f16 v[172:175], v[10:13], v[188:191], v[172:175]
	s_waitcnt lgkmcnt(0)
	v_mfma_f32_16x16x32_f16 v[8:11], v[10:13], v[192:195], v[22:25]
	s_waitcnt vmcnt(4)
	v_mfma_f32_16x16x32_f16 v[22:25], v[122:125], v[78:81], v[30:33]
	v_mfma_f32_16x16x32_f16 v[30:33], v[122:125], v[86:89], v[38:41]
	v_mfma_f32_16x16x32_f16 v[200:203], v[122:125], v[94:97], v[46:49]
	v_mfma_f32_16x16x32_f16 v[48:51], v[122:125], v[102:105], v[50:53]
	v_mfma_f32_16x16x32_f16 v[176:179], v[122:125], v[134:137], v[176:179]
	v_mfma_f32_16x16x32_f16 v[180:183], v[122:125], v[148:151], v[180:183]
	v_mfma_f32_16x16x32_f16 v[184:187], v[122:125], v[188:191], v[184:187]
	v_mfma_f32_16x16x32_f16 v[4:7], v[122:125], v[192:195], v[4:7]
	s_waitcnt vmcnt(3)
	v_mfma_f32_16x16x32_f16 v[12:15], v[126:129], v[78:81], v[14:17]
	v_mfma_f32_16x16x32_f16 v[78:81], v[126:129], v[86:89], v[26:29]
	v_mfma_f32_16x16x32_f16 v[86:89], v[126:129], v[94:97], v[34:37]
	v_mfma_f32_16x16x32_f16 v[40:43], v[126:129], v[102:105], v[42:45]
	v_mfma_f32_16x16x32_f16 v[94:97], v[126:129], v[134:137], v[54:57]
	v_mfma_f32_16x16x32_f16 v[102:105], v[126:129], v[148:151], v[58:61]
	v_mfma_f32_16x16x32_f16 v[64:67], v[126:129], v[188:191], v[62:65]
	v_mfma_f32_16x16x32_f16 v[0:3], v[126:129], v[192:195], v[0:3]
	s_nop 1
	ds_read_b128 v[60:63], v141
	ds_read_b128 v[122:125], v141 offset:8192
	ds_read_b128 v[126:129], v141 offset:16384
	ds_read_b128 v[134:137], v141 offset:24576
	ds_read_b128 v[148:151], v141 offset:32768
	ds_read_b128 v[188:191], v141 offset:40960
	ds_read_b128 v[192:195], v141 offset:49152
	ds_read_b128 v[138:141], v141 offset:57344
	s_waitcnt vmcnt(2) lgkmcnt(7)
	v_mfma_f32_16x16x32_f16 v[74:77], v[18:21], v[60:63], v[74:77]
	s_waitcnt lgkmcnt(6)
	v_mfma_f32_16x16x32_f16 v[152:155], v[18:21], v[122:125], v[152:155]
	s_waitcnt lgkmcnt(5)
	v_mfma_f32_16x16x32_f16 v[156:159], v[18:21], v[126:129], v[156:159]
	s_waitcnt lgkmcnt(4)
	v_mfma_f32_16x16x32_f16 v[160:163], v[18:21], v[134:137], v[160:163]
	s_waitcnt lgkmcnt(3)
	v_mfma_f32_16x16x32_f16 v[56:59], v[18:21], v[148:151], v[164:167]
	s_waitcnt lgkmcnt(2)
	v_mfma_f32_16x16x32_f16 v[52:55], v[18:21], v[188:191], v[168:171]
	s_waitcnt lgkmcnt(1)
	v_mfma_f32_16x16x32_f16 v[44:47], v[18:21], v[192:195], v[172:175]
	s_waitcnt lgkmcnt(0)
	v_mfma_f32_16x16x32_f16 v[36:39], v[18:21], v[138:141], v[8:11]
	s_waitcnt vmcnt(1)
	v_mfma_f32_16x16x32_f16 v[164:167], v[106:109], v[60:63], v[22:25]
	v_mfma_f32_16x16x32_f16 v[168:171], v[106:109], v[122:125], v[30:33]
	v_mfma_f32_16x16x32_f16 v[172:175], v[106:109], v[126:129], v[200:203]
	v_mfma_f32_16x16x32_f16 v[200:203], v[106:109], v[134:137], v[48:51]
	v_mfma_f32_16x16x32_f16 v[32:35], v[106:109], v[148:151], v[176:179]
	v_mfma_f32_16x16x32_f16 v[24:27], v[106:109], v[188:191], v[180:183]
	v_mfma_f32_16x16x32_f16 v[20:23], v[106:109], v[192:195], v[184:187]
	v_mfma_f32_16x16x32_f16 v[16:19], v[106:109], v[138:141], v[4:7]
	s_waitcnt vmcnt(0)
	v_mfma_f32_16x16x32_f16 v[106:109], v[196:199], v[60:63], v[12:15]
	v_mfma_f32_16x16x32_f16 v[78:81], v[196:199], v[122:125], v[78:81]
	v_mfma_f32_16x16x32_f16 v[86:89], v[196:199], v[126:129], v[86:89]
	v_mfma_f32_16x16x32_f16 v[60:63], v[196:199], v[134:137], v[40:43]
	v_mfma_f32_16x16x32_f16 v[12:15], v[196:199], v[148:151], v[94:97]
	v_mfma_f32_16x16x32_f16 v[8:11], v[196:199], v[188:191], v[102:105]
	v_mfma_f32_16x16x32_f16 v[4:7], v[196:199], v[192:195], v[64:67]
	v_mfma_f32_16x16x32_f16 v[0:3], v[196:199], v[138:141], v[0:3]
	global_load_dwordx4 v[48:51], v[120:121], off offset:1536
	global_load_dwordx4 v[40:43], v[120:121], off offset:1600
	global_load_dwordx4 v[28:31], v[120:121], off offset:1664
	v_mov_b32_e32 v94, v157
	v_mov_b32_e32 v95, v158
	v_mov_b32_e32 v96, v161
	v_mov_b32_e32 v97, v162
	v_mov_b32_e32 v64, v153
	v_mov_b32_e32 v65, v154
	v_mov_b32_e32 v102, v169
	v_mov_b32_e32 v103, v170
	v_mov_b32_e32 v104, v173
	v_mov_b32_e32 v105, v174
	v_mov_b32_e32 v118, v201
	v_mov_b32_e32 v119, v202
	s_barrier
	s_waitcnt vmcnt(2)
	v_pk_add_f32 v[74:75], v[74:75], v[48:49]
	v_add_f32_e32 v82, v152, v48
	v_pk_mov_b32 v[120:121], v[48:49], v[50:51] op_sel:[1,0]
	v_add_f32_e32 v49, v155, v51
	s_waitcnt vmcnt(1)
	v_pk_add_f32 v[122:123], v[164:165], v[40:41]
	v_add_f32_e32 v98, v168, v40
	v_pk_mov_b32 v[66:67], v[40:41], v[42:43] op_sel:[1,0]
	v_add_f32_e32 v41, v171, v43
	v_pk_add_f32 v[76:77], v[76:77], v[50:51]
	v_add_f32_e32 v50, v156, v48
	v_add_f32_e32 v85, v159, v51
	v_add_f32_e32 v90, v160, v48
	v_add_f32_e32 v93, v163, v51
	v_pk_add_f32 v[124:125], v[166:167], v[42:43]
	v_add_f32_e32 v42, v172, v40
	v_add_f32_e32 v101, v175, v43
	v_add_f32_e32 v126, v200, v40
	v_add_f32_e32 v127, v203, v43
	v_cvt_f16_f32_e32 v98, v98
	v_cvt_f16_f32_e32 v41, v41
	v_cvt_pk_f16_f32 v74, v74, v75
	v_cvt_pk_f16_f32 v75, v76, v77
	v_cvt_f16_f32_e32 v50, v50
	v_pk_add_f32 v[76:77], v[94:95], v[120:121]
	v_cvt_f16_f32_e32 v85, v85
	v_cvt_f16_f32_e32 v90, v90
	v_pk_add_f32 v[94:95], v[96:97], v[120:121]
	v_cvt_f16_f32_e32 v93, v93
	v_cvt_pk_f16_f32 v96, v122, v123
	v_pk_add_f32 v[64:65], v[64:65], v[120:121]
	v_pk_add_f32 v[102:103], v[102:103], v[66:67]
	v_pk_add_f32 v[104:105], v[104:105], v[66:67]
	v_pk_add_f32 v[118:119], v[118:119], v[66:67]
	v_cvt_pk_f16_f32 v76, v76, v77
	v_cvt_pk_f16_f32 v77, v94, v95
	v_cvt_pk_f16_f32 v95, v102, v103
	s_waitcnt vmcnt(0)
	v_pk_add_f32 v[106:107], v[106:107], v[28:29]
	v_pk_add_f32 v[108:109], v[108:109], v[30:31]
	v_cvt_pk_f16_f32 v97, v124, v125
	v_cvt_pk_f16_f32 v64, v82, v64
	v_cvt_pk_f16_f32 v65, v65, v49
	v_pack_b32_f16 v94, v98, v95
	v_alignbit_b32 v95, v41, v95, 16
	v_add_f32_e32 v78, v78, v28
	v_cvt_pk_f16_f32 v106, v106, v107
	v_cvt_pk_f16_f32 v107, v108, v109
	ds_write2_b64 v130, v[74:75], v[96:97] offset1:4
	ds_write_b64 v130, v[106:107] offset:64
	v_pack_b32_f16 v74, v50, v76
	v_alignbit_b32 v75, v85, v76, 16
	v_pack_b32_f16 v76, v90, v77
	v_alignbit_b32 v77, v93, v77, 16
	v_cvt_pk_f16_f32 v96, v42, v104
	v_cvt_pk_f16_f32 v97, v105, v101
	v_cvt_pk_f16_f32 v102, v126, v118
	v_cvt_pk_f16_f32 v103, v119, v127
	ds_write2_b64 v132, v[64:65], v[94:95] offset0:32 offset1:36
	ds_write2_b64 v131, v[74:75], v[96:97] offset0:64 offset1:68
	ds_write2_b64 v91, v[76:77], v[102:103] offset0:96 offset1:100
	v_pk_mov_b32 v[64:65], v[28:29], v[30:31] op_sel:[1,0]
	v_add_f32_e32 v29, v81, v31
	v_mov_b32_e32 v74, v79
	v_mov_b32_e32 v75, v80
	v_pk_add_f32 v[74:75], v[74:75], v[64:65]
	v_add_f32_e32 v56, v56, v48
	v_cvt_pk_f16_f32 v74, v78, v74
	v_cvt_pk_f16_f32 v75, v75, v29
	v_add_f32_e32 v29, v86, v28
	v_add_f32_e32 v30, v89, v31
	ds_write_b64 v130, v[74:75] offset:12608
	v_mov_b32_e32 v74, v87
	v_mov_b32_e32 v75, v88
	v_pk_add_f32 v[74:75], v[74:75], v[64:65]
	v_add_f32_e32 v52, v52, v48
	v_cvt_pk_f16_f32 v74, v29, v74
	v_cvt_pk_f16_f32 v75, v75, v30
	v_add_f32_e32 v29, v60, v28
	v_add_f32_e32 v30, v63, v31
	v_mov_b32_e32 v60, v61
	v_mov_b32_e32 v61, v62
	v_pk_add_f32 v[60:61], v[60:61], v[64:65]
	ds_write_b64 v130, v[74:75] offset:25152
	v_cvt_pk_f16_f32 v60, v29, v60
	v_cvt_pk_f16_f32 v61, v61, v30
	ds_write_b64 v130, v[60:61] offset:37696
	s_waitcnt lgkmcnt(0)
	s_barrier
	ds_read_b128 v[60:63], v83
	ds_read_b128 v[74:77], v84
	v_add_u32_e32 v29, 0x300, v111
	v_add_u32_e32 v30, v29, v112
	v_add_f32_e32 v44, v44, v48
	s_waitcnt lgkmcnt(1)
	buffer_store_dwordx4 v[60:63], v30, s[0:3], 0 offen sc1
	v_add_u32_e32 v30, 0x300, v113
	ds_read_b128 v[60:63], v92
	v_add_u32_e32 v41, v30, v114
	s_waitcnt lgkmcnt(1)
	buffer_store_dwordx4 v[74:77], v41, s[0:3], 0 offen sc1
	ds_read_b128 v[74:77], v99
	v_add_u32_e32 v41, 0x300, v115
	v_add_u32_e32 v42, v41, v116
	s_waitcnt lgkmcnt(1)
	buffer_store_dwordx4 v[60:63], v42, s[0:3], 0 offen sc1
	v_add_u32_e32 v42, 0x300, v117
	ds_read_b128 v[60:63], v100
	v_add_u32_e32 v49, v42, v142
	s_waitcnt lgkmcnt(1)
	buffer_store_dwordx4 v[74:77], v49, s[0:3], 0 offen sc1
	ds_read_b128 v[74:77], v110
	v_add_u32_e32 v49, 0x300, v144
	v_add_u32_e32 v50, v49, v143
	s_waitcnt lgkmcnt(1)
	buffer_store_dwordx4 v[60:63], v50, s[0:3], 0 offen sc1
	v_add_u32_e32 v50, 0x300, v145
	v_add_f32_e32 v36, v36, v48
	v_add_u32_e32 v60, v50, v146
	s_waitcnt lgkmcnt(0)
	buffer_store_dwordx4 v[74:77], v60, s[0:3], 0 offen sc1
	v_cvt_f16_f32_e32 v60, v56
	v_mov_b32_e32 v56, v57
	v_mov_b32_e32 v57, v58
	v_add_f32_e32 v58, v59, v51
	v_cvt_f16_f32_e32 v58, v58
	v_pk_add_f32 v[56:57], v[56:57], v[120:121]
	v_add_f32_e32 v32, v32, v40
	v_cvt_pk_f16_f32 v57, v56, v57
	v_pack_b32_f16 v56, v60, v57
	v_alignbit_b32 v57, v58, v57, 16
	v_cvt_f16_f32_e32 v58, v52
	v_mov_b32_e32 v52, v53
	v_mov_b32_e32 v53, v54
	v_add_f32_e32 v54, v55, v51
	v_cvt_f16_f32_e32 v54, v54
	v_pk_add_f32 v[52:53], v[52:53], v[120:121]
	v_add_f32_e32 v24, v24, v40
	v_cvt_pk_f16_f32 v53, v52, v53
	v_pack_b32_f16 v52, v58, v53
	v_alignbit_b32 v53, v54, v53, 16
	v_cvt_f16_f32_e32 v54, v44
	v_mov_b32_e32 v44, v45
	v_mov_b32_e32 v45, v46
	v_add_f32_e32 v46, v47, v51
	v_cvt_f16_f32_e32 v46, v46
	v_pk_add_f32 v[44:45], v[44:45], v[120:121]
	s_nop 0
	v_cvt_pk_f16_f32 v45, v44, v45
	v_pack_b32_f16 v44, v54, v45
	v_alignbit_b32 v45, v46, v45, 16
	v_cvt_f16_f32_e32 v46, v36
	v_mov_b32_e32 v36, v37
	v_mov_b32_e32 v37, v38
	v_add_f32_e32 v38, v39, v51
	v_cvt_f16_f32_e32 v38, v38
	v_pk_add_f32 v[36:37], v[36:37], v[120:121]
	s_barrier
	v_cvt_pk_f16_f32 v37, v36, v37
	v_pack_b32_f16 v36, v46, v37
	v_alignbit_b32 v37, v38, v37, 16
	v_cvt_f16_f32_e32 v38, v32
	v_mov_b32_e32 v32, v33
	v_mov_b32_e32 v33, v34
	v_add_f32_e32 v34, v35, v43
	v_cvt_f16_f32_e32 v34, v34
	v_pk_add_f32 v[32:33], v[32:33], v[66:67]
	s_nop 0
	v_cvt_pk_f16_f32 v33, v32, v33
	v_pack_b32_f16 v32, v38, v33
	v_alignbit_b32 v33, v34, v33, 16
	ds_write2_b64 v130, v[56:57], v[32:33] offset1:4
	v_cvt_f16_f32_e32 v32, v24
	v_mov_b32_e32 v24, v25
	v_mov_b32_e32 v25, v26
	v_add_f32_e32 v26, v27, v43
	v_cvt_f16_f32_e32 v26, v26
	v_pk_add_f32 v[24:25], v[24:25], v[66:67]
	v_add_f32_e32 v20, v20, v40
	v_cvt_pk_f16_f32 v25, v24, v25
	v_pack_b32_f16 v24, v32, v25
	v_alignbit_b32 v25, v26, v25, 16
	ds_write2_b64 v132, v[52:53], v[24:25] offset0:32 offset1:36
	v_cvt_f16_f32_e32 v24, v20
	v_mov_b32_e32 v20, v21
	v_mov_b32_e32 v21, v22
	v_add_f32_e32 v22, v23, v43
	v_cvt_f16_f32_e32 v22, v22
	v_pk_add_f32 v[20:21], v[20:21], v[66:67]
	v_add_f32_e32 v16, v16, v40
	v_cvt_pk_f16_f32 v21, v20, v21
	v_pack_b32_f16 v20, v24, v21
	v_alignbit_b32 v21, v22, v21, 16
	ds_write2_b64 v131, v[44:45], v[20:21] offset0:64 offset1:68
	v_cvt_f16_f32_e32 v20, v16
	v_mov_b32_e32 v16, v17
	v_mov_b32_e32 v17, v18
	v_add_f32_e32 v18, v19, v43
	v_cvt_f16_f32_e32 v18, v18
	v_pk_add_f32 v[16:17], v[16:17], v[66:67]
	v_add_f32_e32 v12, v12, v28
	v_cvt_pk_f16_f32 v17, v16, v17
	v_pack_b32_f16 v16, v20, v17
	v_alignbit_b32 v17, v18, v17, 16
	ds_write2_b64 v91, v[36:37], v[16:17] offset0:96 offset1:100
	v_cvt_f16_f32_e32 v16, v12
	v_mov_b32_e32 v12, v13
	v_mov_b32_e32 v13, v14
	v_add_f32_e32 v14, v15, v31
	v_cvt_f16_f32_e32 v14, v14
	v_pk_add_f32 v[12:13], v[12:13], v[64:65]
	v_add_f32_e32 v8, v8, v28
	v_cvt_pk_f16_f32 v13, v12, v13
	v_pack_b32_f16 v12, v16, v13
	v_alignbit_b32 v13, v14, v13, 16
	ds_write_b64 v130, v[12:13] offset:64
	v_cvt_f16_f32_e32 v12, v8
	v_mov_b32_e32 v8, v9
	v_mov_b32_e32 v9, v10
	v_add_f32_e32 v10, v11, v31
	v_cvt_f16_f32_e32 v10, v10
	v_pk_add_f32 v[8:9], v[8:9], v[64:65]
	v_add_f32_e32 v4, v4, v28
	v_cvt_pk_f16_f32 v9, v8, v9
	v_pack_b32_f16 v8, v12, v9
	v_alignbit_b32 v9, v10, v9, 16
	ds_write_b64 v130, v[8:9] offset:12608
	v_cvt_f16_f32_e32 v8, v4
	v_mov_b32_e32 v4, v5
	v_mov_b32_e32 v5, v6
	v_add_f32_e32 v6, v7, v31
	v_cvt_f16_f32_e32 v6, v6
	v_pk_add_f32 v[4:5], v[4:5], v[64:65]
	v_add_f32_e32 v0, v0, v28
	v_cvt_pk_f16_f32 v5, v4, v5
	v_pack_b32_f16 v4, v8, v5
	v_alignbit_b32 v5, v6, v5, 16
	ds_write_b64 v130, v[4:5] offset:25152
	v_cvt_f16_f32_e32 v4, v0
	v_mov_b32_e32 v0, v1
	v_mov_b32_e32 v1, v2
	v_add_f32_e32 v2, v3, v31
	v_cvt_f16_f32_e32 v2, v2
	v_pk_add_f32 v[0:1], v[0:1], v[64:65]
	v_add_u32_e32 v8, v29, v68
	v_cvt_pk_f16_f32 v1, v0, v1
	v_pack_b32_f16 v0, v4, v1
	v_alignbit_b32 v1, v2, v1, 16
	ds_write_b64 v130, v[0:1] offset:37696
	s_waitcnt lgkmcnt(0)
	s_barrier
	ds_read_b128 v[0:3], v83
	ds_read_b128 v[4:7], v84
	v_add_u32_e32 v12, v42, v70
	s_waitcnt lgkmcnt(1)
	buffer_store_dwordx4 v[0:3], v8, s[0:3], 0 offen sc1
	ds_read_b128 v[0:3], v92
	v_add_u32_e32 v8, v30, v69
	s_waitcnt lgkmcnt(1)
	buffer_store_dwordx4 v[4:7], v8, s[0:3], 0 offen sc1
	v_add_u32_e32 v8, v41, v72
	ds_read_b128 v[4:7], v99
	s_waitcnt lgkmcnt(1)
	buffer_store_dwordx4 v[0:3], v8, s[0:3], 0 offen sc1
	ds_read_b128 v[0:3], v100
	ds_read_b128 v[8:11], v110
	s_waitcnt lgkmcnt(2)
	buffer_store_dwordx4 v[4:7], v12, s[0:3], 0 offen sc1
	s_nop 1
	v_add_u32_e32 v4, v49, v71
	s_waitcnt lgkmcnt(1)
	buffer_store_dwordx4 v[0:3], v4, s[0:3], 0 offen sc1
	s_nop 1
	v_add_u32_e32 v0, v50, v73
	s_waitcnt lgkmcnt(0)
	buffer_store_dwordx4 v[8:11], v0, s[0:3], 0 offen sc1
	s_endpgm
	.p2alignl 8, 3212836864

.LBB4_155:
	s_setprio 0
	s_load_dword s0, s[0:1], 0x88
	s_lshl_b32 s1, s45, 6
	s_and_b32 s1, s1, 0xfffffe00
	s_or_b32 s2, s1, s44
	v_readfirstlane_b32 s4, v0
	s_waitcnt lgkmcnt(0)
	s_mul_i32 s3, s0, 0x60000
	s_mul_hi_i32 s1, s0, 0x60000
	s_add_u32 s3, s28, s3
	s_mulk_i32 s0, 0x300
	s_addc_u32 s5, s29, s1
	s_ashr_i32 s1, s0, 31
	s_lshl_b64 s[0:1], s[0:1], 2
	s_add_u32 s0, s30, s0
	s_addc_u32 s1, s31, s1
	s_lshr_b32 s6, s4, 6
	s_and_b32 s25, s25, 0xffff
	s_mul_i32 s4, s6, 0x6000
	v_and_b32_e32 v2, 63, v0
	s_mul_hi_u32 s7, s6, 0x6000
	s_add_u32 s4, s3, s4
	s_addc_u32 s5, s5, s7
	v_lshlrev_b32_e32 v56, 4, v2
	v_mov_b32_e32 v57, 0
	v_lshl_add_u64 v[54:55], s[4:5], 0, v[56:57]
	s_movk_i32 s3, 0x1000
	v_add_co_u32_e32 v50, vcc, s3, v54
	s_movk_i32 s3, 0x2000
	s_nop 0
	v_addc_co_u32_e32 v51, vcc, 0, v55, vcc
	v_add_co_u32_e32 v52, vcc, s3, v54
	global_load_dwordx4 v[2:5], v56, s[4:5] offset:1024
	global_load_dwordx4 v[6:9], v56, s[4:5] offset:2048
	v_addc_co_u32_e32 v53, vcc, 0, v55, vcc
	global_load_dwordx4 v[10:13], v56, s[4:5] offset:3072
	global_load_dwordx4 v[14:17], v[52:53], off offset:-4096
	global_load_dwordx4 v[18:21], v[50:51], off offset:1024
	global_load_dwordx4 v[22:25], v[50:51], off offset:2048
	global_load_dwordx4 v[26:29], v56, s[4:5]
	global_load_dwordx4 v[30:33], v[50:51], off offset:3072
	global_load_dwordx4 v[34:37], v[52:53], off
	global_load_dwordx4 v[38:41], v[52:53], off offset:1024
	global_load_dwordx4 v[42:45], v[52:53], off offset:2048
	global_load_dwordx4 v[46:49], v[52:53], off offset:3072
	s_movk_i32 s3, 0x3000
	v_add_co_u32_e32 v58, vcc, s3, v54
	s_movk_i32 s3, 0x4000
	s_nop 0
	v_addc_co_u32_e32 v59, vcc, 0, v55, vcc
	v_add_co_u32_e32 v140, vcc, s3, v54
	s_nop 1
	v_addc_co_u32_e32 v141, vcc, 0, v55, vcc
	s_barrier
	global_load_dwordx4 v[50:53], v[140:141], off offset:-4096
	global_load_dwordx4 v[62:65], v[58:59], off offset:1024
	global_load_dwordx4 v[68:71], v[58:59], off offset:2048
	v_lshlrev_b32_e32 v67, 9, v1
	v_xor_b32_e32 v61, v167, v1
	v_lshl_or_b32 v66, v61, 4, v67
	ds_read_b128 v[72:75], v66
	ds_read_b128 v[76:79], v66 offset:8192
	ds_read_b128 v[80:83], v66 offset:16384
	ds_read_b128 v[84:87], v66 offset:24576
	v_mul_u32_u24_e32 v60, 0x556, v0
	v_lshrrev_b32_e32 v60, 16, v60
	s_mul_i32 s3, s6, 48
	v_lshlrev_b32_e32 v61, 3, v60
	s_movk_i32 s5, 0x47
	v_lshl_or_b32 v56, v167, 2, s3
	s_mov_b32 s3, 0xfffffd0
	v_bitop3_b32 v61, v61, s5, v60 bitop3:0xc8
	s_mov_b32 s27, 0x20000
	s_mov_b32 s26, 0x1800000
	s_mul_i32 s4, s6, 0x60
	v_mul_lo_u32 v150, v60, s3
	v_or_b32_e32 v61, s2, v61
	s_waitcnt vmcnt(8) lgkmcnt(3)
	v_mfma_f32_16x16x32_f16 v[88:91], v[26:29], v[72:75], 0
	s_waitcnt lgkmcnt(2)
	v_mfma_f32_16x16x32_f16 v[92:95], v[26:29], v[76:79], 0
	s_waitcnt lgkmcnt(1)
	v_mfma_f32_16x16x32_f16 v[96:99], v[26:29], v[80:83], 0
	s_waitcnt lgkmcnt(0)
	v_mfma_f32_16x16x32_f16 v[26:29], v[26:29], v[84:87], 0
	v_mfma_f32_16x16x32_f16 v[100:103], v[2:5], v[72:75], 0
	v_mfma_f32_16x16x32_f16 v[104:107], v[2:5], v[76:79], 0
	v_mfma_f32_16x16x32_f16 v[108:111], v[2:5], v[80:83], 0
	v_mfma_f32_16x16x32_f16 v[2:5], v[2:5], v[84:87], 0
	v_mfma_f32_16x16x32_f16 v[112:115], v[6:9], v[72:75], 0
	v_mfma_f32_16x16x32_f16 v[74:77], v[6:9], v[76:79], 0
	v_mfma_f32_16x16x32_f16 v[78:81], v[6:9], v[80:83], 0
	v_mfma_f32_16x16x32_f16 v[6:9], v[6:9], v[84:87], 0
	global_load_dwordx4 v[82:85], v[58:59], off offset:3072
	global_load_dwordx4 v[116:119], v[140:141], off
	global_load_dwordx4 v[120:123], v[140:141], off offset:1024
	v_bitop3_b32 v58, v167, v1, 4 bitop3:0x36
	v_lshl_or_b32 v72, v58, 4, v67
	ds_read_b128 v[124:127], v72
	ds_read_b128 v[128:131], v72 offset:8192
	ds_read_b128 v[132:135], v72 offset:16384
	ds_read_b128 v[136:139], v72 offset:24576
	s_waitcnt lgkmcnt(3)
	v_mfma_f32_16x16x32_f16 v[86:89], v[10:13], v[124:127], v[88:91]
	s_waitcnt lgkmcnt(2)
	v_mfma_f32_16x16x32_f16 v[90:93], v[10:13], v[128:131], v[92:95]
	s_waitcnt lgkmcnt(1)
	v_mfma_f32_16x16x32_f16 v[94:97], v[10:13], v[132:135], v[96:99]
	s_waitcnt lgkmcnt(0)
	v_mfma_f32_16x16x32_f16 v[10:13], v[10:13], v[136:139], v[26:29]
	v_mfma_f32_16x16x32_f16 v[26:29], v[14:17], v[124:127], v[100:103]
	v_mfma_f32_16x16x32_f16 v[98:101], v[14:17], v[128:131], v[104:107]
	v_mfma_f32_16x16x32_f16 v[102:105], v[14:17], v[132:135], v[108:111]
	v_mfma_f32_16x16x32_f16 v[2:5], v[14:17], v[136:139], v[2:5]
	v_mfma_f32_16x16x32_f16 v[14:17], v[18:21], v[124:127], v[112:115]
	v_mfma_f32_16x16x32_f16 v[106:109], v[18:21], v[128:131], v[74:77]
	v_mfma_f32_16x16x32_f16 v[76:79], v[18:21], v[132:135], v[78:81]
	v_mfma_f32_16x16x32_f16 v[6:9], v[18:21], v[136:139], v[6:9]
	s_movk_i32 s5, 0x5000
	v_add_co_u32_e32 v58, vcc, s5, v54
	global_load_dwordx4 v[110:113], v[140:141], off offset:2048
	global_load_dwordx4 v[124:127], v[140:141], off offset:3072
	v_addc_co_u32_e32 v59, vcc, 0, v55, vcc
	global_load_dwordx4 v[128:131], v[58:59], off
	v_bitop3_b32 v18, v167, v1, 8 bitop3:0x36
	v_lshl_or_b32 v74, v18, 4, v67
	ds_read_b128 v[18:21], v74
	ds_read_b128 v[132:135], v74 offset:8192
	ds_read_b128 v[136:139], v74 offset:16384
	ds_read_b128 v[140:143], v74 offset:24576
	s_waitcnt lgkmcnt(3)
	v_mfma_f32_16x16x32_f16 v[86:89], v[22:25], v[18:21], v[86:89]
	s_waitcnt lgkmcnt(2)
	v_mfma_f32_16x16x32_f16 v[90:93], v[22:25], v[132:135], v[90:93]
	s_waitcnt lgkmcnt(1)
	v_mfma_f32_16x16x32_f16 v[94:97], v[22:25], v[136:139], v[94:97]
	s_waitcnt lgkmcnt(0)
	v_mfma_f32_16x16x32_f16 v[10:13], v[22:25], v[140:143], v[10:13]
	s_waitcnt vmcnt(13)
	v_mfma_f32_16x16x32_f16 v[22:25], v[30:33], v[18:21], v[26:29]
	v_mfma_f32_16x16x32_f16 v[26:29], v[30:33], v[132:135], v[98:101]
	v_mfma_f32_16x16x32_f16 v[98:101], v[30:33], v[136:139], v[102:105]
	v_mfma_f32_16x16x32_f16 v[2:5], v[30:33], v[140:143], v[2:5]
	s_waitcnt vmcnt(12)
	v_mfma_f32_16x16x32_f16 v[14:17], v[34:37], v[18:21], v[14:17]
	v_mfma_f32_16x16x32_f16 v[18:21], v[34:37], v[132:135], v[106:109]
	v_mfma_f32_16x16x32_f16 v[30:33], v[34:37], v[136:139], v[76:79]
	v_mfma_f32_16x16x32_f16 v[6:9], v[34:37], v[140:143], v[6:9]
	global_load_dwordx4 v[102:105], v[58:59], off offset:1024
	global_load_dwordx4 v[106:109], v[58:59], off offset:2048
	global_load_dwordx4 v[132:135], v[58:59], off offset:3072
	v_bitop3_b32 v34, v167, v1, 12 bitop3:0x36
	v_lshl_or_b32 v75, v34, 4, v67
	ds_read_b128 v[34:37], v75
	ds_read_b128 v[76:79], v75 offset:8192
	ds_read_b128 v[136:139], v75 offset:16384
	ds_read_b128 v[140:143], v75 offset:24576
	s_waitcnt vmcnt(14) lgkmcnt(3)
	v_mfma_f32_16x16x32_f16 v[86:89], v[38:41], v[34:37], v[86:89]
	s_waitcnt lgkmcnt(2)
	v_mfma_f32_16x16x32_f16 v[90:93], v[38:41], v[76:79], v[90:93]
	s_waitcnt lgkmcnt(1)
	v_mfma_f32_16x16x32_f16 v[94:97], v[38:41], v[136:139], v[94:97]
	s_waitcnt lgkmcnt(0)
	v_mfma_f32_16x16x32_f16 v[10:13], v[38:41], v[140:143], v[10:13]
	s_waitcnt vmcnt(13)
	v_mfma_f32_16x16x32_f16 v[38:41], v[42:45], v[34:37], v[22:25]
	v_mfma_f32_16x16x32_f16 v[144:147], v[42:45], v[76:79], v[26:29]
	v_mfma_f32_16x16x32_f16 v[98:101], v[42:45], v[136:139], v[98:101]
	v_mfma_f32_16x16x32_f16 v[2:5], v[42:45], v[140:143], v[2:5]
	s_waitcnt vmcnt(12)
	v_mfma_f32_16x16x32_f16 v[14:17], v[46:49], v[34:37], v[14:17]
	v_mfma_f32_16x16x32_f16 v[18:21], v[46:49], v[76:79], v[18:21]
	v_mfma_f32_16x16x32_f16 v[30:33], v[46:49], v[136:139], v[30:33]
	v_mfma_f32_16x16x32_f16 v[6:9], v[46:49], v[140:143], v[6:9]
	s_mov_b32 s5, 0x30000
	v_add_co_u32_e32 v58, vcc, s5, v54
	s_mov_b32 s5, 0x31000
	s_nop 0
	v_addc_co_u32_e32 v59, vcc, 0, v55, vcc
	v_add_co_u32_e32 v148, vcc, s5, v54
	v_bitop3_b32 v42, v167, v1, 16 bitop3:0x36
	s_nop 0
	v_addc_co_u32_e32 v149, vcc, 0, v55, vcc
	global_load_dwordx4 v[34:37], v[148:149], off offset:-4096
	global_load_dwordx4 v[26:29], v[58:59], off offset:1024
	global_load_dwordx4 v[22:25], v[58:59], off offset:2048
	v_lshl_or_b32 v76, v42, 4, v67
	ds_read_b128 v[42:45], v76
	ds_read_b128 v[46:49], v76 offset:8192
	ds_read_b128 v[78:81], v76 offset:16384
	ds_read_b128 v[136:139], v76 offset:24576
	s_waitcnt vmcnt(14) lgkmcnt(3)
	v_mfma_f32_16x16x32_f16 v[86:89], v[50:53], v[42:45], v[86:89]
	s_waitcnt lgkmcnt(2)
	v_mfma_f32_16x16x32_f16 v[90:93], v[50:53], v[46:49], v[90:93]
	s_waitcnt lgkmcnt(1)
	v_mfma_f32_16x16x32_f16 v[94:97], v[50:53], v[78:81], v[94:97]
	s_waitcnt lgkmcnt(0)
	v_mfma_f32_16x16x32_f16 v[10:13], v[50:53], v[136:139], v[10:13]
	s_waitcnt vmcnt(13)
	v_mfma_f32_16x16x32_f16 v[38:41], v[62:65], v[42:45], v[38:41]
	v_mfma_f32_16x16x32_f16 v[50:53], v[62:65], v[46:49], v[144:147]
	v_mfma_f32_16x16x32_f16 v[98:101], v[62:65], v[78:81], v[98:101]
	v_mfma_f32_16x16x32_f16 v[62:65], v[62:65], v[136:139], v[2:5]
	s_waitcnt vmcnt(12)
	v_mfma_f32_16x16x32_f16 v[42:45], v[68:71], v[42:45], v[14:17]
	v_mfma_f32_16x16x32_f16 v[18:21], v[68:71], v[46:49], v[18:21]
	v_mfma_f32_16x16x32_f16 v[30:33], v[68:71], v[78:81], v[30:33]
	v_mfma_f32_16x16x32_f16 v[46:49], v[68:71], v[136:139], v[6:9]
	global_load_dwordx4 v[14:17], v[58:59], off offset:3072
	s_nop 1
	global_load_dwordx4 v[6:9], v[148:149], off
	global_load_dwordx4 v[2:5], v[148:149], off offset:1024
	v_bitop3_b32 v58, v167, v1, 20 bitop3:0x36
	v_lshl_or_b32 v77, v58, 4, v67
	ds_read_b128 v[68:71], v77
	ds_read_b128 v[78:81], v77 offset:8192
	ds_read_b128 v[136:139], v77 offset:16384
	ds_read_b128 v[140:143], v77 offset:24576
	s_waitcnt vmcnt(14) lgkmcnt(3)
	v_mfma_f32_16x16x32_f16 v[86:89], v[82:85], v[68:71], v[86:89]
	s_waitcnt lgkmcnt(2)
	v_mfma_f32_16x16x32_f16 v[90:93], v[82:85], v[78:81], v[90:93]
	s_waitcnt lgkmcnt(1)
	v_mfma_f32_16x16x32_f16 v[94:97], v[82:85], v[136:139], v[94:97]
	s_waitcnt lgkmcnt(0)
	v_mfma_f32_16x16x32_f16 v[82:85], v[82:85], v[140:143], v[10:13]
	s_waitcnt vmcnt(13)
	v_mfma_f32_16x16x32_f16 v[38:41], v[116:119], v[68:71], v[38:41]
	v_mfma_f32_16x16x32_f16 v[50:53], v[116:119], v[78:81], v[50:53]
	v_mfma_f32_16x16x32_f16 v[98:101], v[116:119], v[136:139], v[98:101]
	v_mfma_f32_16x16x32_f16 v[62:65], v[116:119], v[140:143], v[62:65]
	s_waitcnt vmcnt(12)
	v_mfma_f32_16x16x32_f16 v[42:45], v[120:123], v[68:71], v[42:45]
	v_mfma_f32_16x16x32_f16 v[68:71], v[120:123], v[78:81], v[18:21]
	v_mfma_f32_16x16x32_f16 v[114:117], v[120:123], v[136:139], v[30:33]
	v_mfma_f32_16x16x32_f16 v[46:49], v[120:123], v[140:143], v[46:49]
	s_mov_b32 s5, 0x33000
	v_add_co_u32_e32 v58, vcc, s5, v54
	global_load_dwordx4 v[18:21], v[148:149], off offset:2048
	global_load_dwordx4 v[10:13], v[148:149], off offset:3072
	v_addc_co_u32_e32 v59, vcc, 0, v55, vcc
	global_load_dwordx4 v[30:33], v[58:59], off offset:-4096
	v_bitop3_b32 v73, v167, v1, 24 bitop3:0x36
	v_lshl_or_b32 v78, v73, 4, v67
	ds_read_b128 v[118:121], v78
	ds_read_b128 v[136:139], v78 offset:8192
	ds_read_b128 v[140:143], v78 offset:16384
	ds_read_b128 v[144:147], v78 offset:24576
	s_mov_b32 s5, 0x32000
	v_add_co_u32_e32 v148, vcc, s5, v54
	s_nop 1
	v_addc_co_u32_e32 v149, vcc, 0, v55, vcc
	s_waitcnt vmcnt(14) lgkmcnt(3)
	v_mfma_f32_16x16x32_f16 v[86:89], v[110:113], v[118:121], v[86:89]
	s_waitcnt lgkmcnt(2)
	v_mfma_f32_16x16x32_f16 v[90:93], v[110:113], v[136:139], v[90:93]
	s_waitcnt lgkmcnt(1)
	v_mfma_f32_16x16x32_f16 v[94:97], v[110:113], v[140:143], v[94:97]
	s_waitcnt lgkmcnt(0)
	v_mfma_f32_16x16x32_f16 v[80:83], v[110:113], v[144:147], v[82:85]
	s_waitcnt vmcnt(13)
	v_mfma_f32_16x16x32_f16 v[110:113], v[124:127], v[118:121], v[38:41]
	v_mfma_f32_16x16x32_f16 v[50:53], v[124:127], v[136:139], v[50:53]
	v_mfma_f32_16x16x32_f16 v[98:101], v[124:127], v[140:143], v[98:101]
	v_mfma_f32_16x16x32_f16 v[62:65], v[124:127], v[144:147], v[62:65]
	s_waitcnt vmcnt(12)
	v_mfma_f32_16x16x32_f16 v[118:121], v[128:131], v[118:121], v[42:45]
	v_mfma_f32_16x16x32_f16 v[68:71], v[128:131], v[136:139], v[68:71]
	v_mfma_f32_16x16x32_f16 v[114:117], v[128:131], v[140:143], v[114:117]
	v_mfma_f32_16x16x32_f16 v[122:125], v[128:131], v[144:147], v[46:49]
	s_nop 2
	global_load_dwordx4 v[46:49], v[148:149], off offset:1024
	global_load_dwordx4 v[42:45], v[148:149], off offset:2048
	global_load_dwordx4 v[38:41], v[148:149], off offset:3072
	v_bitop3_b32 v73, v167, v1, 28 bitop3:0x36
	v_lshl_or_b32 v79, v73, 4, v67
	ds_read_b128 v[126:129], v79
	ds_read_b128 v[136:139], v79 offset:8192
	ds_read_b128 v[140:143], v79 offset:16384
	ds_read_b128 v[144:147], v79 offset:24576
	s_waitcnt vmcnt(14) lgkmcnt(3)
	v_mfma_f32_16x16x32_f16 v[84:87], v[102:105], v[126:129], v[86:89]
	s_waitcnt lgkmcnt(2)
	v_mfma_f32_16x16x32_f16 v[88:91], v[102:105], v[136:139], v[90:93]
	s_waitcnt lgkmcnt(1)
	v_mfma_f32_16x16x32_f16 v[92:95], v[102:105], v[140:143], v[94:97]
	s_waitcnt lgkmcnt(0)
	v_mfma_f32_16x16x32_f16 v[80:83], v[102:105], v[144:147], v[80:83]
	s_waitcnt vmcnt(13)
	v_mfma_f32_16x16x32_f16 v[102:105], v[106:109], v[126:129], v[110:113]
	v_mfma_f32_16x16x32_f16 v[110:113], v[106:109], v[136:139], v[50:53]
	v_mfma_f32_16x16x32_f16 v[96:99], v[106:109], v[140:143], v[98:101]
	v_mfma_f32_16x16x32_f16 v[62:65], v[106:109], v[144:147], v[62:65]
	s_waitcnt vmcnt(12)
	v_mfma_f32_16x16x32_f16 v[106:109], v[132:135], v[126:129], v[118:121]
	v_mfma_f32_16x16x32_f16 v[118:121], v[132:135], v[136:139], v[68:71]
	v_mfma_f32_16x16x32_f16 v[114:117], v[132:135], v[140:143], v[114:117]
	v_mfma_f32_16x16x32_f16 v[50:53], v[132:135], v[144:147], v[122:125]
	v_lshl_add_u64 v[56:57], v[56:57], 2, s[0:1]
	s_nop 1
	global_load_dwordx4 v[122:125], v[56:57], off
	global_load_dwordx4 v[126:129], v[56:57], off offset:64
	global_load_dwordx4 v[130:133], v[56:57], off offset:128
	v_lshl_or_b32 v67, v167, 3, s4
	s_movk_i32 s0, 0x310
	v_mov_b32_e32 v100, v89
	v_mov_b32_e32 v101, v90
	v_mov_b32_e32 v134, v93
	v_mov_b32_e32 v135, v94
	v_mov_b32_e32 v140, v97
	v_mov_b32_e32 v141, v98
	v_mad_u32_u24 v69, v1, s0, v67
	v_mov_b32_e32 v143, v64
	v_mov_b32_e32 v136, v81
	v_mov_b32_e32 v137, v82
	v_mov_b32_e32 v138, v111
	v_mov_b32_e32 v139, v112
	v_mov_b32_e32 v142, v63
	v_add_u32_e32 v73, 0x8000, v69
	s_barrier
	v_add_u32_e32 v70, 0xb000, v69
	v_add_u32_e32 v71, 0xe000, v69
	v_add_u32_e32 v68, 0x9300, v69
	s_movk_i32 s1, 0x600
	s_movk_i32 s6, 0x1c7
	s_waitcnt vmcnt(2)
	v_pk_add_f32 v[84:85], v[84:85], v[122:123]
	v_add_f32_e32 v1, v88, v122
	v_pk_mov_b32 v[88:89], v[122:123], v[124:125] op_sel:[1,0]
	v_add_f32_e32 v67, v91, v125
	v_add_f32_e32 v92, v92, v122
	v_add_f32_e32 v93, v95, v125
	v_add_f32_e32 v94, v80, v122
	v_add_f32_e32 v95, v83, v125
	s_waitcnt vmcnt(1)
	v_add_f32_e32 v97, v110, v126
	v_add_f32_e32 v98, v113, v129
	v_add_f32_e32 v96, v96, v126
	v_add_f32_e32 v99, v99, v129
	v_cvt_pk_f16_f32 v64, v84, v85
	v_cvt_f16_f32_e32 v1, v1
	v_pk_add_f32 v[84:85], v[100:101], v[88:89]
	v_cvt_f16_f32_e32 v67, v67
	v_cvt_f16_f32_e32 v100, v92
	v_cvt_f16_f32_e32 v101, v93
	v_cvt_f16_f32_e32 v97, v97
	v_cvt_f16_f32_e32 v98, v98
	v_pk_add_f32 v[86:87], v[86:87], v[124:125]
	v_pk_add_f32 v[80:81], v[102:103], v[126:127]
	v_pk_add_f32 v[82:83], v[104:105], v[128:129]
	v_pk_mov_b32 v[90:91], v[126:127], v[128:129] op_sel:[1,0]
	v_cvt_f16_f32_e32 v96, v96
	v_cvt_f16_f32_e32 v99, v99
	v_add_f32_e32 v102, v62, v126
	v_add_f32_e32 v103, v65, v129
	s_waitcnt vmcnt(0)
	v_pk_add_f32 v[62:63], v[106:107], v[130:131]
	v_cvt_pk_f16_f32 v65, v86, v87
	v_pk_add_f32 v[86:87], v[134:135], v[88:89]
	v_pk_add_f32 v[88:89], v[136:137], v[88:89]
	v_cvt_pk_f16_f32 v80, v80, v81
	v_cvt_pk_f16_f32 v81, v82, v83
	v_pk_add_f32 v[82:83], v[138:139], v[90:91]
	v_pk_add_f32 v[92:93], v[140:141], v[90:91]
	v_cvt_pk_f16_f32 v62, v62, v63
	v_cvt_pk_f16_f32 v63, v84, v85
	v_cvt_pk_f16_f32 v84, v86, v87
	v_cvt_pk_f16_f32 v86, v82, v83
	v_cvt_pk_f16_f32 v87, v92, v93
	ds_write2_b64 v73, v[64:65], v[80:81] offset1:4
	v_pack_b32_f16 v64, v1, v63
	v_alignbit_b32 v65, v67, v63, 16
	v_pack_b32_f16 v80, v100, v84
	v_alignbit_b32 v81, v101, v84, 16
	v_cvt_pk_f16_f32 v82, v94, v88
	v_cvt_pk_f16_f32 v83, v89, v95
	v_pack_b32_f16 v84, v97, v86
	v_alignbit_b32 v85, v98, v86, 16
	v_pack_b32_f16 v86, v96, v87
	v_alignbit_b32 v87, v99, v87, 16
	ds_write2_b64 v70, v[64:65], v[84:85] offset0:32 offset1:36
	ds_write2_b64 v71, v[80:81], v[86:87] offset0:64 offset1:68
	v_pk_add_f32 v[64:65], v[108:109], v[132:133]
	v_add_f32_e32 v1, v118, v130
	v_cvt_pk_f16_f32 v63, v64, v65
	v_add_f32_e32 v67, v121, v133
	ds_write_b64 v69, v[62:63] offset:32832
	v_mov_b32_e32 v62, v119
	v_mov_b32_e32 v63, v120
	v_pk_mov_b32 v[64:65], v[130:131], v[132:133] op_sel:[1,0]
	v_pk_add_f32 v[62:63], v[62:63], v[64:65]
	v_cvt_pk_f16_f32 v62, v1, v62
	v_add_f32_e32 v1, v114, v130
	v_cvt_pk_f16_f32 v63, v63, v67
	ds_write_b64 v69, v[62:63] offset:45376
	v_mov_b32_e32 v62, v115
	v_mov_b32_e32 v63, v116
	v_pk_add_f32 v[62:63], v[62:63], v[64:65]
	v_add_f32_e32 v67, v117, v133
	v_cvt_pk_f16_f32 v62, v1, v62
	v_add_f32_e32 v1, v50, v130
	v_mov_b32_e32 v50, v51
	v_mov_b32_e32 v51, v52
	v_add_f32_e32 v52, v53, v133
	v_pk_add_f32 v[90:91], v[142:143], v[90:91]
	v_pk_add_f32 v[50:51], v[50:51], v[64:65]
	v_cvt_pk_f16_f32 v88, v102, v90
	v_cvt_pk_f16_f32 v89, v91, v103
	v_add_u32_e32 v80, 0x8000, v68
	v_cvt_pk_f16_f32 v63, v63, v67
	v_cvt_pk_f16_f32 v50, v1, v50
	v_cvt_pk_f16_f32 v51, v51, v52
	ds_write2_b64 v80, v[82:83], v[88:89] offset1:4
	ds_write_b64 v69, v[62:63] offset:57920
	ds_write_b64 v68, v[50:51] offset:32832
	s_waitcnt lgkmcnt(0)
	s_barrier
	global_load_dwordx4 v[82:85], v[58:59], off
	global_load_dwordx4 v[86:89], v[58:59], off offset:1024
	global_load_dwordx4 v[90:93], v[58:59], off offset:2048
	v_add_lshl_u32 v52, v150, v0, 4
	v_mad_u64_u32 v[50:51], s[4:5], v61, s1, v[52:53]
	v_or_b32_e32 v1, 0x200, v0
	v_mad_u32_u24 v51, v60, s0, v52
	v_mul_u32_u24_e32 v52, 0x556, v1
	v_lshrrev_b32_e32 v53, 16, v52
	v_mul_lo_u32 v52, v53, s3
	v_add_lshl_u32 v52, v52, v1, 4
	v_lshlrev_b32_e32 v1, 3, v53
	s_movk_i32 s4, 0xc7
	ds_read_b128 v[60:63], v51 offset:32768
	v_bitop3_b32 v1, v1, s4, v53 bitop3:0xc8
	v_or_b32_e32 v1, s2, v1
	v_mad_u32_u24 v81, v53, s0, v52
	v_mad_u64_u32 v[52:53], s[4:5], v1, s1, v[52:53]
	v_or_b32_e32 v1, 0x400, v0
	v_mul_u32_u24_e32 v53, 0x556, v1
	v_lshrrev_b32_e32 v53, 16, v53
	ds_read_b128 v[94:97], v81 offset:32768
	s_waitcnt lgkmcnt(1)
	buffer_store_dwordx4 v[60:63], v50, s[24:27], 0 offen sc1
	s_waitcnt lgkmcnt(0)
	buffer_store_dwordx4 v[94:97], v52, s[24:27], 0 offen sc1
	v_lshlrev_b32_e32 v61, 3, v53
	v_mul_lo_u32 v60, v53, s3
	v_bitop3_b32 v61, v61, s6, v53 bitop3:0xc8
	v_or_b32_e32 v61, s2, v61
	v_add_lshl_u32 v62, v60, v1, 4
	v_mad_u64_u32 v[60:61], s[4:5], v61, s1, v[62:63]
	v_or_b32_e32 v1, 0x600, v0
	v_mad_u32_u24 v53, v53, s0, v62
	v_mul_u32_u24_e32 v61, 0x556, v1
	ds_read_b128 v[62:65], v53 offset:32768
	v_lshrrev_b32_e32 v67, 16, v61
	v_mul_lo_u32 v94, v67, s3
	v_add_lshl_u32 v98, v94, v1, 4
	v_lshrrev_b32_e32 v1, 13, v61
	v_mad_u32_u24 v160, v67, s0, v98
	v_and_b32_e32 v1, 0x1c0, v1
	v_bfe_u32 v61, v61, 16, 3
	ds_read_b128 v[94:97], v160 offset:32768
	v_or3_b32 v1, s2, v61, v1
	s_waitcnt lgkmcnt(1)
	buffer_store_dwordx4 v[62:65], v60, s[24:27], 0 offen sc1
	s_nop 1
	v_mad_u64_u32 v[62:63], s[4:5], v1, s1, v[98:99]
	v_or_b32_e32 v1, 0x800, v0
	v_mul_u32_u24_e32 v61, 0xaab, v1
	v_lshrrev_b32_e32 v61, 17, v61
	v_mul_lo_u32 v63, v61, s3
	v_lshlrev_b32_e32 v64, 3, v61
	s_waitcnt lgkmcnt(0)
	buffer_store_dwordx4 v[94:97], v62, s[24:27], 0 offen sc1
	v_bitop3_b32 v64, v64, s6, v61 bitop3:0xc8
	v_or_b32_e32 v64, s2, v64
	v_add_lshl_u32 v94, v63, v1, 4
	v_mad_u32_u24 v61, v61, s0, v94
	v_or_b32_e32 v0, 0xa00, v0
	v_mad_u64_u32 v[64:65], s[4:5], v64, s1, v[94:95]
	ds_read_b128 v[94:97], v61 offset:32768
	v_mul_u32_u24_e32 v1, 0xaab, v0
	v_lshrrev_b32_e32 v63, 17, v1
	v_mul_lo_u32 v65, v63, s3
	v_add_lshl_u32 v0, v65, v0, 4
	v_mad_u32_u24 v63, v63, s0, v0
	ds_read_b128 v[98:101], v63 offset:32768
	s_waitcnt lgkmcnt(1)
	buffer_store_dwordx4 v[94:97], v64, s[24:27], 0 offen sc1
	ds_read_b128 v[94:97], v66
	ds_read_b128 v[102:105], v66 offset:8192
	ds_read_b128 v[106:109], v66 offset:16384
	ds_read_b128 v[110:113], v66 offset:24576
	v_lshrrev_b32_e32 v65, 14, v1
	v_and_b32_e32 v65, 0x1c0, v65
	v_bfe_u32 v1, v1, 17, 3
	v_or3_b32 v1, s2, v1, v65
	v_mad_u64_u32 v[66:67], s[0:1], v1, s1, v[0:1]
	s_waitcnt lgkmcnt(4)
	buffer_store_dwordx4 v[98:101], v66, s[24:27], 0 offen sc1
	s_waitcnt lgkmcnt(3)
	s_nop 0
	v_mfma_f32_16x16x32_f16 v[98:101], v[34:37], v[94:97], 0
	s_waitcnt lgkmcnt(2)
	v_mfma_f32_16x16x32_f16 v[114:117], v[34:37], v[102:105], 0
	s_waitcnt lgkmcnt(1)
	v_mfma_f32_16x16x32_f16 v[118:121], v[34:37], v[106:109], 0
	s_waitcnt lgkmcnt(0)
	v_mfma_f32_16x16x32_f16 v[34:37], v[34:37], v[110:113], 0
	v_mfma_f32_16x16x32_f16 v[122:125], v[26:29], v[94:97], 0
	v_mfma_f32_16x16x32_f16 v[126:129], v[26:29], v[102:105], 0
	v_mfma_f32_16x16x32_f16 v[130:133], v[26:29], v[106:109], 0
	v_mfma_f32_16x16x32_f16 v[26:29], v[26:29], v[110:113], 0
	v_mfma_f32_16x16x32_f16 v[94:97], v[22:25], v[94:97], 0
	v_mfma_f32_16x16x32_f16 v[102:105], v[22:25], v[102:105], 0
	v_mfma_f32_16x16x32_f16 v[106:109], v[22:25], v[106:109], 0
	v_mfma_f32_16x16x32_f16 v[22:25], v[22:25], v[110:113], 0
	s_mov_b32 s0, 0x34000
	v_add_co_u32_e32 v158, vcc, s0, v54
	s_mov_b32 s0, 0x35000
	s_nop 0
	v_addc_co_u32_e32 v159, vcc, 0, v55, vcc
	v_add_co_u32_e32 v54, vcc, s0, v54
	s_nop 1
	v_addc_co_u32_e32 v55, vcc, 0, v55, vcc
	global_load_dwordx4 v[110:113], v[54:55], off offset:-4096
	global_load_dwordx4 v[134:137], v[58:59], off offset:3072
	global_load_dwordx4 v[138:141], v[158:159], off offset:1024
	ds_read_b128 v[142:145], v72
	ds_read_b128 v[146:149], v72 offset:8192
	ds_read_b128 v[150:153], v72 offset:16384
	ds_read_b128 v[154:157], v72 offset:24576
	s_waitcnt lgkmcnt(3)
	v_mfma_f32_16x16x32_f16 v[98:101], v[14:17], v[142:145], v[98:101]
	s_waitcnt lgkmcnt(2)
	v_mfma_f32_16x16x32_f16 v[114:117], v[14:17], v[146:149], v[114:117]
	s_waitcnt lgkmcnt(1)
	v_mfma_f32_16x16x32_f16 v[118:121], v[14:17], v[150:153], v[118:121]
	s_waitcnt lgkmcnt(0)
	v_mfma_f32_16x16x32_f16 v[14:17], v[14:17], v[154:157], v[34:37]
	v_mfma_f32_16x16x32_f16 v[34:37], v[6:9], v[142:145], v[122:125]
	v_mfma_f32_16x16x32_f16 v[122:125], v[6:9], v[146:149], v[126:129]
	v_mfma_f32_16x16x32_f16 v[126:129], v[6:9], v[150:153], v[130:133]
	v_mfma_f32_16x16x32_f16 v[6:9], v[6:9], v[154:157], v[26:29]
	v_mfma_f32_16x16x32_f16 v[26:29], v[2:5], v[142:145], v[94:97]
	v_mfma_f32_16x16x32_f16 v[94:97], v[2:5], v[146:149], v[102:105]
	v_mfma_f32_16x16x32_f16 v[102:105], v[2:5], v[150:153], v[106:109]
	v_mfma_f32_16x16x32_f16 v[0:3], v[2:5], v[154:157], v[22:25]
	s_nop 2
	global_load_dwordx4 v[22:25], v[158:159], off offset:2048
	global_load_dwordx4 v[106:109], v[158:159], off offset:3072
	global_load_dwordx4 v[130:133], v[54:55], off
	ds_read_b128 v[142:145], v74
	ds_read_b128 v[146:149], v74 offset:8192
	ds_read_b128 v[150:153], v74 offset:16384
	ds_read_b128 v[154:157], v74 offset:24576
	s_waitcnt lgkmcnt(3)
	v_mfma_f32_16x16x32_f16 v[98:101], v[18:21], v[142:145], v[98:101]
	s_waitcnt lgkmcnt(2)
	v_mfma_f32_16x16x32_f16 v[114:117], v[18:21], v[146:149], v[114:117]
	s_waitcnt lgkmcnt(1)
	v_mfma_f32_16x16x32_f16 v[118:121], v[18:21], v[150:153], v[118:121]
	s_waitcnt lgkmcnt(0)
	v_mfma_f32_16x16x32_f16 v[14:17], v[18:21], v[154:157], v[14:17]
	v_mfma_f32_16x16x32_f16 v[18:21], v[10:13], v[142:145], v[34:37]
	v_mfma_f32_16x16x32_f16 v[34:37], v[10:13], v[146:149], v[122:125]
	v_mfma_f32_16x16x32_f16 v[122:125], v[10:13], v[150:153], v[126:129]
	v_mfma_f32_16x16x32_f16 v[4:7], v[10:13], v[154:157], v[6:9]
	v_mfma_f32_16x16x32_f16 v[8:11], v[30:33], v[142:145], v[26:29]
	v_mfma_f32_16x16x32_f16 v[26:29], v[30:33], v[146:149], v[94:97]
	v_mfma_f32_16x16x32_f16 v[94:97], v[30:33], v[150:153], v[102:105]
	v_mfma_f32_16x16x32_f16 v[0:3], v[30:33], v[154:157], v[0:3]
	global_load_dwordx4 v[30:33], v[54:55], off offset:1024
	s_nop 0
	global_load_dwordx4 v[102:105], v[54:55], off offset:2048
	global_load_dwordx4 v[126:129], v[54:55], off offset:3072
	ds_read_b128 v[142:145], v75
	ds_read_b128 v[146:149], v75 offset:8192
	ds_read_b128 v[150:153], v75 offset:16384
	ds_read_b128 v[154:157], v75 offset:24576
	s_waitcnt lgkmcnt(3)
	v_mfma_f32_16x16x32_f16 v[98:101], v[46:49], v[142:145], v[98:101]
	s_waitcnt lgkmcnt(2)
	v_mfma_f32_16x16x32_f16 v[114:117], v[46:49], v[146:149], v[114:117]
	s_waitcnt lgkmcnt(1)
	v_mfma_f32_16x16x32_f16 v[118:121], v[46:49], v[150:153], v[118:121]
	s_waitcnt lgkmcnt(0)
	v_mfma_f32_16x16x32_f16 v[12:15], v[46:49], v[154:157], v[14:17]
	v_mfma_f32_16x16x32_f16 v[16:19], v[42:45], v[142:145], v[18:21]
	v_mfma_f32_16x16x32_f16 v[34:37], v[42:45], v[146:149], v[34:37]
	v_mfma_f32_16x16x32_f16 v[46:49], v[42:45], v[150:153], v[122:125]
	v_mfma_f32_16x16x32_f16 v[4:7], v[42:45], v[154:157], v[4:7]
	v_mfma_f32_16x16x32_f16 v[8:11], v[38:41], v[142:145], v[8:11]
	v_mfma_f32_16x16x32_f16 v[26:29], v[38:41], v[146:149], v[26:29]
	v_mfma_f32_16x16x32_f16 v[42:45], v[38:41], v[150:153], v[94:97]
	v_mfma_f32_16x16x32_f16 v[0:3], v[38:41], v[154:157], v[0:3]
	ds_read_b128 v[38:41], v76
	s_nop 0
	ds_read_b128 v[94:97], v76 offset:8192
	ds_read_b128 v[122:125], v76 offset:16384
	ds_read_b128 v[142:145], v76 offset:24576
	s_waitcnt vmcnt(17) lgkmcnt(3)
	v_mfma_f32_16x16x32_f16 v[98:101], v[82:85], v[38:41], v[98:101]
	s_waitcnt lgkmcnt(2)
	v_mfma_f32_16x16x32_f16 v[114:117], v[82:85], v[94:97], v[114:117]
	s_waitcnt lgkmcnt(1)
	v_mfma_f32_16x16x32_f16 v[118:121], v[82:85], v[122:125], v[118:121]
	s_waitcnt lgkmcnt(0)
	v_mfma_f32_16x16x32_f16 v[12:15], v[82:85], v[142:145], v[12:15]
	s_waitcnt vmcnt(16)
	v_mfma_f32_16x16x32_f16 v[16:19], v[86:89], v[38:41], v[16:19]
	v_mfma_f32_16x16x32_f16 v[34:37], v[86:89], v[94:97], v[34:37]
	v_mfma_f32_16x16x32_f16 v[46:49], v[86:89], v[122:125], v[46:49]
	v_mfma_f32_16x16x32_f16 v[4:7], v[86:89], v[142:145], v[4:7]
	s_waitcnt vmcnt(15)
	v_mfma_f32_16x16x32_f16 v[8:11], v[90:93], v[38:41], v[8:11]
	v_mfma_f32_16x16x32_f16 v[26:29], v[90:93], v[94:97], v[26:29]
	v_mfma_f32_16x16x32_f16 v[38:41], v[90:93], v[122:125], v[42:45]
	v_mfma_f32_16x16x32_f16 v[0:3], v[90:93], v[142:145], v[0:3]
	s_nop 1
	ds_read_b128 v[42:45], v77
	ds_read_b128 v[82:85], v77 offset:8192
	ds_read_b128 v[86:89], v77 offset:16384
	ds_read_b128 v[74:77], v77 offset:24576
	s_waitcnt vmcnt(7) lgkmcnt(3)
	v_mfma_f32_16x16x32_f16 v[90:93], v[134:137], v[42:45], v[98:101]
	s_waitcnt lgkmcnt(2)
	v_mfma_f32_16x16x32_f16 v[94:97], v[134:137], v[82:85], v[114:117]
	s_waitcnt lgkmcnt(1)
	v_mfma_f32_16x16x32_f16 v[98:101], v[134:137], v[86:89], v[118:121]
	s_waitcnt lgkmcnt(0)
	v_mfma_f32_16x16x32_f16 v[12:15], v[134:137], v[74:77], v[12:15]
	v_mfma_f32_16x16x32_f16 v[16:19], v[110:113], v[42:45], v[16:19]
	v_mfma_f32_16x16x32_f16 v[34:37], v[110:113], v[82:85], v[34:37]
	v_mfma_f32_16x16x32_f16 v[46:49], v[110:113], v[86:89], v[46:49]
	v_mfma_f32_16x16x32_f16 v[4:7], v[110:113], v[74:77], v[4:7]
	s_waitcnt vmcnt(6)
	v_mfma_f32_16x16x32_f16 v[8:11], v[138:141], v[42:45], v[8:11]
	v_mfma_f32_16x16x32_f16 v[26:29], v[138:141], v[82:85], v[26:29]
	v_mfma_f32_16x16x32_f16 v[38:41], v[138:141], v[86:89], v[38:41]
	v_mfma_f32_16x16x32_f16 v[0:3], v[138:141], v[74:77], v[0:3]
	ds_read_b128 v[42:45], v78
	ds_read_b128 v[74:77], v78 offset:8192
	ds_read_b128 v[82:85], v78 offset:16384
	ds_read_b128 v[86:89], v78 offset:24576
	s_waitcnt vmcnt(5) lgkmcnt(3)
	v_mfma_f32_16x16x32_f16 v[90:93], v[22:25], v[42:45], v[90:93]
	s_waitcnt lgkmcnt(2)
	v_mfma_f32_16x16x32_f16 v[94:97], v[22:25], v[74:77], v[94:97]
	s_waitcnt lgkmcnt(1)
	v_mfma_f32_16x16x32_f16 v[98:101], v[22:25], v[82:85], v[98:101]
	s_waitcnt lgkmcnt(0)
	v_mfma_f32_16x16x32_f16 v[12:15], v[22:25], v[86:89], v[12:15]
	s_waitcnt vmcnt(4)
	v_mfma_f32_16x16x32_f16 v[16:19], v[106:109], v[42:45], v[16:19]
	v_mfma_f32_16x16x32_f16 v[20:23], v[106:109], v[74:77], v[34:37]
	v_mfma_f32_16x16x32_f16 v[34:37], v[106:109], v[82:85], v[46:49]
	v_mfma_f32_16x16x32_f16 v[4:7], v[106:109], v[86:89], v[4:7]
	s_waitcnt vmcnt(3)
	v_mfma_f32_16x16x32_f16 v[8:11], v[130:133], v[42:45], v[8:11]
	v_mfma_f32_16x16x32_f16 v[24:27], v[130:133], v[74:77], v[26:29]
	v_mfma_f32_16x16x32_f16 v[38:41], v[130:133], v[82:85], v[38:41]
	v_mfma_f32_16x16x32_f16 v[0:3], v[130:133], v[86:89], v[0:3]
	ds_read_b128 v[42:45], v79
	ds_read_b128 v[46:49], v79 offset:8192
	ds_read_b128 v[74:77], v79 offset:16384
	ds_read_b128 v[82:85], v79 offset:24576
	s_waitcnt vmcnt(2) lgkmcnt(3)
	v_mfma_f32_16x16x32_f16 v[86:89], v[30:33], v[42:45], v[90:93]
	s_waitcnt lgkmcnt(2)
	v_mfma_f32_16x16x32_f16 v[90:93], v[30:33], v[46:49], v[94:97]
	s_waitcnt lgkmcnt(1)
	v_mfma_f32_16x16x32_f16 v[94:97], v[30:33], v[74:77], v[98:101]
	s_waitcnt lgkmcnt(0)
	v_mfma_f32_16x16x32_f16 v[12:15], v[30:33], v[82:85], v[12:15]
	s_waitcnt vmcnt(1)
	v_mfma_f32_16x16x32_f16 v[16:19], v[102:105], v[42:45], v[16:19]
	v_mfma_f32_16x16x32_f16 v[20:23], v[102:105], v[46:49], v[20:23]
	v_mfma_f32_16x16x32_f16 v[28:31], v[102:105], v[74:77], v[34:37]
	v_mfma_f32_16x16x32_f16 v[4:7], v[102:105], v[82:85], v[4:7]
	s_waitcnt vmcnt(0)
	v_mfma_f32_16x16x32_f16 v[8:11], v[126:129], v[42:45], v[8:11]
	v_mfma_f32_16x16x32_f16 v[24:27], v[126:129], v[46:49], v[24:27]
	v_mfma_f32_16x16x32_f16 v[32:35], v[126:129], v[74:77], v[38:41]
	v_mfma_f32_16x16x32_f16 v[0:3], v[126:129], v[82:85], v[0:3]
	s_nop 1
	global_load_dwordx4 v[36:39], v[56:57], off offset:1536
	global_load_dwordx4 v[40:43], v[56:57], off offset:1600
	global_load_dwordx4 v[44:47], v[56:57], off offset:1664
	v_mov_b32_e32 v58, v21
	v_mov_b32_e32 v59, v22
	v_mov_b32_e32 v74, v29
	v_mov_b32_e32 v56, v13
	v_mov_b32_e32 v57, v14
	v_mov_b32_e32 v75, v30
	v_mov_b32_e32 v48, v91
	v_mov_b32_e32 v49, v92
	v_mov_b32_e32 v54, v95
	v_mov_b32_e32 v55, v96
	v_mov_b32_e32 v76, v5
	v_mov_b32_e32 v77, v6
	s_barrier
	s_waitcnt vmcnt(2)
	v_pk_add_f32 v[78:79], v[86:87], v[36:37]
	v_pk_add_f32 v[82:83], v[88:89], v[38:39]
	v_add_f32_e32 v21, v90, v36
	v_pk_mov_b32 v[84:85], v[36:37], v[38:39] op_sel:[1,0]
	v_add_f32_e32 v22, v93, v39
	v_add_f32_e32 v29, v94, v36
	v_add_f32_e32 v36, v12, v36
	v_add_f32_e32 v37, v15, v39
	s_waitcnt vmcnt(1)
	v_add_f32_e32 v38, v20, v40
	v_add_f32_e32 v23, v23, v43
	v_add_f32_e32 v30, v97, v39
	v_pk_add_f32 v[12:13], v[16:17], v[40:41]
	v_pk_add_f32 v[14:15], v[18:19], v[42:43]
	v_pk_mov_b32 v[16:17], v[40:41], v[42:43] op_sel:[1,0]
	v_add_f32_e32 v28, v28, v40
	v_add_f32_e32 v31, v31, v43
	v_add_f32_e32 v39, v4, v40
	v_add_f32_e32 v40, v7, v43
	v_cvt_f16_f32_e32 v41, v21
	v_cvt_f16_f32_e32 v42, v22
	v_cvt_f16_f32_e32 v38, v38
	v_cvt_f16_f32_e32 v43, v23
	s_waitcnt vmcnt(0)
	v_pk_add_f32 v[4:5], v[8:9], v[44:45]
	v_pk_add_f32 v[6:7], v[10:11], v[46:47]
	v_pk_add_f32 v[10:11], v[48:49], v[84:85]
	v_pk_add_f32 v[20:21], v[56:57], v[84:85]
	v_cvt_pk_f16_f32 v12, v12, v13
	v_cvt_pk_f16_f32 v13, v14, v15
	v_pk_add_f32 v[14:15], v[58:59], v[16:17]
	v_cvt_pk_f16_f32 v8, v78, v79
	v_cvt_pk_f16_f32 v9, v82, v83
	v_pk_add_f32 v[18:19], v[54:55], v[84:85]
	v_pk_add_f32 v[22:23], v[74:75], v[16:17]
	v_pk_add_f32 v[16:17], v[76:77], v[16:17]
	v_cvt_pk_f16_f32 v4, v4, v5
	v_cvt_pk_f16_f32 v5, v6, v7
	v_cvt_pk_f16_f32 v6, v10, v11
	v_cvt_pk_f16_f32 v11, v14, v15
	ds_write2_b64 v73, v[8:9], v[12:13] offset1:4
	ds_write_b64 v69, v[4:5] offset:32832
	v_pack_b32_f16 v4, v41, v6
	v_alignbit_b32 v5, v42, v6, 16
	v_cvt_pk_f16_f32 v8, v36, v20
	v_cvt_pk_f16_f32 v9, v21, v37
	v_pack_b32_f16 v10, v38, v11
	v_alignbit_b32 v11, v43, v11, 16
	v_add_f32_e32 v24, v24, v44
	v_cvt_pk_f16_f32 v6, v29, v18
	v_cvt_pk_f16_f32 v7, v19, v30
	v_cvt_pk_f16_f32 v12, v28, v22
	v_cvt_pk_f16_f32 v13, v23, v31
	v_cvt_pk_f16_f32 v14, v39, v16
	v_cvt_pk_f16_f32 v15, v17, v40
	ds_write2_b64 v70, v[4:5], v[10:11] offset0:32 offset1:36
	ds_write2_b64 v71, v[6:7], v[12:13] offset0:64 offset1:68
	ds_write2_b64 v80, v[8:9], v[14:15] offset1:4
	v_add_f32_e32 v8, v27, v47
	v_mov_b32_e32 v4, v25
	v_mov_b32_e32 v5, v26
	v_pk_mov_b32 v[6:7], v[44:45], v[46:47] op_sel:[1,0]
	v_add_f32_e32 v9, v35, v47
	v_pk_add_f32 v[4:5], v[4:5], v[6:7]
	v_cvt_f16_f32_e32 v9, v9
	v_cvt_pk_f16_f32 v4, v24, v4
	v_cvt_pk_f16_f32 v5, v5, v8
	ds_write_b64 v69, v[4:5] offset:45376
	v_add_f32_e32 v4, v32, v44
	v_cvt_f16_f32_e32 v8, v4
	v_mov_b32_e32 v4, v33
	v_mov_b32_e32 v5, v34
	v_pk_add_f32 v[4:5], v[4:5], v[6:7]
	v_add_f32_e32 v0, v0, v44
	v_cvt_pk_f16_f32 v5, v4, v5
	v_pack_b32_f16 v4, v8, v5
	v_alignbit_b32 v5, v9, v5, 16
	ds_write_b64 v69, v[4:5] offset:57920
	v_cvt_f16_f32_e32 v4, v0
	v_mov_b32_e32 v0, v1
	v_mov_b32_e32 v1, v2
	v_add_f32_e32 v2, v3, v47
	v_cvt_f16_f32_e32 v2, v2
	v_pk_add_f32 v[0:1], v[0:1], v[6:7]
	s_nop 0
	v_cvt_pk_f16_f32 v1, v0, v1
	v_pack_b32_f16 v0, v4, v1
	v_alignbit_b32 v1, v2, v1, 16
	ds_write_b64 v68, v[0:1] offset:32832
	s_waitcnt lgkmcnt(0)
	s_barrier
	ds_read_b128 v[0:3], v51 offset:32768
	ds_read_b128 v[4:7], v81 offset:32768
	s_waitcnt lgkmcnt(1)
	buffer_store_dwordx4 v[0:3], v50, s[24:27], 0 offen offset:768 sc1
	ds_read_b128 v[0:3], v53 offset:32768
	ds_read_b128 v[8:11], v160 offset:32768
	ds_read_b128 v[12:15], v61 offset:32768
	ds_read_b128 v[16:19], v63 offset:32768
	s_waitcnt lgkmcnt(4)
	buffer_store_dwordx4 v[4:7], v52, s[24:27], 0 offen offset:768 sc1
	s_waitcnt lgkmcnt(3)
	buffer_store_dwordx4 v[0:3], v60, s[24:27], 0 offen offset:768 sc1
	s_waitcnt lgkmcnt(2)
	buffer_store_dwordx4 v[8:11], v62, s[24:27], 0 offen offset:768 sc1
	s_waitcnt lgkmcnt(1)
	buffer_store_dwordx4 v[12:15], v64, s[24:27], 0 offen offset:768 sc1
	s_waitcnt lgkmcnt(0)
	buffer_store_dwordx4 v[16:19], v66, s[24:27], 0 offen offset:768 sc1
	s_endpgm
	.p2alignl 8, 3212836864

.LBB5_79:
	s_mul_i32 s0, s13, s3
	s_lshl_b32 s1, s15, 6
	s_add_i32 s0, s0, s12
	s_and_b32 s1, s1, 0xfffffe00
	s_or_b32 s6, s1, s2
	s_mul_i32 s2, s0, 0x60000
	s_mul_hi_i32 s1, s0, 0x60000
	s_add_u32 s2, s8, s2
	s_mulk_i32 s0, 0x300
	s_addc_u32 s7, s9, s1
	s_ashr_i32 s1, s0, 31
	s_lshl_b64 s[0:1], s[0:1], 2
	s_add_u32 s4, s10, s0
	s_addc_u32 s5, s11, s1
	s_mul_i32 s0, s3, 0x1800000
	s_mul_hi_i32 s1, s3, 0x1800000
	s_add_u32 s0, s20, s0
	v_readfirstlane_b32 s3, v0
	s_addc_u32 s1, s21, s1
	s_lshr_b32 s8, s3, 6
	s_and_b32 s1, s1, 0xffff
	s_mul_i32 s9, s8, 0x6000
	v_and_b32_e32 v2, 63, v0
	s_mul_hi_u32 s3, s8, 0x6000
	s_add_u32 s2, s2, s9
	s_addc_u32 s3, s7, s3
	v_lshlrev_b32_e32 v56, 4, v2
	v_mov_b32_e32 v57, 0
	v_lshl_add_u64 v[54:55], s[2:3], 0, v[56:57]
	s_movk_i32 s7, 0x1000
	v_add_co_u32_e32 v50, vcc, s7, v54
	s_movk_i32 s7, 0x2000
	s_nop 0
	v_addc_co_u32_e32 v51, vcc, 0, v55, vcc
	v_add_co_u32_e32 v52, vcc, s7, v54
	global_load_dwordx4 v[2:5], v56, s[2:3] offset:1024
	global_load_dwordx4 v[6:9], v56, s[2:3] offset:2048
	v_addc_co_u32_e32 v53, vcc, 0, v55, vcc
	global_load_dwordx4 v[10:13], v56, s[2:3] offset:3072
	global_load_dwordx4 v[14:17], v[52:53], off offset:-4096
	global_load_dwordx4 v[18:21], v[50:51], off offset:1024
	global_load_dwordx4 v[22:25], v[50:51], off offset:2048
	global_load_dwordx4 v[26:29], v56, s[2:3]
	global_load_dwordx4 v[30:33], v[50:51], off offset:3072
	global_load_dwordx4 v[34:37], v[52:53], off
	global_load_dwordx4 v[38:41], v[52:53], off offset:1024
	global_load_dwordx4 v[42:45], v[52:53], off offset:2048
	global_load_dwordx4 v[46:49], v[52:53], off offset:3072
	s_movk_i32 s2, 0x3000
	v_add_co_u32_e32 v58, vcc, s2, v54
	s_movk_i32 s2, 0x4000
	s_nop 0
	v_addc_co_u32_e32 v59, vcc, 0, v55, vcc
	v_add_co_u32_e32 v140, vcc, s2, v54
	s_waitcnt lgkmcnt(0)
	s_nop 0
	v_addc_co_u32_e32 v141, vcc, 0, v55, vcc
	s_barrier
	global_load_dwordx4 v[50:53], v[140:141], off offset:-4096
	global_load_dwordx4 v[62:65], v[58:59], off offset:1024
	global_load_dwordx4 v[68:71], v[58:59], off offset:2048
	v_lshlrev_b32_e32 v67, 9, v1
	v_xor_b32_e32 v61, v158, v1
	v_lshl_or_b32 v66, v61, 4, v67
	ds_read_b128 v[72:75], v66
	ds_read_b128 v[76:79], v66 offset:8192
	ds_read_b128 v[80:83], v66 offset:16384
	ds_read_b128 v[84:87], v66 offset:24576
	v_mul_u32_u24_e32 v60, 0x556, v0
	v_lshrrev_b32_e32 v60, 16, v60
	s_mul_i32 s7, s8, 48
	v_lshlrev_b32_e32 v61, 3, v60
	s_movk_i32 s9, 0x47
	v_lshl_or_b32 v56, v158, 2, s7
	s_mov_b32 s7, 0xfffffd0
	v_bitop3_b32 v61, v61, s9, v60 bitop3:0xc8
	s_mov_b32 s2, 0x1800000
	s_mov_b32 s3, 0x20000
	s_mulk_i32 s8, 0x60
	v_mul_lo_u32 v150, v60, s7
	v_or_b32_e32 v61, s6, v61
	s_waitcnt vmcnt(8) lgkmcnt(3)
	v_mfma_f32_16x16x32_f16 v[88:91], v[26:29], v[72:75], 0
	s_waitcnt lgkmcnt(2)
	v_mfma_f32_16x16x32_f16 v[92:95], v[26:29], v[76:79], 0
	s_waitcnt lgkmcnt(1)
	v_mfma_f32_16x16x32_f16 v[96:99], v[26:29], v[80:83], 0
	s_waitcnt lgkmcnt(0)
	v_mfma_f32_16x16x32_f16 v[26:29], v[26:29], v[84:87], 0
	v_mfma_f32_16x16x32_f16 v[100:103], v[2:5], v[72:75], 0
	v_mfma_f32_16x16x32_f16 v[104:107], v[2:5], v[76:79], 0
	v_mfma_f32_16x16x32_f16 v[108:111], v[2:5], v[80:83], 0
	v_mfma_f32_16x16x32_f16 v[2:5], v[2:5], v[84:87], 0
	v_mfma_f32_16x16x32_f16 v[112:115], v[6:9], v[72:75], 0
	v_mfma_f32_16x16x32_f16 v[74:77], v[6:9], v[76:79], 0
	v_mfma_f32_16x16x32_f16 v[78:81], v[6:9], v[80:83], 0
	v_mfma_f32_16x16x32_f16 v[6:9], v[6:9], v[84:87], 0
	global_load_dwordx4 v[82:85], v[58:59], off offset:3072
	global_load_dwordx4 v[116:119], v[140:141], off
	global_load_dwordx4 v[120:123], v[140:141], off offset:1024
	v_bitop3_b32 v58, v158, v1, 4 bitop3:0x36
	v_lshl_or_b32 v72, v58, 4, v67
	ds_read_b128 v[124:127], v72
	ds_read_b128 v[128:131], v72 offset:8192
	ds_read_b128 v[132:135], v72 offset:16384
	ds_read_b128 v[136:139], v72 offset:24576
	s_waitcnt lgkmcnt(3)
	v_mfma_f32_16x16x32_f16 v[86:89], v[10:13], v[124:127], v[88:91]
	s_waitcnt lgkmcnt(2)
	v_mfma_f32_16x16x32_f16 v[90:93], v[10:13], v[128:131], v[92:95]
	s_waitcnt lgkmcnt(1)
	v_mfma_f32_16x16x32_f16 v[94:97], v[10:13], v[132:135], v[96:99]
	s_waitcnt lgkmcnt(0)
	v_mfma_f32_16x16x32_f16 v[10:13], v[10:13], v[136:139], v[26:29]
	v_mfma_f32_16x16x32_f16 v[26:29], v[14:17], v[124:127], v[100:103]
	v_mfma_f32_16x16x32_f16 v[98:101], v[14:17], v[128:131], v[104:107]
	v_mfma_f32_16x16x32_f16 v[102:105], v[14:17], v[132:135], v[108:111]
	v_mfma_f32_16x16x32_f16 v[2:5], v[14:17], v[136:139], v[2:5]
	v_mfma_f32_16x16x32_f16 v[14:17], v[18:21], v[124:127], v[112:115]
	v_mfma_f32_16x16x32_f16 v[106:109], v[18:21], v[128:131], v[74:77]
	v_mfma_f32_16x16x32_f16 v[76:79], v[18:21], v[132:135], v[78:81]
	v_mfma_f32_16x16x32_f16 v[6:9], v[18:21], v[136:139], v[6:9]
	s_movk_i32 s9, 0x5000
	v_add_co_u32_e32 v58, vcc, s9, v54
	global_load_dwordx4 v[110:113], v[140:141], off offset:2048
	global_load_dwordx4 v[124:127], v[140:141], off offset:3072
	v_addc_co_u32_e32 v59, vcc, 0, v55, vcc
	global_load_dwordx4 v[128:131], v[58:59], off
	v_bitop3_b32 v18, v158, v1, 8 bitop3:0x36
	v_lshl_or_b32 v74, v18, 4, v67
	ds_read_b128 v[18:21], v74
	ds_read_b128 v[132:135], v74 offset:8192
	ds_read_b128 v[136:139], v74 offset:16384
	ds_read_b128 v[140:143], v74 offset:24576
	s_waitcnt lgkmcnt(3)
	v_mfma_f32_16x16x32_f16 v[86:89], v[22:25], v[18:21], v[86:89]
	s_waitcnt lgkmcnt(2)
	v_mfma_f32_16x16x32_f16 v[90:93], v[22:25], v[132:135], v[90:93]
	s_waitcnt lgkmcnt(1)
	v_mfma_f32_16x16x32_f16 v[94:97], v[22:25], v[136:139], v[94:97]
	s_waitcnt lgkmcnt(0)
	v_mfma_f32_16x16x32_f16 v[10:13], v[22:25], v[140:143], v[10:13]
	s_waitcnt vmcnt(13)
	v_mfma_f32_16x16x32_f16 v[22:25], v[30:33], v[18:21], v[26:29]
	v_mfma_f32_16x16x32_f16 v[26:29], v[30:33], v[132:135], v[98:101]
	v_mfma_f32_16x16x32_f16 v[98:101], v[30:33], v[136:139], v[102:105]
	v_mfma_f32_16x16x32_f16 v[2:5], v[30:33], v[140:143], v[2:5]
	s_waitcnt vmcnt(12)
	v_mfma_f32_16x16x32_f16 v[14:17], v[34:37], v[18:21], v[14:17]
	v_mfma_f32_16x16x32_f16 v[18:21], v[34:37], v[132:135], v[106:109]
	v_mfma_f32_16x16x32_f16 v[30:33], v[34:37], v[136:139], v[76:79]
	v_mfma_f32_16x16x32_f16 v[6:9], v[34:37], v[140:143], v[6:9]
	global_load_dwordx4 v[102:105], v[58:59], off offset:1024
	global_load_dwordx4 v[106:109], v[58:59], off offset:2048
	global_load_dwordx4 v[132:135], v[58:59], off offset:3072
	v_bitop3_b32 v34, v158, v1, 12 bitop3:0x36
	v_lshl_or_b32 v75, v34, 4, v67
	ds_read_b128 v[34:37], v75
	ds_read_b128 v[76:79], v75 offset:8192
	ds_read_b128 v[136:139], v75 offset:16384
	ds_read_b128 v[140:143], v75 offset:24576
	s_waitcnt vmcnt(14) lgkmcnt(3)
	v_mfma_f32_16x16x32_f16 v[86:89], v[38:41], v[34:37], v[86:89]
	s_waitcnt lgkmcnt(2)
	v_mfma_f32_16x16x32_f16 v[90:93], v[38:41], v[76:79], v[90:93]
	s_waitcnt lgkmcnt(1)
	v_mfma_f32_16x16x32_f16 v[94:97], v[38:41], v[136:139], v[94:97]
	s_waitcnt lgkmcnt(0)
	v_mfma_f32_16x16x32_f16 v[10:13], v[38:41], v[140:143], v[10:13]
	s_waitcnt vmcnt(13)
	v_mfma_f32_16x16x32_f16 v[38:41], v[42:45], v[34:37], v[22:25]
	v_mfma_f32_16x16x32_f16 v[144:147], v[42:45], v[76:79], v[26:29]
	v_mfma_f32_16x16x32_f16 v[98:101], v[42:45], v[136:139], v[98:101]
	v_mfma_f32_16x16x32_f16 v[2:5], v[42:45], v[140:143], v[2:5]
	s_waitcnt vmcnt(12)
	v_mfma_f32_16x16x32_f16 v[14:17], v[46:49], v[34:37], v[14:17]
	v_mfma_f32_16x16x32_f16 v[18:21], v[46:49], v[76:79], v[18:21]
	v_mfma_f32_16x16x32_f16 v[30:33], v[46:49], v[136:139], v[30:33]
	v_mfma_f32_16x16x32_f16 v[6:9], v[46:49], v[140:143], v[6:9]
	s_mov_b32 s9, 0x30000
	v_add_co_u32_e32 v58, vcc, s9, v54
	s_mov_b32 s9, 0x31000
	s_nop 0
	v_addc_co_u32_e32 v59, vcc, 0, v55, vcc
	v_add_co_u32_e32 v148, vcc, s9, v54
	v_bitop3_b32 v42, v158, v1, 16 bitop3:0x36
	s_nop 0
	v_addc_co_u32_e32 v149, vcc, 0, v55, vcc
	global_load_dwordx4 v[34:37], v[148:149], off offset:-4096
	global_load_dwordx4 v[26:29], v[58:59], off offset:1024
	global_load_dwordx4 v[22:25], v[58:59], off offset:2048
	v_lshl_or_b32 v76, v42, 4, v67
	ds_read_b128 v[42:45], v76
	ds_read_b128 v[46:49], v76 offset:8192
	ds_read_b128 v[78:81], v76 offset:16384
	ds_read_b128 v[136:139], v76 offset:24576
	s_waitcnt vmcnt(14) lgkmcnt(3)
	v_mfma_f32_16x16x32_f16 v[86:89], v[50:53], v[42:45], v[86:89]
	s_waitcnt lgkmcnt(2)
	v_mfma_f32_16x16x32_f16 v[90:93], v[50:53], v[46:49], v[90:93]
	s_waitcnt lgkmcnt(1)
	v_mfma_f32_16x16x32_f16 v[94:97], v[50:53], v[78:81], v[94:97]
	s_waitcnt lgkmcnt(0)
	v_mfma_f32_16x16x32_f16 v[10:13], v[50:53], v[136:139], v[10:13]
	s_waitcnt vmcnt(13)
	v_mfma_f32_16x16x32_f16 v[38:41], v[62:65], v[42:45], v[38:41]
	v_mfma_f32_16x16x32_f16 v[50:53], v[62:65], v[46:49], v[144:147]
	v_mfma_f32_16x16x32_f16 v[98:101], v[62:65], v[78:81], v[98:101]
	v_mfma_f32_16x16x32_f16 v[62:65], v[62:65], v[136:139], v[2:5]
	s_waitcnt vmcnt(12)
	v_mfma_f32_16x16x32_f16 v[42:45], v[68:71], v[42:45], v[14:17]
	v_mfma_f32_16x16x32_f16 v[18:21], v[68:71], v[46:49], v[18:21]
	v_mfma_f32_16x16x32_f16 v[30:33], v[68:71], v[78:81], v[30:33]
	v_mfma_f32_16x16x32_f16 v[46:49], v[68:71], v[136:139], v[6:9]
	global_load_dwordx4 v[14:17], v[58:59], off offset:3072
	s_nop 1
	global_load_dwordx4 v[6:9], v[148:149], off
	global_load_dwordx4 v[2:5], v[148:149], off offset:1024
	v_bitop3_b32 v58, v158, v1, 20 bitop3:0x36
	v_lshl_or_b32 v77, v58, 4, v67
	ds_read_b128 v[68:71], v77
	ds_read_b128 v[78:81], v77 offset:8192
	ds_read_b128 v[136:139], v77 offset:16384
	ds_read_b128 v[140:143], v77 offset:24576
	s_waitcnt vmcnt(14) lgkmcnt(3)
	v_mfma_f32_16x16x32_f16 v[86:89], v[82:85], v[68:71], v[86:89]
	s_waitcnt lgkmcnt(2)
	v_mfma_f32_16x16x32_f16 v[90:93], v[82:85], v[78:81], v[90:93]
	s_waitcnt lgkmcnt(1)
	v_mfma_f32_16x16x32_f16 v[94:97], v[82:85], v[136:139], v[94:97]
	s_waitcnt lgkmcnt(0)
	v_mfma_f32_16x16x32_f16 v[82:85], v[82:85], v[140:143], v[10:13]
	s_waitcnt vmcnt(13)
	v_mfma_f32_16x16x32_f16 v[38:41], v[116:119], v[68:71], v[38:41]
	v_mfma_f32_16x16x32_f16 v[50:53], v[116:119], v[78:81], v[50:53]
	v_mfma_f32_16x16x32_f16 v[98:101], v[116:119], v[136:139], v[98:101]
	v_mfma_f32_16x16x32_f16 v[62:65], v[116:119], v[140:143], v[62:65]
	s_waitcnt vmcnt(12)
	v_mfma_f32_16x16x32_f16 v[42:45], v[120:123], v[68:71], v[42:45]
	v_mfma_f32_16x16x32_f16 v[68:71], v[120:123], v[78:81], v[18:21]
	v_mfma_f32_16x16x32_f16 v[114:117], v[120:123], v[136:139], v[30:33]
	v_mfma_f32_16x16x32_f16 v[46:49], v[120:123], v[140:143], v[46:49]
	s_mov_b32 s9, 0x33000
	v_add_co_u32_e32 v58, vcc, s9, v54
	global_load_dwordx4 v[18:21], v[148:149], off offset:2048
	global_load_dwordx4 v[10:13], v[148:149], off offset:3072
	v_addc_co_u32_e32 v59, vcc, 0, v55, vcc
	global_load_dwordx4 v[30:33], v[58:59], off offset:-4096
	v_bitop3_b32 v73, v158, v1, 24 bitop3:0x36
	v_lshl_or_b32 v78, v73, 4, v67
	ds_read_b128 v[118:121], v78
	ds_read_b128 v[136:139], v78 offset:8192
	ds_read_b128 v[140:143], v78 offset:16384
	ds_read_b128 v[144:147], v78 offset:24576
	s_mov_b32 s9, 0x32000
	v_add_co_u32_e32 v148, vcc, s9, v54
	s_nop 1
	v_addc_co_u32_e32 v149, vcc, 0, v55, vcc
	s_waitcnt vmcnt(14) lgkmcnt(3)
	v_mfma_f32_16x16x32_f16 v[86:89], v[110:113], v[118:121], v[86:89]
	s_waitcnt lgkmcnt(2)
	v_mfma_f32_16x16x32_f16 v[90:93], v[110:113], v[136:139], v[90:93]
	s_waitcnt lgkmcnt(1)
	v_mfma_f32_16x16x32_f16 v[94:97], v[110:113], v[140:143], v[94:97]
	s_waitcnt lgkmcnt(0)
	v_mfma_f32_16x16x32_f16 v[80:83], v[110:113], v[144:147], v[82:85]
	s_waitcnt vmcnt(13)
	v_mfma_f32_16x16x32_f16 v[110:113], v[124:127], v[118:121], v[38:41]
	v_mfma_f32_16x16x32_f16 v[50:53], v[124:127], v[136:139], v[50:53]
	v_mfma_f32_16x16x32_f16 v[98:101], v[124:127], v[140:143], v[98:101]
	v_mfma_f32_16x16x32_f16 v[62:65], v[124:127], v[144:147], v[62:65]
	s_waitcnt vmcnt(12)
	v_mfma_f32_16x16x32_f16 v[118:121], v[128:131], v[118:121], v[42:45]
	v_mfma_f32_16x16x32_f16 v[68:71], v[128:131], v[136:139], v[68:71]
	v_mfma_f32_16x16x32_f16 v[114:117], v[128:131], v[140:143], v[114:117]
	v_mfma_f32_16x16x32_f16 v[122:125], v[128:131], v[144:147], v[46:49]
	s_nop 2
	global_load_dwordx4 v[46:49], v[148:149], off offset:1024
	global_load_dwordx4 v[42:45], v[148:149], off offset:2048
	global_load_dwordx4 v[38:41], v[148:149], off offset:3072
	v_bitop3_b32 v73, v158, v1, 28 bitop3:0x36
	v_lshl_or_b32 v79, v73, 4, v67
	ds_read_b128 v[126:129], v79
	ds_read_b128 v[136:139], v79 offset:8192
	ds_read_b128 v[140:143], v79 offset:16384
	ds_read_b128 v[144:147], v79 offset:24576
	s_waitcnt vmcnt(14) lgkmcnt(3)
	v_mfma_f32_16x16x32_f16 v[84:87], v[102:105], v[126:129], v[86:89]
	s_waitcnt lgkmcnt(2)
	v_mfma_f32_16x16x32_f16 v[88:91], v[102:105], v[136:139], v[90:93]
	s_waitcnt lgkmcnt(1)
	v_mfma_f32_16x16x32_f16 v[92:95], v[102:105], v[140:143], v[94:97]
	s_waitcnt lgkmcnt(0)
	v_mfma_f32_16x16x32_f16 v[80:83], v[102:105], v[144:147], v[80:83]
	s_waitcnt vmcnt(13)
	v_mfma_f32_16x16x32_f16 v[102:105], v[106:109], v[126:129], v[110:113]
	v_mfma_f32_16x16x32_f16 v[110:113], v[106:109], v[136:139], v[50:53]
	v_mfma_f32_16x16x32_f16 v[96:99], v[106:109], v[140:143], v[98:101]
	v_mfma_f32_16x16x32_f16 v[62:65], v[106:109], v[144:147], v[62:65]
	s_waitcnt vmcnt(12)
	v_mfma_f32_16x16x32_f16 v[106:109], v[132:135], v[126:129], v[118:121]
	v_mfma_f32_16x16x32_f16 v[118:121], v[132:135], v[136:139], v[68:71]
	v_mfma_f32_16x16x32_f16 v[114:117], v[132:135], v[140:143], v[114:117]
	v_mfma_f32_16x16x32_f16 v[50:53], v[132:135], v[144:147], v[122:125]
	v_lshl_add_u64 v[56:57], v[56:57], 2, s[4:5]
	s_nop 1
	global_load_dwordx4 v[122:125], v[56:57], off
	global_load_dwordx4 v[126:129], v[56:57], off offset:64
	global_load_dwordx4 v[130:133], v[56:57], off offset:128
	v_lshl_or_b32 v67, v158, 3, s8
	s_movk_i32 s4, 0x310
	v_mov_b32_e32 v100, v89
	v_mov_b32_e32 v101, v90
	v_mov_b32_e32 v134, v93
	v_mov_b32_e32 v135, v94
	v_mov_b32_e32 v140, v97
	v_mov_b32_e32 v141, v98
	v_mad_u32_u24 v69, v1, s4, v67
	v_mov_b32_e32 v143, v64
	v_mov_b32_e32 v136, v81
	v_mov_b32_e32 v137, v82
	v_mov_b32_e32 v138, v111
	v_mov_b32_e32 v139, v112
	v_mov_b32_e32 v142, v63
	v_add_u32_e32 v73, 0x8000, v69
	s_barrier
	v_add_u32_e32 v70, 0xb000, v69
	v_add_u32_e32 v71, 0xe000, v69
	v_add_u32_e32 v68, 0x9300, v69
	s_movk_i32 s5, 0x600
	s_movk_i32 s10, 0x1c7
	s_waitcnt vmcnt(2)
	v_pk_add_f32 v[84:85], v[84:85], v[122:123]
	v_add_f32_e32 v1, v88, v122
	v_pk_mov_b32 v[88:89], v[122:123], v[124:125] op_sel:[1,0]
	v_add_f32_e32 v67, v91, v125
	v_add_f32_e32 v92, v92, v122
	v_add_f32_e32 v93, v95, v125
	v_add_f32_e32 v94, v80, v122
	v_add_f32_e32 v95, v83, v125
	s_waitcnt vmcnt(1)
	v_add_f32_e32 v97, v110, v126
	v_add_f32_e32 v98, v113, v129
	v_add_f32_e32 v96, v96, v126
	v_add_f32_e32 v99, v99, v129
	v_cvt_pk_f16_f32 v64, v84, v85
	v_cvt_f16_f32_e32 v1, v1
	v_pk_add_f32 v[84:85], v[100:101], v[88:89]
	v_cvt_f16_f32_e32 v67, v67
	v_cvt_f16_f32_e32 v100, v92
	v_cvt_f16_f32_e32 v101, v93
	v_cvt_f16_f32_e32 v97, v97
	v_cvt_f16_f32_e32 v98, v98
	v_pk_add_f32 v[86:87], v[86:87], v[124:125]
	v_pk_add_f32 v[80:81], v[102:103], v[126:127]
	v_pk_add_f32 v[82:83], v[104:105], v[128:129]
	v_pk_mov_b32 v[90:91], v[126:127], v[128:129] op_sel:[1,0]
	v_cvt_f16_f32_e32 v96, v96
	v_cvt_f16_f32_e32 v99, v99
	v_add_f32_e32 v102, v62, v126
	v_add_f32_e32 v103, v65, v129
	s_waitcnt vmcnt(0)
	v_pk_add_f32 v[62:63], v[106:107], v[130:131]
	v_cvt_pk_f16_f32 v65, v86, v87
	v_pk_add_f32 v[86:87], v[134:135], v[88:89]
	v_pk_add_f32 v[88:89], v[136:137], v[88:89]
	v_cvt_pk_f16_f32 v80, v80, v81
	v_cvt_pk_f16_f32 v81, v82, v83
	v_pk_add_f32 v[82:83], v[138:139], v[90:91]
	v_pk_add_f32 v[92:93], v[140:141], v[90:91]
	v_cvt_pk_f16_f32 v62, v62, v63
	v_cvt_pk_f16_f32 v63, v84, v85
	v_cvt_pk_f16_f32 v84, v86, v87
	v_cvt_pk_f16_f32 v86, v82, v83
	v_cvt_pk_f16_f32 v87, v92, v93
	ds_write2_b64 v73, v[64:65], v[80:81] offset1:4
	v_pack_b32_f16 v64, v1, v63
	v_alignbit_b32 v65, v67, v63, 16
	v_pack_b32_f16 v80, v100, v84
	v_alignbit_b32 v81, v101, v84, 16
	v_cvt_pk_f16_f32 v82, v94, v88
	v_cvt_pk_f16_f32 v83, v89, v95
	v_pack_b32_f16 v84, v97, v86
	v_alignbit_b32 v85, v98, v86, 16
	v_pack_b32_f16 v86, v96, v87
	v_alignbit_b32 v87, v99, v87, 16
	ds_write2_b64 v70, v[64:65], v[84:85] offset0:32 offset1:36
	ds_write2_b64 v71, v[80:81], v[86:87] offset0:64 offset1:68
	v_pk_add_f32 v[64:65], v[108:109], v[132:133]
	v_add_f32_e32 v1, v118, v130
	v_cvt_pk_f16_f32 v63, v64, v65
	v_add_f32_e32 v67, v121, v133
	ds_write_b64 v69, v[62:63] offset:32832
	v_mov_b32_e32 v62, v119
	v_mov_b32_e32 v63, v120
	v_pk_mov_b32 v[64:65], v[130:131], v[132:133] op_sel:[1,0]
	v_pk_add_f32 v[62:63], v[62:63], v[64:65]
	v_cvt_pk_f16_f32 v62, v1, v62
	v_add_f32_e32 v1, v114, v130
	v_cvt_pk_f16_f32 v63, v63, v67
	ds_write_b64 v69, v[62:63] offset:45376
	v_mov_b32_e32 v62, v115
	v_mov_b32_e32 v63, v116
	v_pk_add_f32 v[62:63], v[62:63], v[64:65]
	v_add_f32_e32 v67, v117, v133
	v_cvt_pk_f16_f32 v62, v1, v62
	v_add_f32_e32 v1, v50, v130
	v_mov_b32_e32 v50, v51
	v_mov_b32_e32 v51, v52
	v_add_f32_e32 v52, v53, v133
	v_pk_add_f32 v[90:91], v[142:143], v[90:91]
	v_pk_add_f32 v[50:51], v[50:51], v[64:65]
	v_cvt_pk_f16_f32 v88, v102, v90
	v_cvt_pk_f16_f32 v89, v91, v103
	v_add_u32_e32 v80, 0x8000, v68
	v_cvt_pk_f16_f32 v63, v63, v67
	v_cvt_pk_f16_f32 v50, v1, v50
	v_cvt_pk_f16_f32 v51, v51, v52
	ds_write2_b64 v80, v[82:83], v[88:89] offset1:4
	ds_write_b64 v69, v[62:63] offset:57920
	ds_write_b64 v68, v[50:51] offset:32832
	s_waitcnt lgkmcnt(0)
	s_barrier
	global_load_dwordx4 v[82:85], v[58:59], off
	global_load_dwordx4 v[86:89], v[58:59], off offset:1024
	global_load_dwordx4 v[90:93], v[58:59], off offset:2048
	v_add_lshl_u32 v52, v150, v0, 4
	v_mad_u64_u32 v[50:51], s[8:9], v61, s5, v[52:53]
	v_or_b32_e32 v1, 0x200, v0
	v_mad_u32_u24 v51, v60, s4, v52
	v_mul_u32_u24_e32 v52, 0x556, v1
	v_lshrrev_b32_e32 v53, 16, v52
	v_mul_lo_u32 v52, v53, s7
	v_add_lshl_u32 v52, v52, v1, 4
	v_lshlrev_b32_e32 v1, 3, v53
	s_movk_i32 s8, 0xc7
	ds_read_b128 v[60:63], v51 offset:32768
	v_bitop3_b32 v1, v1, s8, v53 bitop3:0xc8
	v_or_b32_e32 v1, s6, v1
	v_mad_u32_u24 v81, v53, s4, v52
	v_mad_u64_u32 v[52:53], s[8:9], v1, s5, v[52:53]
	v_or_b32_e32 v1, 0x400, v0
	v_mul_u32_u24_e32 v53, 0x556, v1
	v_lshrrev_b32_e32 v53, 16, v53
	ds_read_b128 v[94:97], v81 offset:32768
	s_waitcnt lgkmcnt(1)
	buffer_store_dwordx4 v[60:63], v50, s[0:3], 0 offen sc1
	s_waitcnt lgkmcnt(0)
	buffer_store_dwordx4 v[94:97], v52, s[0:3], 0 offen sc1
	v_lshlrev_b32_e32 v61, 3, v53
	v_mul_lo_u32 v60, v53, s7
	v_bitop3_b32 v61, v61, s10, v53 bitop3:0xc8
	v_or_b32_e32 v61, s6, v61
	v_add_lshl_u32 v62, v60, v1, 4
	v_mad_u64_u32 v[60:61], s[8:9], v61, s5, v[62:63]
	v_or_b32_e32 v1, 0x600, v0
	v_mad_u32_u24 v53, v53, s4, v62
	v_mul_u32_u24_e32 v61, 0x556, v1
	ds_read_b128 v[62:65], v53 offset:32768
	v_lshrrev_b32_e32 v67, 16, v61
	v_mul_lo_u32 v94, v67, s7
	v_add_lshl_u32 v98, v94, v1, 4
	v_lshrrev_b32_e32 v1, 13, v61
	v_mad_u32_u24 v160, v67, s4, v98
	v_and_b32_e32 v1, 0x1c0, v1
	v_bfe_u32 v61, v61, 16, 3
	ds_read_b128 v[94:97], v160 offset:32768
	v_or3_b32 v1, s6, v61, v1
	s_waitcnt lgkmcnt(1)
	buffer_store_dwordx4 v[62:65], v60, s[0:3], 0 offen sc1
	s_nop 1
	v_mad_u64_u32 v[62:63], s[8:9], v1, s5, v[98:99]
	v_or_b32_e32 v1, 0x800, v0
	v_mul_u32_u24_e32 v61, 0xaab, v1
	v_lshrrev_b32_e32 v61, 17, v61
	v_mul_lo_u32 v63, v61, s7
	v_lshlrev_b32_e32 v64, 3, v61
	s_waitcnt lgkmcnt(0)
	buffer_store_dwordx4 v[94:97], v62, s[0:3], 0 offen sc1
	v_bitop3_b32 v64, v64, s10, v61 bitop3:0xc8
	v_or_b32_e32 v64, s6, v64
	v_add_lshl_u32 v94, v63, v1, 4
	v_mad_u32_u24 v61, v61, s4, v94
	v_or_b32_e32 v0, 0xa00, v0
	v_mad_u64_u32 v[64:65], s[8:9], v64, s5, v[94:95]
	ds_read_b128 v[94:97], v61 offset:32768
	v_mul_u32_u24_e32 v1, 0xaab, v0
	v_lshrrev_b32_e32 v63, 17, v1
	v_mul_lo_u32 v65, v63, s7
	v_add_lshl_u32 v0, v65, v0, 4
	v_mad_u32_u24 v63, v63, s4, v0
	ds_read_b128 v[98:101], v63 offset:32768
	s_waitcnt lgkmcnt(1)
	buffer_store_dwordx4 v[94:97], v64, s[0:3], 0 offen sc1
	ds_read_b128 v[94:97], v66
	ds_read_b128 v[102:105], v66 offset:8192
	ds_read_b128 v[106:109], v66 offset:16384
	ds_read_b128 v[110:113], v66 offset:24576
	v_lshrrev_b32_e32 v65, 14, v1
	v_and_b32_e32 v65, 0x1c0, v65
	v_bfe_u32 v1, v1, 17, 3
	v_or3_b32 v1, s6, v1, v65
	v_mad_u64_u32 v[66:67], s[4:5], v1, s5, v[0:1]
	s_waitcnt lgkmcnt(4)
	buffer_store_dwordx4 v[98:101], v66, s[0:3], 0 offen sc1
	s_waitcnt lgkmcnt(3)
	s_nop 0
	v_mfma_f32_16x16x32_f16 v[98:101], v[34:37], v[94:97], 0
	s_waitcnt lgkmcnt(2)
	v_mfma_f32_16x16x32_f16 v[114:117], v[34:37], v[102:105], 0
	s_waitcnt lgkmcnt(1)
	v_mfma_f32_16x16x32_f16 v[118:121], v[34:37], v[106:109], 0
	s_waitcnt lgkmcnt(0)
	v_mfma_f32_16x16x32_f16 v[34:37], v[34:37], v[110:113], 0
	v_mfma_f32_16x16x32_f16 v[122:125], v[26:29], v[94:97], 0
	v_mfma_f32_16x16x32_f16 v[126:129], v[26:29], v[102:105], 0
	v_mfma_f32_16x16x32_f16 v[130:133], v[26:29], v[106:109], 0
	v_mfma_f32_16x16x32_f16 v[26:29], v[26:29], v[110:113], 0
	v_mfma_f32_16x16x32_f16 v[94:97], v[22:25], v[94:97], 0
	v_mfma_f32_16x16x32_f16 v[102:105], v[22:25], v[102:105], 0
	v_mfma_f32_16x16x32_f16 v[106:109], v[22:25], v[106:109], 0
	v_mfma_f32_16x16x32_f16 v[22:25], v[22:25], v[110:113], 0
	s_mov_b32 s4, 0x34000
	v_add_co_u32_e32 v158, vcc, s4, v54
	s_mov_b32 s4, 0x35000
	s_nop 0
	v_addc_co_u32_e32 v159, vcc, 0, v55, vcc
	v_add_co_u32_e32 v54, vcc, s4, v54
	s_nop 1
	v_addc_co_u32_e32 v55, vcc, 0, v55, vcc
	global_load_dwordx4 v[110:113], v[54:55], off offset:-4096
	global_load_dwordx4 v[134:137], v[58:59], off offset:3072
	global_load_dwordx4 v[138:141], v[158:159], off offset:1024
	ds_read_b128 v[142:145], v72
	ds_read_b128 v[146:149], v72 offset:8192
	ds_read_b128 v[150:153], v72 offset:16384
	ds_read_b128 v[154:157], v72 offset:24576
	s_waitcnt lgkmcnt(3)
	v_mfma_f32_16x16x32_f16 v[98:101], v[14:17], v[142:145], v[98:101]
	s_waitcnt lgkmcnt(2)
	v_mfma_f32_16x16x32_f16 v[114:117], v[14:17], v[146:149], v[114:117]
	s_waitcnt lgkmcnt(1)
	v_mfma_f32_16x16x32_f16 v[118:121], v[14:17], v[150:153], v[118:121]
	s_waitcnt lgkmcnt(0)
	v_mfma_f32_16x16x32_f16 v[14:17], v[14:17], v[154:157], v[34:37]
	v_mfma_f32_16x16x32_f16 v[34:37], v[6:9], v[142:145], v[122:125]
	v_mfma_f32_16x16x32_f16 v[122:125], v[6:9], v[146:149], v[126:129]
	v_mfma_f32_16x16x32_f16 v[126:129], v[6:9], v[150:153], v[130:133]
	v_mfma_f32_16x16x32_f16 v[6:9], v[6:9], v[154:157], v[26:29]
	v_mfma_f32_16x16x32_f16 v[26:29], v[2:5], v[142:145], v[94:97]
	v_mfma_f32_16x16x32_f16 v[94:97], v[2:5], v[146:149], v[102:105]
	v_mfma_f32_16x16x32_f16 v[102:105], v[2:5], v[150:153], v[106:109]
	v_mfma_f32_16x16x32_f16 v[0:3], v[2:5], v[154:157], v[22:25]
	s_nop 2
	global_load_dwordx4 v[22:25], v[158:159], off offset:2048
	global_load_dwordx4 v[106:109], v[158:159], off offset:3072
	global_load_dwordx4 v[130:133], v[54:55], off
	ds_read_b128 v[142:145], v74
	ds_read_b128 v[146:149], v74 offset:8192
	ds_read_b128 v[150:153], v74 offset:16384
	ds_read_b128 v[154:157], v74 offset:24576
	s_waitcnt lgkmcnt(3)
	v_mfma_f32_16x16x32_f16 v[98:101], v[18:21], v[142:145], v[98:101]
	s_waitcnt lgkmcnt(2)
	v_mfma_f32_16x16x32_f16 v[114:117], v[18:21], v[146:149], v[114:117]
	s_waitcnt lgkmcnt(1)
	v_mfma_f32_16x16x32_f16 v[118:121], v[18:21], v[150:153], v[118:121]
	s_waitcnt lgkmcnt(0)
	v_mfma_f32_16x16x32_f16 v[14:17], v[18:21], v[154:157], v[14:17]
	v_mfma_f32_16x16x32_f16 v[18:21], v[10:13], v[142:145], v[34:37]
	v_mfma_f32_16x16x32_f16 v[34:37], v[10:13], v[146:149], v[122:125]
	v_mfma_f32_16x16x32_f16 v[122:125], v[10:13], v[150:153], v[126:129]
	v_mfma_f32_16x16x32_f16 v[4:7], v[10:13], v[154:157], v[6:9]
	v_mfma_f32_16x16x32_f16 v[8:11], v[30:33], v[142:145], v[26:29]
	v_mfma_f32_16x16x32_f16 v[26:29], v[30:33], v[146:149], v[94:97]
	v_mfma_f32_16x16x32_f16 v[94:97], v[30:33], v[150:153], v[102:105]
	v_mfma_f32_16x16x32_f16 v[0:3], v[30:33], v[154:157], v[0:3]
	global_load_dwordx4 v[30:33], v[54:55], off offset:1024
	s_nop 0
	global_load_dwordx4 v[102:105], v[54:55], off offset:2048
	global_load_dwordx4 v[126:129], v[54:55], off offset:3072
	ds_read_b128 v[142:145], v75
	ds_read_b128 v[146:149], v75 offset:8192
	ds_read_b128 v[150:153], v75 offset:16384
	ds_read_b128 v[154:157], v75 offset:24576
	s_waitcnt lgkmcnt(3)
	v_mfma_f32_16x16x32_f16 v[98:101], v[46:49], v[142:145], v[98:101]
	s_waitcnt lgkmcnt(2)
	v_mfma_f32_16x16x32_f16 v[114:117], v[46:49], v[146:149], v[114:117]
	s_waitcnt lgkmcnt(1)
	v_mfma_f32_16x16x32_f16 v[118:121], v[46:49], v[150:153], v[118:121]
	s_waitcnt lgkmcnt(0)
	v_mfma_f32_16x16x32_f16 v[12:15], v[46:49], v[154:157], v[14:17]
	v_mfma_f32_16x16x32_f16 v[16:19], v[42:45], v[142:145], v[18:21]
	v_mfma_f32_16x16x32_f16 v[34:37], v[42:45], v[146:149], v[34:37]
	v_mfma_f32_16x16x32_f16 v[46:49], v[42:45], v[150:153], v[122:125]
	v_mfma_f32_16x16x32_f16 v[4:7], v[42:45], v[154:157], v[4:7]
	v_mfma_f32_16x16x32_f16 v[8:11], v[38:41], v[142:145], v[8:11]
	v_mfma_f32_16x16x32_f16 v[26:29], v[38:41], v[146:149], v[26:29]
	v_mfma_f32_16x16x32_f16 v[42:45], v[38:41], v[150:153], v[94:97]
	v_mfma_f32_16x16x32_f16 v[0:3], v[38:41], v[154:157], v[0:3]
	ds_read_b128 v[38:41], v76
	s_nop 0
	ds_read_b128 v[94:97], v76 offset:8192
	ds_read_b128 v[122:125], v76 offset:16384
	ds_read_b128 v[142:145], v76 offset:24576
	s_waitcnt vmcnt(17) lgkmcnt(3)
	v_mfma_f32_16x16x32_f16 v[98:101], v[82:85], v[38:41], v[98:101]
	s_waitcnt lgkmcnt(2)
	v_mfma_f32_16x16x32_f16 v[114:117], v[82:85], v[94:97], v[114:117]
	s_waitcnt lgkmcnt(1)
	v_mfma_f32_16x16x32_f16 v[118:121], v[82:85], v[122:125], v[118:121]
	s_waitcnt lgkmcnt(0)
	v_mfma_f32_16x16x32_f16 v[12:15], v[82:85], v[142:145], v[12:15]
	s_waitcnt vmcnt(16)
	v_mfma_f32_16x16x32_f16 v[16:19], v[86:89], v[38:41], v[16:19]
	v_mfma_f32_16x16x32_f16 v[34:37], v[86:89], v[94:97], v[34:37]
	v_mfma_f32_16x16x32_f16 v[46:49], v[86:89], v[122:125], v[46:49]
	v_mfma_f32_16x16x32_f16 v[4:7], v[86:89], v[142:145], v[4:7]
	s_waitcnt vmcnt(15)
	v_mfma_f32_16x16x32_f16 v[8:11], v[90:93], v[38:41], v[8:11]
	v_mfma_f32_16x16x32_f16 v[26:29], v[90:93], v[94:97], v[26:29]
	v_mfma_f32_16x16x32_f16 v[38:41], v[90:93], v[122:125], v[42:45]
	v_mfma_f32_16x16x32_f16 v[0:3], v[90:93], v[142:145], v[0:3]
	s_nop 1
	ds_read_b128 v[42:45], v77
	ds_read_b128 v[82:85], v77 offset:8192
	ds_read_b128 v[86:89], v77 offset:16384
	ds_read_b128 v[74:77], v77 offset:24576
	s_waitcnt vmcnt(7) lgkmcnt(3)
	v_mfma_f32_16x16x32_f16 v[90:93], v[134:137], v[42:45], v[98:101]
	s_waitcnt lgkmcnt(2)
	v_mfma_f32_16x16x32_f16 v[94:97], v[134:137], v[82:85], v[114:117]
	s_waitcnt lgkmcnt(1)
	v_mfma_f32_16x16x32_f16 v[98:101], v[134:137], v[86:89], v[118:121]
	s_waitcnt lgkmcnt(0)
	v_mfma_f32_16x16x32_f16 v[12:15], v[134:137], v[74:77], v[12:15]
	v_mfma_f32_16x16x32_f16 v[16:19], v[110:113], v[42:45], v[16:19]
	v_mfma_f32_16x16x32_f16 v[34:37], v[110:113], v[82:85], v[34:37]
	v_mfma_f32_16x16x32_f16 v[46:49], v[110:113], v[86:89], v[46:49]
	v_mfma_f32_16x16x32_f16 v[4:7], v[110:113], v[74:77], v[4:7]
	s_waitcnt vmcnt(6)
	v_mfma_f32_16x16x32_f16 v[8:11], v[138:141], v[42:45], v[8:11]
	v_mfma_f32_16x16x32_f16 v[26:29], v[138:141], v[82:85], v[26:29]
	v_mfma_f32_16x16x32_f16 v[38:41], v[138:141], v[86:89], v[38:41]
	v_mfma_f32_16x16x32_f16 v[0:3], v[138:141], v[74:77], v[0:3]
	ds_read_b128 v[42:45], v78
	ds_read_b128 v[74:77], v78 offset:8192
	ds_read_b128 v[82:85], v78 offset:16384
	ds_read_b128 v[86:89], v78 offset:24576
	s_waitcnt vmcnt(5) lgkmcnt(3)
	v_mfma_f32_16x16x32_f16 v[90:93], v[22:25], v[42:45], v[90:93]
	s_waitcnt lgkmcnt(2)
	v_mfma_f32_16x16x32_f16 v[94:97], v[22:25], v[74:77], v[94:97]
	s_waitcnt lgkmcnt(1)
	v_mfma_f32_16x16x32_f16 v[98:101], v[22:25], v[82:85], v[98:101]
	s_waitcnt lgkmcnt(0)
	v_mfma_f32_16x16x32_f16 v[12:15], v[22:25], v[86:89], v[12:15]
	s_waitcnt vmcnt(4)
	v_mfma_f32_16x16x32_f16 v[16:19], v[106:109], v[42:45], v[16:19]
	v_mfma_f32_16x16x32_f16 v[20:23], v[106:109], v[74:77], v[34:37]
	v_mfma_f32_16x16x32_f16 v[34:37], v[106:109], v[82:85], v[46:49]
	v_mfma_f32_16x16x32_f16 v[4:7], v[106:109], v[86:89], v[4:7]
	s_waitcnt vmcnt(3)
	v_mfma_f32_16x16x32_f16 v[8:11], v[130:133], v[42:45], v[8:11]
	v_mfma_f32_16x16x32_f16 v[24:27], v[130:133], v[74:77], v[26:29]
	v_mfma_f32_16x16x32_f16 v[38:41], v[130:133], v[82:85], v[38:41]
	v_mfma_f32_16x16x32_f16 v[0:3], v[130:133], v[86:89], v[0:3]
	ds_read_b128 v[42:45], v79
	ds_read_b128 v[46:49], v79 offset:8192
	ds_read_b128 v[74:77], v79 offset:16384
	ds_read_b128 v[82:85], v79 offset:24576
	s_waitcnt vmcnt(2) lgkmcnt(3)
	v_mfma_f32_16x16x32_f16 v[86:89], v[30:33], v[42:45], v[90:93]
	s_waitcnt lgkmcnt(2)
	v_mfma_f32_16x16x32_f16 v[90:93], v[30:33], v[46:49], v[94:97]
	s_waitcnt lgkmcnt(1)
	v_mfma_f32_16x16x32_f16 v[94:97], v[30:33], v[74:77], v[98:101]
	s_waitcnt lgkmcnt(0)
	v_mfma_f32_16x16x32_f16 v[12:15], v[30:33], v[82:85], v[12:15]
	s_waitcnt vmcnt(1)
	v_mfma_f32_16x16x32_f16 v[16:19], v[102:105], v[42:45], v[16:19]
	v_mfma_f32_16x16x32_f16 v[20:23], v[102:105], v[46:49], v[20:23]
	v_mfma_f32_16x16x32_f16 v[28:31], v[102:105], v[74:77], v[34:37]
	v_mfma_f32_16x16x32_f16 v[4:7], v[102:105], v[82:85], v[4:7]
	s_waitcnt vmcnt(0)
	v_mfma_f32_16x16x32_f16 v[8:11], v[126:129], v[42:45], v[8:11]
	v_mfma_f32_16x16x32_f16 v[24:27], v[126:129], v[46:49], v[24:27]
	v_mfma_f32_16x16x32_f16 v[32:35], v[126:129], v[74:77], v[38:41]
	v_mfma_f32_16x16x32_f16 v[0:3], v[126:129], v[82:85], v[0:3]
	s_nop 1
	global_load_dwordx4 v[36:39], v[56:57], off offset:1536
	global_load_dwordx4 v[40:43], v[56:57], off offset:1600
	global_load_dwordx4 v[44:47], v[56:57], off offset:1664
	v_mov_b32_e32 v58, v21
	v_mov_b32_e32 v59, v22
	v_mov_b32_e32 v74, v29
	v_mov_b32_e32 v56, v13
	v_mov_b32_e32 v57, v14
	v_mov_b32_e32 v75, v30
	v_mov_b32_e32 v48, v91
	v_mov_b32_e32 v49, v92
	v_mov_b32_e32 v54, v95
	v_mov_b32_e32 v55, v96
	v_mov_b32_e32 v76, v5
	v_mov_b32_e32 v77, v6
	s_barrier
	s_waitcnt vmcnt(2)
	v_pk_add_f32 v[78:79], v[86:87], v[36:37]
	v_pk_add_f32 v[82:83], v[88:89], v[38:39]
	v_add_f32_e32 v21, v90, v36
	v_pk_mov_b32 v[84:85], v[36:37], v[38:39] op_sel:[1,0]
	v_add_f32_e32 v22, v93, v39
	v_add_f32_e32 v29, v94, v36
	v_add_f32_e32 v36, v12, v36
	v_add_f32_e32 v37, v15, v39
	s_waitcnt vmcnt(1)
	v_add_f32_e32 v38, v20, v40
	v_add_f32_e32 v23, v23, v43
	v_add_f32_e32 v30, v97, v39
	v_pk_add_f32 v[12:13], v[16:17], v[40:41]
	v_pk_add_f32 v[14:15], v[18:19], v[42:43]
	v_pk_mov_b32 v[16:17], v[40:41], v[42:43] op_sel:[1,0]
	v_add_f32_e32 v28, v28, v40
	v_add_f32_e32 v31, v31, v43
	v_add_f32_e32 v39, v4, v40
	v_add_f32_e32 v40, v7, v43
	v_cvt_f16_f32_e32 v41, v21
	v_cvt_f16_f32_e32 v42, v22
	v_cvt_f16_f32_e32 v38, v38
	v_cvt_f16_f32_e32 v43, v23
	s_waitcnt vmcnt(0)
	v_pk_add_f32 v[4:5], v[8:9], v[44:45]
	v_pk_add_f32 v[6:7], v[10:11], v[46:47]
	v_pk_add_f32 v[10:11], v[48:49], v[84:85]
	v_pk_add_f32 v[20:21], v[56:57], v[84:85]
	v_cvt_pk_f16_f32 v12, v12, v13
	v_cvt_pk_f16_f32 v13, v14, v15
	v_pk_add_f32 v[14:15], v[58:59], v[16:17]
	v_cvt_pk_f16_f32 v8, v78, v79
	v_cvt_pk_f16_f32 v9, v82, v83
	v_pk_add_f32 v[18:19], v[54:55], v[84:85]
	v_pk_add_f32 v[22:23], v[74:75], v[16:17]
	v_pk_add_f32 v[16:17], v[76:77], v[16:17]
	v_cvt_pk_f16_f32 v4, v4, v5
	v_cvt_pk_f16_f32 v5, v6, v7
	v_cvt_pk_f16_f32 v6, v10, v11
	v_cvt_pk_f16_f32 v11, v14, v15
	ds_write2_b64 v73, v[8:9], v[12:13] offset1:4
	ds_write_b64 v69, v[4:5] offset:32832
	v_pack_b32_f16 v4, v41, v6
	v_alignbit_b32 v5, v42, v6, 16
	v_cvt_pk_f16_f32 v8, v36, v20
	v_cvt_pk_f16_f32 v9, v21, v37
	v_pack_b32_f16 v10, v38, v11
	v_alignbit_b32 v11, v43, v11, 16
	v_add_f32_e32 v24, v24, v44
	v_cvt_pk_f16_f32 v6, v29, v18
	v_cvt_pk_f16_f32 v7, v19, v30
	v_cvt_pk_f16_f32 v12, v28, v22
	v_cvt_pk_f16_f32 v13, v23, v31
	v_cvt_pk_f16_f32 v14, v39, v16
	v_cvt_pk_f16_f32 v15, v17, v40
	ds_write2_b64 v70, v[4:5], v[10:11] offset0:32 offset1:36
	ds_write2_b64 v71, v[6:7], v[12:13] offset0:64 offset1:68
	ds_write2_b64 v80, v[8:9], v[14:15] offset1:4
	v_add_f32_e32 v8, v27, v47
	v_mov_b32_e32 v4, v25
	v_mov_b32_e32 v5, v26
	v_pk_mov_b32 v[6:7], v[44:45], v[46:47] op_sel:[1,0]
	v_add_f32_e32 v9, v35, v47
	v_pk_add_f32 v[4:5], v[4:5], v[6:7]
	v_cvt_f16_f32_e32 v9, v9
	v_cvt_pk_f16_f32 v4, v24, v4
	v_cvt_pk_f16_f32 v5, v5, v8
	ds_write_b64 v69, v[4:5] offset:45376
	v_add_f32_e32 v4, v32, v44
	v_cvt_f16_f32_e32 v8, v4
	v_mov_b32_e32 v4, v33
	v_mov_b32_e32 v5, v34
	v_pk_add_f32 v[4:5], v[4:5], v[6:7]
	v_add_f32_e32 v0, v0, v44
	v_cvt_pk_f16_f32 v5, v4, v5
	v_pack_b32_f16 v4, v8, v5
	v_alignbit_b32 v5, v9, v5, 16
	ds_write_b64 v69, v[4:5] offset:57920
	v_cvt_f16_f32_e32 v4, v0
	v_mov_b32_e32 v0, v1
	v_mov_b32_e32 v1, v2
	v_add_f32_e32 v2, v3, v47
	v_cvt_f16_f32_e32 v2, v2
	v_pk_add_f32 v[0:1], v[0:1], v[6:7]
	s_nop 0
	v_cvt_pk_f16_f32 v1, v0, v1
	v_pack_b32_f16 v0, v4, v1
	v_alignbit_b32 v1, v2, v1, 16
	ds_write_b64 v68, v[0:1] offset:32832
	s_waitcnt lgkmcnt(0)
	s_barrier
	ds_read_b128 v[0:3], v51 offset:32768
	ds_read_b128 v[4:7], v81 offset:32768
	s_waitcnt lgkmcnt(1)
	buffer_store_dwordx4 v[0:3], v50, s[0:3], 0 offen offset:768 sc1
	ds_read_b128 v[0:3], v53 offset:32768
	ds_read_b128 v[8:11], v160 offset:32768
	ds_read_b128 v[12:15], v61 offset:32768
	ds_read_b128 v[16:19], v63 offset:32768
	s_waitcnt lgkmcnt(4)
	buffer_store_dwordx4 v[4:7], v52, s[0:3], 0 offen offset:768 sc1
	s_waitcnt lgkmcnt(3)
	buffer_store_dwordx4 v[0:3], v60, s[0:3], 0 offen offset:768 sc1
	s_waitcnt lgkmcnt(2)
	buffer_store_dwordx4 v[8:11], v62, s[0:3], 0 offen offset:768 sc1
	s_waitcnt lgkmcnt(1)
	buffer_store_dwordx4 v[12:15], v64, s[0:3], 0 offen offset:768 sc1
	s_waitcnt lgkmcnt(0)
	buffer_store_dwordx4 v[16:19], v66, s[0:3], 0 offen offset:768 sc1
	s_endpgm
	.p2alignl 8, 3212836864
